# GEMM K-loops: in each load segment the LDS-DMA issue block now precedes the ds_read fragment loads (37 segments)
# baseline (speedup 1.0000x reference)
.LBB0_120:
	s_add_u32 s41, s15, s18
	s_addc_u32 s42, s24, s19
	s_add_u32 s66, s18, 0x100
	s_addc_u32 s67, s19, 0
	s_cmp_eq_u32 s40, 28
	s_cselect_b64 s[70:71], -1, 0
	s_and_b64 s[2:3], s[70:71], exec
	s_cselect_b32 s69, s5, s42
	s_cselect_b32 s68, s13, s41
	s_cselect_b32 s41, 0, s66
	v_lshl_add_u64 v[198:199], v[132:133], 0, s[18:19]
	s_add_i32 m0, s92, 0xc000
	s_nop 0
	global_load_lds_dwordx4 v[198:199], off
	v_lshl_add_u64 v[198:199], v[134:135], 0, s[18:19]
	s_add_i32 m0, s92, 0xe000
	s_nop 0
	global_load_lds_dwordx4 v[198:199], off
	ds_read_b128 v[136:139], v211
	ds_read_b128 v[140:143], v211 offset:1024
	ds_read_b128 v[144:147], v211 offset:2048
	ds_read_b128 v[148:151], v211 offset:3072
	ds_read_b128 v[152:155], v212
	ds_read_b128 v[156:159], v212 offset:1024
	ds_read_b128 v[160:163], v212 offset:2048
	ds_read_b128 v[186:189], v212 offset:3072
	ds_read_b128 v[190:193], v213
	ds_read_b128 v[194:197], v213 offset:1024
	ds_read_b128 v[214:217], v213 offset:2048
	ds_read_b128 v[218:221], v213 offset:3072
	ds_read_b128 v[222:225], v213 offset:4096
	ds_read_b128 v[226:229], v213 offset:5120
	ds_read_b128 v[230:233], v213 offset:6144
	ds_read_b128 v[234:237], v213 offset:7168
	s_waitcnt vmcnt(8)
	s_waitcnt lgkmcnt(0)
	s_barrier
	s_setprio 1
	s_waitcnt lgkmcnt(0)
	v_mfma_f32_16x16x32_bf16 v[128:131], v[136:139], v[190:193], v[128:131]
	v_mfma_f32_16x16x32_bf16 v[124:127], v[144:147], v[190:193], v[124:127]
	v_mfma_f32_16x16x32_bf16 v[120:123], v[136:139], v[214:217], v[120:123]
	v_mfma_f32_16x16x32_bf16 v[112:115], v[144:147], v[214:217], v[112:115]
	v_mfma_f32_16x16x32_bf16 v[104:107], v[136:139], v[222:225], v[104:107]
	v_mfma_f32_16x16x32_bf16 v[96:99], v[144:147], v[222:225], v[96:99]
	v_mfma_f32_16x16x32_bf16 v[88:91], v[136:139], v[230:233], v[88:91]
	v_mfma_f32_16x16x32_bf16 v[80:83], v[144:147], v[230:233], v[80:83]
	v_mfma_f32_16x16x32_bf16 v[128:131], v[140:143], v[194:197], v[128:131]
	v_mfma_f32_16x16x32_bf16 v[124:127], v[148:151], v[194:197], v[124:127]
	v_mfma_f32_16x16x32_bf16 v[120:123], v[140:143], v[218:221], v[120:123]
	v_mfma_f32_16x16x32_bf16 v[112:115], v[148:151], v[218:221], v[112:115]
	v_mfma_f32_16x16x32_bf16 v[104:107], v[140:143], v[226:229], v[104:107]
	v_mfma_f32_16x16x32_bf16 v[96:99], v[148:151], v[226:229], v[96:99]
	v_mfma_f32_16x16x32_bf16 v[88:91], v[140:143], v[234:237], v[88:91]
	v_mfma_f32_16x16x32_bf16 v[80:83], v[148:151], v[234:237], v[80:83]
	s_setprio 0
	s_setprio 1
	v_mfma_f32_16x16x32_bf16 v[116:119], v[152:155], v[190:193], v[116:119]
	v_mfma_f32_16x16x32_bf16 v[108:111], v[160:163], v[190:193], v[108:111]
	v_mfma_f32_16x16x32_bf16 v[100:103], v[152:155], v[214:217], v[100:103]
	v_mfma_f32_16x16x32_bf16 v[92:95], v[160:163], v[214:217], v[92:95]
	v_mfma_f32_16x16x32_bf16 v[84:87], v[152:155], v[222:225], v[84:87]
	v_mfma_f32_16x16x32_bf16 v[76:79], v[160:163], v[222:225], v[76:79]
	v_mfma_f32_16x16x32_bf16 v[72:75], v[152:155], v[230:233], v[72:75]
	v_mfma_f32_16x16x32_bf16 v[68:71], v[160:163], v[230:233], v[68:71]
	v_mfma_f32_16x16x32_bf16 v[116:119], v[156:159], v[194:197], v[116:119]
	v_mfma_f32_16x16x32_bf16 v[108:111], v[186:189], v[194:197], v[108:111]
	v_mfma_f32_16x16x32_bf16 v[100:103], v[156:159], v[218:221], v[100:103]
	v_mfma_f32_16x16x32_bf16 v[92:95], v[186:189], v[218:221], v[92:95]
	v_mfma_f32_16x16x32_bf16 v[84:87], v[156:159], v[226:229], v[84:87]
	v_mfma_f32_16x16x32_bf16 v[76:79], v[186:189], v[226:229], v[76:79]
	v_mfma_f32_16x16x32_bf16 v[72:75], v[156:159], v[234:237], v[72:75]
	v_mfma_f32_16x16x32_bf16 v[68:71], v[186:189], v[234:237], v[68:71]
	s_setprio 0
	s_barrier
	s_add_i32 s2, s54, s96
	v_lshl_add_u64 v[198:199], s[68:69], 0, v[166:167]
	s_mov_b32 m0, s2
	s_nop 0
	global_load_lds_dwordx4 v[198:199], off
	s_add_i32 m0, s2, 0x2000
	s_add_u32 s2, s68, 0x80000
	v_lshl_add_u64 v[238:239], s[68:69], 0, v[170:171]
	s_addc_u32 s3, s69, 0
	s_add_i32 s18, s55, s96
	global_load_lds_dwordx4 v[238:239], off
	v_lshl_add_u64 v[240:241], s[2:3], 0, v[166:167]
	s_mov_b32 m0, s18
	s_nop 0
	global_load_lds_dwordx4 v[240:241], off
	v_lshl_add_u64 v[240:241], s[2:3], 0, v[170:171]
	s_add_i32 m0, s18, 0x2000
	s_and_b64 s[2:3], s[10:11], s[70:71]
	s_and_b64 s[2:3], s[2:3], exec
	s_cselect_b32 s2, s62, s16
	s_cselect_b32 s3, s63, s17
	s_add_u32 s2, s2, s41
	s_addc_u32 s3, s3, 0
	global_load_lds_dwordx4 v[240:241], off
	v_lshl_add_u64 v[240:241], s[2:3], 0, v[164:165]
	s_mov_b32 m0, s92
	v_lshl_add_u64 v[244:245], s[2:3], 0, v[168:169]
	global_load_lds_dwordx4 v[240:241], off
	s_mov_b32 m0, s52
	s_nop 0
	global_load_lds_dwordx4 v[244:245], off
	ds_read_b128 v[190:193], v213 offset:16384
	ds_read_b128 v[194:197], v213 offset:17408
	ds_read_b128 v[214:217], v213 offset:18432
	ds_read_b128 v[218:221], v213 offset:19456
	ds_read_b128 v[222:225], v213 offset:20480
	ds_read_b128 v[226:229], v213 offset:21504
	ds_read_b128 v[230:233], v213 offset:22528
	ds_read_b128 v[234:237], v213 offset:23552
	s_waitcnt vmcnt(8)
	s_waitcnt lgkmcnt(0)
	s_barrier
	s_setprio 1
	s_waitcnt lgkmcnt(0)
	v_mfma_f32_16x16x32_bf16 v[64:67], v[136:139], v[190:193], v[64:67]
	v_mfma_f32_16x16x32_bf16 v[60:63], v[144:147], v[190:193], v[60:63]
	v_mfma_f32_16x16x32_bf16 v[52:55], v[136:139], v[214:217], v[52:55]
	v_mfma_f32_16x16x32_bf16 v[44:47], v[144:147], v[214:217], v[44:47]
	v_mfma_f32_16x16x32_bf16 v[36:39], v[136:139], v[222:225], v[36:39]
	v_mfma_f32_16x16x32_bf16 v[28:31], v[144:147], v[222:225], v[28:31]
	v_mfma_f32_16x16x32_bf16 v[20:23], v[136:139], v[230:233], v[20:23]
	v_mfma_f32_16x16x32_bf16 v[12:15], v[144:147], v[230:233], v[12:15]
	v_mfma_f32_16x16x32_bf16 v[64:67], v[140:143], v[194:197], v[64:67]
	v_mfma_f32_16x16x32_bf16 v[60:63], v[148:151], v[194:197], v[60:63]
	v_mfma_f32_16x16x32_bf16 v[52:55], v[140:143], v[218:221], v[52:55]
	v_mfma_f32_16x16x32_bf16 v[44:47], v[148:151], v[218:221], v[44:47]
	v_mfma_f32_16x16x32_bf16 v[36:39], v[140:143], v[226:229], v[36:39]
	v_mfma_f32_16x16x32_bf16 v[28:31], v[148:151], v[226:229], v[28:31]
	v_mfma_f32_16x16x32_bf16 v[20:23], v[140:143], v[234:237], v[20:23]
	v_mfma_f32_16x16x32_bf16 v[12:15], v[148:151], v[234:237], v[12:15]
	s_setprio 0
	s_setprio 1
	v_mfma_f32_16x16x32_bf16 v[56:59], v[152:155], v[190:193], v[56:59]
	v_mfma_f32_16x16x32_bf16 v[48:51], v[160:163], v[190:193], v[48:51]
	v_mfma_f32_16x16x32_bf16 v[40:43], v[152:155], v[214:217], v[40:43]
	v_mfma_f32_16x16x32_bf16 v[32:35], v[160:163], v[214:217], v[32:35]
	v_mfma_f32_16x16x32_bf16 v[24:27], v[152:155], v[222:225], v[24:27]
	v_mfma_f32_16x16x32_bf16 v[16:19], v[160:163], v[222:225], v[16:19]
	v_mfma_f32_16x16x32_bf16 v[8:11], v[152:155], v[230:233], v[8:11]
	v_mfma_f32_16x16x32_bf16 v[4:7], v[160:163], v[230:233], v[4:7]
	v_mfma_f32_16x16x32_bf16 v[56:59], v[156:159], v[194:197], v[56:59]
	v_mfma_f32_16x16x32_bf16 v[48:51], v[186:189], v[194:197], v[48:51]
	v_mfma_f32_16x16x32_bf16 v[40:43], v[156:159], v[218:221], v[40:43]
	v_mfma_f32_16x16x32_bf16 v[32:35], v[186:189], v[218:221], v[32:35]
	v_mfma_f32_16x16x32_bf16 v[24:27], v[156:159], v[226:229], v[24:27]
	v_mfma_f32_16x16x32_bf16 v[16:19], v[186:189], v[226:229], v[16:19]
	v_mfma_f32_16x16x32_bf16 v[8:11], v[156:159], v[234:237], v[8:11]
	v_mfma_f32_16x16x32_bf16 v[4:7], v[186:189], v[234:237], v[4:7]
	s_setprio 0
	s_barrier
	s_add_u32 s2, s2, 0x80000
	s_addc_u32 s3, s3, 0
	s_mov_b32 m0, s53
	v_lshl_add_u64 v[246:247], s[2:3], 0, v[164:165]
	global_load_lds_dwordx4 v[246:247], off
	v_lshl_add_u64 v[246:247], s[2:3], 0, v[168:169]
	s_mov_b32 m0, s50
	s_nop 0
	global_load_lds_dwordx4 v[246:247], off
	s_add_i32 s18, 0, 0x18000
	v_add_u32_e32 v3, s18, v209
	s_add_i32 s19, 0, 0x1c000
	ds_read_b128 v[136:139], v3
	ds_read_b128 v[140:143], v3 offset:1024
	ds_read_b128 v[144:147], v3 offset:2048
	ds_read_b128 v[148:151], v3 offset:3072
	v_add_u32_e32 v3, s19, v209
	ds_read_b128 v[152:155], v3
	ds_read_b128 v[156:159], v3 offset:1024
	ds_read_b128 v[160:163], v3 offset:2048
	ds_read_b128 v[186:189], v3 offset:3072
	ds_read_b128 v[190:193], v213 offset:32768
	ds_read_b128 v[194:197], v213 offset:33792
	ds_read_b128 v[214:217], v213 offset:34816
	ds_read_b128 v[218:221], v213 offset:35840
	ds_read_b128 v[222:225], v213 offset:36864
	ds_read_b128 v[226:229], v213 offset:37888
	ds_read_b128 v[230:233], v213 offset:38912
	ds_read_b128 v[234:237], v213 offset:39936
	s_waitcnt vmcnt(8)
	s_waitcnt lgkmcnt(0)
	s_barrier
	s_setprio 1
	s_waitcnt lgkmcnt(0)
	v_mfma_f32_16x16x32_bf16 v[128:131], v[136:139], v[190:193], v[128:131]
	v_mfma_f32_16x16x32_bf16 v[124:127], v[144:147], v[190:193], v[124:127]
	v_mfma_f32_16x16x32_bf16 v[120:123], v[136:139], v[214:217], v[120:123]
	v_mfma_f32_16x16x32_bf16 v[112:115], v[144:147], v[214:217], v[112:115]
	v_mfma_f32_16x16x32_bf16 v[104:107], v[136:139], v[222:225], v[104:107]
	v_mfma_f32_16x16x32_bf16 v[96:99], v[144:147], v[222:225], v[96:99]
	v_mfma_f32_16x16x32_bf16 v[88:91], v[136:139], v[230:233], v[88:91]
	v_mfma_f32_16x16x32_bf16 v[80:83], v[144:147], v[230:233], v[80:83]
	v_mfma_f32_16x16x32_bf16 v[128:131], v[140:143], v[194:197], v[128:131]
	v_mfma_f32_16x16x32_bf16 v[124:127], v[148:151], v[194:197], v[124:127]
	v_mfma_f32_16x16x32_bf16 v[120:123], v[140:143], v[218:221], v[120:123]
	v_mfma_f32_16x16x32_bf16 v[112:115], v[148:151], v[218:221], v[112:115]
	v_mfma_f32_16x16x32_bf16 v[104:107], v[140:143], v[226:229], v[104:107]
	v_mfma_f32_16x16x32_bf16 v[96:99], v[148:151], v[226:229], v[96:99]
	v_mfma_f32_16x16x32_bf16 v[88:91], v[140:143], v[234:237], v[88:91]
	v_mfma_f32_16x16x32_bf16 v[80:83], v[148:151], v[234:237], v[80:83]
	s_setprio 0
	s_setprio 1
	v_mfma_f32_16x16x32_bf16 v[116:119], v[152:155], v[190:193], v[116:119]
	v_mfma_f32_16x16x32_bf16 v[108:111], v[160:163], v[190:193], v[108:111]
	v_mfma_f32_16x16x32_bf16 v[100:103], v[152:155], v[214:217], v[100:103]
	v_mfma_f32_16x16x32_bf16 v[92:95], v[160:163], v[214:217], v[92:95]
	v_mfma_f32_16x16x32_bf16 v[84:87], v[152:155], v[222:225], v[84:87]
	v_mfma_f32_16x16x32_bf16 v[76:79], v[160:163], v[222:225], v[76:79]
	v_mfma_f32_16x16x32_bf16 v[72:75], v[152:155], v[230:233], v[72:75]
	v_mfma_f32_16x16x32_bf16 v[68:71], v[160:163], v[230:233], v[68:71]
	v_mfma_f32_16x16x32_bf16 v[116:119], v[156:159], v[194:197], v[116:119]
	v_mfma_f32_16x16x32_bf16 v[108:111], v[186:189], v[194:197], v[108:111]
	v_mfma_f32_16x16x32_bf16 v[100:103], v[156:159], v[218:221], v[100:103]
	v_mfma_f32_16x16x32_bf16 v[92:95], v[186:189], v[218:221], v[92:95]
	v_mfma_f32_16x16x32_bf16 v[84:87], v[156:159], v[226:229], v[84:87]
	v_mfma_f32_16x16x32_bf16 v[76:79], v[186:189], v[226:229], v[76:79]
	v_mfma_f32_16x16x32_bf16 v[72:75], v[156:159], v[234:237], v[72:75]
	v_mfma_f32_16x16x32_bf16 v[68:71], v[186:189], v[234:237], v[68:71]
	s_setprio 0
	s_barrier
	s_add_i32 s2, s18, s96
	v_lshl_add_u64 v[198:199], v[198:199], 0, s[38:39]
	s_mov_b32 m0, s2
	s_nop 0
	global_load_lds_dwordx4 v[198:199], off
	s_add_i32 m0, s2, 0x2000
	s_add_u32 s2, s68, 0x80080
	v_lshl_add_u64 v[198:199], v[238:239], 0, s[38:39]
	s_addc_u32 s3, s69, 0
	s_add_i32 s18, s19, s96
	global_load_lds_dwordx4 v[198:199], off
	v_lshl_add_u64 v[198:199], s[2:3], 0, v[166:167]
	s_mov_b32 m0, s18
	s_nop 0
	global_load_lds_dwordx4 v[198:199], off
	v_lshl_add_u64 v[198:199], s[2:3], 0, v[170:171]
	s_add_i32 m0, s18, 0x2000
	s_nop 0
	global_load_lds_dwordx4 v[198:199], off
	v_lshl_add_u64 v[198:199], v[240:241], 0, s[38:39]
	s_mov_b32 m0, s56
	s_nop 0
	global_load_lds_dwordx4 v[198:199], off
	v_lshl_add_u64 v[198:199], v[244:245], 0, s[38:39]
	s_mov_b32 m0, s57
	s_nop 0
	global_load_lds_dwordx4 v[198:199], off
	ds_read_b128 v[190:193], v213 offset:49152
	ds_read_b128 v[194:197], v213 offset:50176
	ds_read_b128 v[214:217], v213 offset:51200
	ds_read_b128 v[218:221], v213 offset:52224
	ds_read_b128 v[222:225], v213 offset:53248
	ds_read_b128 v[226:229], v213 offset:54272
	ds_read_b128 v[230:233], v213 offset:55296
	ds_read_b128 v[234:237], v213 offset:56320
	s_waitcnt vmcnt(8)
	s_waitcnt lgkmcnt(0)
	s_barrier
	s_setprio 1
	s_waitcnt lgkmcnt(0)
	v_mfma_f32_16x16x32_bf16 v[64:67], v[136:139], v[190:193], v[64:67]
	v_mfma_f32_16x16x32_bf16 v[60:63], v[144:147], v[190:193], v[60:63]
	v_mfma_f32_16x16x32_bf16 v[52:55], v[136:139], v[214:217], v[52:55]
	v_mfma_f32_16x16x32_bf16 v[44:47], v[144:147], v[214:217], v[44:47]
	v_mfma_f32_16x16x32_bf16 v[36:39], v[136:139], v[222:225], v[36:39]
	v_mfma_f32_16x16x32_bf16 v[28:31], v[144:147], v[222:225], v[28:31]
	v_mfma_f32_16x16x32_bf16 v[20:23], v[136:139], v[230:233], v[20:23]
	v_mfma_f32_16x16x32_bf16 v[12:15], v[144:147], v[230:233], v[12:15]
	v_mfma_f32_16x16x32_bf16 v[64:67], v[140:143], v[194:197], v[64:67]
	v_mfma_f32_16x16x32_bf16 v[60:63], v[148:151], v[194:197], v[60:63]
	v_mfma_f32_16x16x32_bf16 v[52:55], v[140:143], v[218:221], v[52:55]
	v_mfma_f32_16x16x32_bf16 v[44:47], v[148:151], v[218:221], v[44:47]
	v_mfma_f32_16x16x32_bf16 v[36:39], v[140:143], v[226:229], v[36:39]
	v_mfma_f32_16x16x32_bf16 v[28:31], v[148:151], v[226:229], v[28:31]
	v_mfma_f32_16x16x32_bf16 v[20:23], v[140:143], v[234:237], v[20:23]
	v_mfma_f32_16x16x32_bf16 v[12:15], v[148:151], v[234:237], v[12:15]
	s_setprio 0
	s_setprio 1
	v_mfma_f32_16x16x32_bf16 v[56:59], v[152:155], v[190:193], v[56:59]
	v_mfma_f32_16x16x32_bf16 v[48:51], v[160:163], v[190:193], v[48:51]
	v_mfma_f32_16x16x32_bf16 v[40:43], v[152:155], v[214:217], v[40:43]
	v_mfma_f32_16x16x32_bf16 v[32:35], v[160:163], v[214:217], v[32:35]
	v_mfma_f32_16x16x32_bf16 v[24:27], v[152:155], v[222:225], v[24:27]
	v_mfma_f32_16x16x32_bf16 v[16:19], v[160:163], v[222:225], v[16:19]
	v_mfma_f32_16x16x32_bf16 v[8:11], v[152:155], v[230:233], v[8:11]
	v_mfma_f32_16x16x32_bf16 v[4:7], v[160:163], v[230:233], v[4:7]
	v_mfma_f32_16x16x32_bf16 v[56:59], v[156:159], v[194:197], v[56:59]
	v_mfma_f32_16x16x32_bf16 v[48:51], v[186:189], v[194:197], v[48:51]
	v_mfma_f32_16x16x32_bf16 v[40:43], v[156:159], v[218:221], v[40:43]
	v_mfma_f32_16x16x32_bf16 v[32:35], v[186:189], v[218:221], v[32:35]
	v_mfma_f32_16x16x32_bf16 v[24:27], v[156:159], v[226:229], v[24:27]
	v_mfma_f32_16x16x32_bf16 v[16:19], v[186:189], v[226:229], v[16:19]
	v_mfma_f32_16x16x32_bf16 v[8:11], v[156:159], v[234:237], v[8:11]
	v_mfma_f32_16x16x32_bf16 v[4:7], v[186:189], v[234:237], v[4:7]
	s_setprio 0
	s_barrier
	s_add_i32 s40, s40, 2
	s_cmp_gt_u32 s40, 29
	s_mov_b64 s[18:19], s[66:67]
	s_cbranch_scc0 .LBB0_120
	v_readlane_b32 s2, v252, 27
	v_readlane_b32 s3, v252, 28
	s_and_b64 vcc, exec, s[2:3]
	s_cbranch_vccz .LBB0_123
	s_barrier

.LBB0_346:
	s_add_u32 s34, s51, s28
	s_addc_u32 s35, s52, s29
	s_add_u32 s30, s28, 0x100
	s_addc_u32 s31, s29, 0
	s_cmp_eq_u32 s53, 28
	s_cselect_b64 s[36:37], -1, 0
	s_and_b64 s[2:3], s[36:37], exec
	s_cselect_b32 s35, s15, s35
	s_cselect_b32 s34, s17, s34
	s_cselect_b32 s54, 0, s30
	v_lshl_add_u64 v[220:221], v[140:141], 0, s[28:29]
	s_add_i32 m0, s21, 0xc000
	s_nop 0
	global_load_lds_dwordx4 v[220:221], off
	v_lshl_add_u64 v[220:221], v[142:143], 0, s[28:29]
	s_add_i32 m0, s21, 0xe000
	s_nop 0
	global_load_lds_dwordx4 v[220:221], off
	ds_read_b128 v[148:151], v1
	ds_read_b128 v[152:155], v1 offset:1024
	ds_read_b128 v[156:159], v1 offset:2048
	ds_read_b128 v[160:163], v1 offset:3072
	ds_read_b128 v[172:175], v145
	ds_read_b128 v[176:179], v145 offset:1024
	ds_read_b128 v[180:183], v145 offset:2048
	ds_read_b128 v[184:187], v145 offset:3072
	ds_read_b128 v[188:191], v146
	ds_read_b128 v[192:195], v146 offset:1024
	ds_read_b128 v[196:199], v146 offset:2048
	ds_read_b128 v[200:203], v146 offset:3072
	ds_read_b128 v[204:207], v146 offset:4096
	ds_read_b128 v[208:211], v146 offset:5120
	ds_read_b128 v[212:215], v146 offset:6144
	ds_read_b128 v[216:219], v146 offset:7168
	s_waitcnt vmcnt(8)
	s_waitcnt lgkmcnt(0)
	s_barrier
	s_setprio 1
	s_waitcnt lgkmcnt(0)
	v_mfma_f32_16x16x32_bf16 v[126:129], v[188:191], v[148:151], v[126:129]
	v_mfma_f32_16x16x32_bf16 v[114:117], v[188:191], v[156:159], v[114:117]
	v_mfma_f32_16x16x32_bf16 v[122:125], v[196:199], v[148:151], v[122:125]
	v_mfma_f32_16x16x32_bf16 v[106:109], v[196:199], v[156:159], v[106:109]
	v_mfma_f32_16x16x32_bf16 v[118:121], v[204:207], v[148:151], v[118:121]
	v_mfma_f32_16x16x32_bf16 v[102:105], v[204:207], v[156:159], v[102:105]
	v_mfma_f32_16x16x32_bf16 v[110:113], v[212:215], v[148:151], v[110:113]
	v_mfma_f32_16x16x32_bf16 v[98:101], v[212:215], v[156:159], v[98:101]
	v_mfma_f32_16x16x32_bf16 v[126:129], v[192:195], v[152:155], v[126:129]
	v_mfma_f32_16x16x32_bf16 v[114:117], v[192:195], v[160:163], v[114:117]
	v_mfma_f32_16x16x32_bf16 v[122:125], v[200:203], v[152:155], v[122:125]
	v_mfma_f32_16x16x32_bf16 v[106:109], v[200:203], v[160:163], v[106:109]
	v_mfma_f32_16x16x32_bf16 v[118:121], v[208:211], v[152:155], v[118:121]
	v_mfma_f32_16x16x32_bf16 v[102:105], v[208:211], v[160:163], v[102:105]
	v_mfma_f32_16x16x32_bf16 v[110:113], v[216:219], v[152:155], v[110:113]
	v_mfma_f32_16x16x32_bf16 v[98:101], v[216:219], v[160:163], v[98:101]
	s_setprio 0
	s_setprio 1
	v_mfma_f32_16x16x32_bf16 v[94:97], v[188:191], v[172:175], v[94:97]
	v_mfma_f32_16x16x32_bf16 v[82:85], v[188:191], v[180:183], v[82:85]
	v_mfma_f32_16x16x32_bf16 v[90:93], v[196:199], v[172:175], v[90:93]
	v_mfma_f32_16x16x32_bf16 v[74:77], v[196:199], v[180:183], v[74:77]
	v_mfma_f32_16x16x32_bf16 v[86:89], v[204:207], v[172:175], v[86:89]
	v_mfma_f32_16x16x32_bf16 v[70:73], v[204:207], v[180:183], v[70:73]
	v_mfma_f32_16x16x32_bf16 v[78:81], v[212:215], v[172:175], v[78:81]
	v_mfma_f32_16x16x32_bf16 v[66:69], v[212:215], v[180:183], v[66:69]
	v_mfma_f32_16x16x32_bf16 v[94:97], v[192:195], v[176:179], v[94:97]
	v_mfma_f32_16x16x32_bf16 v[82:85], v[192:195], v[184:187], v[82:85]
	v_mfma_f32_16x16x32_bf16 v[90:93], v[200:203], v[176:179], v[90:93]
	v_mfma_f32_16x16x32_bf16 v[74:77], v[200:203], v[184:187], v[74:77]
	v_mfma_f32_16x16x32_bf16 v[86:89], v[208:211], v[176:179], v[86:89]
	v_mfma_f32_16x16x32_bf16 v[70:73], v[208:211], v[184:187], v[70:73]
	v_mfma_f32_16x16x32_bf16 v[78:81], v[216:219], v[176:179], v[78:81]
	v_mfma_f32_16x16x32_bf16 v[66:69], v[216:219], v[184:187], v[66:69]
	s_setprio 0
	s_barrier
	s_add_i32 s2, s49, s20
	v_lshl_add_u64 v[220:221], s[34:35], 0, v[164:165]
	s_mov_b32 m0, s2
	s_nop 0
	global_load_lds_dwordx4 v[220:221], off
	s_add_i32 m0, s2, 0x2000
	s_add_u32 s2, s34, 0x80000
	v_lshl_add_u64 v[222:223], s[34:35], 0, v[168:169]
	s_addc_u32 s3, s35, 0
	s_add_i32 s28, s50, s20
	global_load_lds_dwordx4 v[222:223], off
	v_lshl_add_u64 v[224:225], s[2:3], 0, v[164:165]
	s_mov_b32 m0, s28
	s_nop 0
	global_load_lds_dwordx4 v[224:225], off
	v_lshl_add_u64 v[224:225], s[2:3], 0, v[168:169]
	s_add_i32 m0, s28, 0x2000
	s_and_b64 s[2:3], s[6:7], s[36:37]
	s_and_b64 s[2:3], s[2:3], exec
	s_cselect_b32 s2, s18, s26
	s_cselect_b32 s3, s19, s27
	s_add_u32 s2, s2, s54
	s_addc_u32 s3, s3, 0
	global_load_lds_dwordx4 v[224:225], off
	v_lshl_add_u64 v[224:225], s[2:3], 0, v[166:167]
	s_mov_b32 m0, s21
	v_lshl_add_u64 v[226:227], s[2:3], 0, v[170:171]
	global_load_lds_dwordx4 v[224:225], off
	s_mov_b32 m0, s33
	s_nop 0
	global_load_lds_dwordx4 v[226:227], off
	ds_read_b128 v[188:191], v146 offset:16384
	ds_read_b128 v[192:195], v146 offset:17408
	ds_read_b128 v[196:199], v146 offset:18432
	ds_read_b128 v[200:203], v146 offset:19456
	ds_read_b128 v[204:207], v146 offset:20480
	ds_read_b128 v[208:211], v146 offset:21504
	ds_read_b128 v[212:215], v146 offset:22528
	ds_read_b128 v[216:219], v146 offset:23552
	s_waitcnt vmcnt(8)
	s_waitcnt lgkmcnt(0)
	s_barrier
	s_setprio 1
	s_waitcnt lgkmcnt(0)
	v_mfma_f32_16x16x32_bf16 v[62:65], v[188:191], v[148:151], v[62:65]
	v_mfma_f32_16x16x32_bf16 v[50:53], v[188:191], v[156:159], v[50:53]
	v_mfma_f32_16x16x32_bf16 v[58:61], v[196:199], v[148:151], v[58:61]
	v_mfma_f32_16x16x32_bf16 v[42:45], v[196:199], v[156:159], v[42:45]
	v_mfma_f32_16x16x32_bf16 v[54:57], v[204:207], v[148:151], v[54:57]
	v_mfma_f32_16x16x32_bf16 v[38:41], v[204:207], v[156:159], v[38:41]
	v_mfma_f32_16x16x32_bf16 v[46:49], v[212:215], v[148:151], v[46:49]
	v_mfma_f32_16x16x32_bf16 v[34:37], v[212:215], v[156:159], v[34:37]
	v_mfma_f32_16x16x32_bf16 v[62:65], v[192:195], v[152:155], v[62:65]
	v_mfma_f32_16x16x32_bf16 v[50:53], v[192:195], v[160:163], v[50:53]
	v_mfma_f32_16x16x32_bf16 v[58:61], v[200:203], v[152:155], v[58:61]
	v_mfma_f32_16x16x32_bf16 v[42:45], v[200:203], v[160:163], v[42:45]
	v_mfma_f32_16x16x32_bf16 v[54:57], v[208:211], v[152:155], v[54:57]
	v_mfma_f32_16x16x32_bf16 v[38:41], v[208:211], v[160:163], v[38:41]
	v_mfma_f32_16x16x32_bf16 v[46:49], v[216:219], v[152:155], v[46:49]
	v_mfma_f32_16x16x32_bf16 v[34:37], v[216:219], v[160:163], v[34:37]
	s_setprio 0
	s_setprio 1
	v_mfma_f32_16x16x32_bf16 v[30:33], v[188:191], v[172:175], v[30:33]
	v_mfma_f32_16x16x32_bf16 v[18:21], v[188:191], v[180:183], v[18:21]
	v_mfma_f32_16x16x32_bf16 v[26:29], v[196:199], v[172:175], v[26:29]
	v_mfma_f32_16x16x32_bf16 v[10:13], v[196:199], v[180:183], v[10:13]
	v_mfma_f32_16x16x32_bf16 v[22:25], v[204:207], v[172:175], v[22:25]
	v_mfma_f32_16x16x32_bf16 v[6:9], v[204:207], v[180:183], v[6:9]
	v_mfma_f32_16x16x32_bf16 v[14:17], v[212:215], v[172:175], v[14:17]
	v_mfma_f32_16x16x32_bf16 v[2:5], v[212:215], v[180:183], v[2:5]
	v_mfma_f32_16x16x32_bf16 v[30:33], v[192:195], v[176:179], v[30:33]
	v_mfma_f32_16x16x32_bf16 v[18:21], v[192:195], v[184:187], v[18:21]
	v_mfma_f32_16x16x32_bf16 v[26:29], v[200:203], v[176:179], v[26:29]
	v_mfma_f32_16x16x32_bf16 v[10:13], v[200:203], v[184:187], v[10:13]
	v_mfma_f32_16x16x32_bf16 v[22:25], v[208:211], v[176:179], v[22:25]
	v_mfma_f32_16x16x32_bf16 v[6:9], v[208:211], v[184:187], v[6:9]
	v_mfma_f32_16x16x32_bf16 v[14:17], v[216:219], v[176:179], v[14:17]
	v_mfma_f32_16x16x32_bf16 v[2:5], v[216:219], v[184:187], v[2:5]
	s_setprio 0
	s_barrier
	s_add_u32 s2, s2, 0x80000
	s_addc_u32 s3, s3, 0
	s_mov_b32 m0, s38
	v_lshl_add_u64 v[228:229], s[2:3], 0, v[166:167]
	global_load_lds_dwordx4 v[228:229], off
	v_lshl_add_u64 v[228:229], s[2:3], 0, v[170:171]
	s_mov_b32 m0, s39
	s_nop 0
	global_load_lds_dwordx4 v[228:229], off
	s_add_i32 s28, 0, 0x18000
	v_add_u32_e32 v147, s28, v144
	s_add_i32 s29, 0, 0x1c000
	ds_read_b128 v[148:151], v147
	ds_read_b128 v[152:155], v147 offset:1024
	ds_read_b128 v[156:159], v147 offset:2048
	ds_read_b128 v[160:163], v147 offset:3072
	v_add_u32_e32 v147, s29, v144
	ds_read_b128 v[172:175], v147
	ds_read_b128 v[176:179], v147 offset:1024
	ds_read_b128 v[180:183], v147 offset:2048
	ds_read_b128 v[184:187], v147 offset:3072
	ds_read_b128 v[188:191], v146 offset:32768
	ds_read_b128 v[192:195], v146 offset:33792
	ds_read_b128 v[196:199], v146 offset:34816
	ds_read_b128 v[200:203], v146 offset:35840
	ds_read_b128 v[204:207], v146 offset:36864
	ds_read_b128 v[208:211], v146 offset:37888
	ds_read_b128 v[212:215], v146 offset:38912
	ds_read_b128 v[216:219], v146 offset:39936
	s_waitcnt vmcnt(8)
	s_waitcnt lgkmcnt(0)
	s_barrier
	s_setprio 1
	s_waitcnt lgkmcnt(0)
	v_mfma_f32_16x16x32_bf16 v[126:129], v[188:191], v[148:151], v[126:129]
	v_mfma_f32_16x16x32_bf16 v[114:117], v[188:191], v[156:159], v[114:117]
	v_mfma_f32_16x16x32_bf16 v[122:125], v[196:199], v[148:151], v[122:125]
	v_mfma_f32_16x16x32_bf16 v[106:109], v[196:199], v[156:159], v[106:109]
	v_mfma_f32_16x16x32_bf16 v[118:121], v[204:207], v[148:151], v[118:121]
	v_mfma_f32_16x16x32_bf16 v[102:105], v[204:207], v[156:159], v[102:105]
	v_mfma_f32_16x16x32_bf16 v[110:113], v[212:215], v[148:151], v[110:113]
	v_mfma_f32_16x16x32_bf16 v[98:101], v[212:215], v[156:159], v[98:101]
	v_mfma_f32_16x16x32_bf16 v[126:129], v[192:195], v[152:155], v[126:129]
	v_mfma_f32_16x16x32_bf16 v[114:117], v[192:195], v[160:163], v[114:117]
	v_mfma_f32_16x16x32_bf16 v[122:125], v[200:203], v[152:155], v[122:125]
	v_mfma_f32_16x16x32_bf16 v[106:109], v[200:203], v[160:163], v[106:109]
	v_mfma_f32_16x16x32_bf16 v[118:121], v[208:211], v[152:155], v[118:121]
	v_mfma_f32_16x16x32_bf16 v[102:105], v[208:211], v[160:163], v[102:105]
	v_mfma_f32_16x16x32_bf16 v[110:113], v[216:219], v[152:155], v[110:113]
	v_mfma_f32_16x16x32_bf16 v[98:101], v[216:219], v[160:163], v[98:101]
	s_setprio 0
	s_setprio 1
	v_mfma_f32_16x16x32_bf16 v[94:97], v[188:191], v[172:175], v[94:97]
	v_mfma_f32_16x16x32_bf16 v[82:85], v[188:191], v[180:183], v[82:85]
	v_mfma_f32_16x16x32_bf16 v[90:93], v[196:199], v[172:175], v[90:93]
	v_mfma_f32_16x16x32_bf16 v[74:77], v[196:199], v[180:183], v[74:77]
	v_mfma_f32_16x16x32_bf16 v[86:89], v[204:207], v[172:175], v[86:89]
	v_mfma_f32_16x16x32_bf16 v[70:73], v[204:207], v[180:183], v[70:73]
	v_mfma_f32_16x16x32_bf16 v[78:81], v[212:215], v[172:175], v[78:81]
	v_mfma_f32_16x16x32_bf16 v[66:69], v[212:215], v[180:183], v[66:69]
	v_mfma_f32_16x16x32_bf16 v[94:97], v[192:195], v[176:179], v[94:97]
	v_mfma_f32_16x16x32_bf16 v[82:85], v[192:195], v[184:187], v[82:85]
	v_mfma_f32_16x16x32_bf16 v[90:93], v[200:203], v[176:179], v[90:93]
	v_mfma_f32_16x16x32_bf16 v[74:77], v[200:203], v[184:187], v[74:77]
	v_mfma_f32_16x16x32_bf16 v[86:89], v[208:211], v[176:179], v[86:89]
	v_mfma_f32_16x16x32_bf16 v[70:73], v[208:211], v[184:187], v[70:73]
	v_mfma_f32_16x16x32_bf16 v[78:81], v[216:219], v[176:179], v[78:81]
	v_mfma_f32_16x16x32_bf16 v[66:69], v[216:219], v[184:187], v[66:69]
	s_setprio 0
	s_barrier
	s_add_i32 s2, s28, s20
	v_lshl_add_u64 v[220:221], v[220:221], 0, s[10:11]
	s_mov_b32 m0, s2
	s_nop 0
	global_load_lds_dwordx4 v[220:221], off
	s_add_i32 m0, s2, 0x2000
	s_add_u32 s2, s34, 0x80080
	v_lshl_add_u64 v[220:221], v[222:223], 0, s[10:11]
	s_addc_u32 s3, s35, 0
	s_add_i32 s28, s29, s20
	global_load_lds_dwordx4 v[220:221], off
	v_lshl_add_u64 v[220:221], s[2:3], 0, v[164:165]
	s_mov_b32 m0, s28
	s_nop 0
	global_load_lds_dwordx4 v[220:221], off
	v_lshl_add_u64 v[220:221], s[2:3], 0, v[168:169]
	s_add_i32 m0, s28, 0x2000
	s_nop 0
	global_load_lds_dwordx4 v[220:221], off
	v_lshl_add_u64 v[220:221], v[224:225], 0, s[10:11]
	s_mov_b32 m0, s43
	s_nop 0
	global_load_lds_dwordx4 v[220:221], off
	v_lshl_add_u64 v[220:221], v[226:227], 0, s[10:11]
	s_mov_b32 m0, s48
	s_nop 0
	global_load_lds_dwordx4 v[220:221], off
	ds_read_b128 v[188:191], v146 offset:49152
	ds_read_b128 v[192:195], v146 offset:50176
	ds_read_b128 v[196:199], v146 offset:51200
	ds_read_b128 v[200:203], v146 offset:52224
	ds_read_b128 v[204:207], v146 offset:53248
	ds_read_b128 v[208:211], v146 offset:54272
	ds_read_b128 v[212:215], v146 offset:55296
	ds_read_b128 v[216:219], v146 offset:56320
	s_waitcnt vmcnt(8)
	s_waitcnt lgkmcnt(0)
	s_barrier
	s_setprio 1
	s_waitcnt lgkmcnt(0)
	v_mfma_f32_16x16x32_bf16 v[62:65], v[188:191], v[148:151], v[62:65]
	v_mfma_f32_16x16x32_bf16 v[50:53], v[188:191], v[156:159], v[50:53]
	v_mfma_f32_16x16x32_bf16 v[58:61], v[196:199], v[148:151], v[58:61]
	v_mfma_f32_16x16x32_bf16 v[42:45], v[196:199], v[156:159], v[42:45]
	v_mfma_f32_16x16x32_bf16 v[54:57], v[204:207], v[148:151], v[54:57]
	v_mfma_f32_16x16x32_bf16 v[38:41], v[204:207], v[156:159], v[38:41]
	v_mfma_f32_16x16x32_bf16 v[46:49], v[212:215], v[148:151], v[46:49]
	v_mfma_f32_16x16x32_bf16 v[34:37], v[212:215], v[156:159], v[34:37]
	v_mfma_f32_16x16x32_bf16 v[62:65], v[192:195], v[152:155], v[62:65]
	v_mfma_f32_16x16x32_bf16 v[50:53], v[192:195], v[160:163], v[50:53]
	v_mfma_f32_16x16x32_bf16 v[58:61], v[200:203], v[152:155], v[58:61]
	v_mfma_f32_16x16x32_bf16 v[42:45], v[200:203], v[160:163], v[42:45]
	v_mfma_f32_16x16x32_bf16 v[54:57], v[208:211], v[152:155], v[54:57]
	v_mfma_f32_16x16x32_bf16 v[38:41], v[208:211], v[160:163], v[38:41]
	v_mfma_f32_16x16x32_bf16 v[46:49], v[216:219], v[152:155], v[46:49]
	v_mfma_f32_16x16x32_bf16 v[34:37], v[216:219], v[160:163], v[34:37]
	s_setprio 0
	s_setprio 1
	v_mfma_f32_16x16x32_bf16 v[30:33], v[188:191], v[172:175], v[30:33]
	v_mfma_f32_16x16x32_bf16 v[18:21], v[188:191], v[180:183], v[18:21]
	v_mfma_f32_16x16x32_bf16 v[26:29], v[196:199], v[172:175], v[26:29]
	v_mfma_f32_16x16x32_bf16 v[10:13], v[196:199], v[180:183], v[10:13]
	v_mfma_f32_16x16x32_bf16 v[22:25], v[204:207], v[172:175], v[22:25]
	v_mfma_f32_16x16x32_bf16 v[6:9], v[204:207], v[180:183], v[6:9]
	v_mfma_f32_16x16x32_bf16 v[14:17], v[212:215], v[172:175], v[14:17]
	v_mfma_f32_16x16x32_bf16 v[2:5], v[212:215], v[180:183], v[2:5]
	v_mfma_f32_16x16x32_bf16 v[30:33], v[192:195], v[176:179], v[30:33]
	v_mfma_f32_16x16x32_bf16 v[18:21], v[192:195], v[184:187], v[18:21]
	v_mfma_f32_16x16x32_bf16 v[26:29], v[200:203], v[176:179], v[26:29]
	v_mfma_f32_16x16x32_bf16 v[10:13], v[200:203], v[184:187], v[10:13]
	v_mfma_f32_16x16x32_bf16 v[22:25], v[208:211], v[176:179], v[22:25]
	v_mfma_f32_16x16x32_bf16 v[6:9], v[208:211], v[184:187], v[6:9]
	v_mfma_f32_16x16x32_bf16 v[14:17], v[216:219], v[176:179], v[14:17]
	v_mfma_f32_16x16x32_bf16 v[2:5], v[216:219], v[184:187], v[2:5]
	s_setprio 0
	s_barrier
	s_add_i32 s53, s53, 2
	s_cmp_gt_u32 s53, 29
	s_mov_b64 s[28:29], s[30:31]
	s_cbranch_scc0 .LBB0_346
	s_and_b64 vcc, exec, s[12:13]
	s_cbranch_vccz .LBB0_349
	s_barrier

.LBB0_712:
	s_mov_b64 s[72:73], s[56:57]
	s_add_u32 s2, s69, s72
	s_addc_u32 s74, s70, s73
	s_add_u32 s56, s72, 0x100
	s_addc_u32 s57, s73, 0
	s_cmpk_eq_i32 s72, 0xf00
	s_cselect_b64 s[58:59], -1, 0
	s_and_b64 s[60:61], s[58:59], exec
	s_cselect_b32 s61, s35, s74
	s_cselect_b32 s60, s68, s2
	s_cselect_b32 s2, 0, s56
	v_lshl_add_u64 v[4:5], v[136:137], 0, s[72:73]
	s_add_i32 m0, s42, 0xc000
	s_nop 0
	global_load_lds_dwordx4 v[4:5], off
	v_lshl_add_u64 v[4:5], v[134:135], 0, s[72:73]
	s_add_i32 m0, s42, 0xe000
	s_nop 0
	global_load_lds_dwordx4 v[4:5], off
	ds_read_b128 v[140:143], v205
	ds_read_b128 v[144:147], v205 offset:1024
	ds_read_b128 v[148:151], v205 offset:2048
	ds_read_b128 v[152:155], v205 offset:3072
	ds_read_b128 v[182:185], v207
	ds_read_b128 v[186:189], v207 offset:1024
	ds_read_b128 v[196:199], v207 offset:2048
	ds_read_b128 v[212:215], v207 offset:3072
	ds_read_b128 v[216:219], v210
	ds_read_b128 v[220:223], v210 offset:1024
	ds_read_b128 v[224:227], v210 offset:2048
	ds_read_b128 v[228:231], v210 offset:3072
	ds_read_b128 v[232:235], v210 offset:4096
	ds_read_b128 v[236:239], v210 offset:5120
	ds_read_b128 v[244:247], v210 offset:6144
	ds_read_b128 v[248:251], v210 offset:7168
	s_waitcnt vmcnt(8)
	s_waitcnt lgkmcnt(0)
	s_barrier
	s_setprio 1
	s_waitcnt lgkmcnt(0)
	v_mfma_f32_16x16x32_bf16 v[130:133], v[140:143], v[216:219], v[130:133]
	v_mfma_f32_16x16x32_bf16 v[126:129], v[148:151], v[216:219], v[126:129]
	v_mfma_f32_16x16x32_bf16 v[114:117], v[140:143], v[224:227], v[114:117]
	v_mfma_f32_16x16x32_bf16 v[110:113], v[148:151], v[224:227], v[110:113]
	v_mfma_f32_16x16x32_bf16 v[98:101], v[140:143], v[232:235], v[98:101]
	v_mfma_f32_16x16x32_bf16 v[94:97], v[148:151], v[232:235], v[94:97]
	v_mfma_f32_16x16x32_bf16 v[82:85], v[140:143], v[244:247], v[82:85]
	v_mfma_f32_16x16x32_bf16 v[78:81], v[148:151], v[244:247], v[78:81]
	v_mfma_f32_16x16x32_bf16 v[130:133], v[144:147], v[220:223], v[130:133]
	v_mfma_f32_16x16x32_bf16 v[126:129], v[152:155], v[220:223], v[126:129]
	v_mfma_f32_16x16x32_bf16 v[114:117], v[144:147], v[228:231], v[114:117]
	v_mfma_f32_16x16x32_bf16 v[110:113], v[152:155], v[228:231], v[110:113]
	v_mfma_f32_16x16x32_bf16 v[98:101], v[144:147], v[236:239], v[98:101]
	v_mfma_f32_16x16x32_bf16 v[94:97], v[152:155], v[236:239], v[94:97]
	v_mfma_f32_16x16x32_bf16 v[82:85], v[144:147], v[248:251], v[82:85]
	v_mfma_f32_16x16x32_bf16 v[78:81], v[152:155], v[248:251], v[78:81]
	s_setprio 0
	s_setprio 1
	v_mfma_f32_16x16x32_bf16 v[122:125], v[182:185], v[216:219], v[122:125]
	v_mfma_f32_16x16x32_bf16 v[118:121], v[196:199], v[216:219], v[118:121]
	v_mfma_f32_16x16x32_bf16 v[106:109], v[182:185], v[224:227], v[106:109]
	v_mfma_f32_16x16x32_bf16 v[102:105], v[196:199], v[224:227], v[102:105]
	v_mfma_f32_16x16x32_bf16 v[90:93], v[182:185], v[232:235], v[90:93]
	v_mfma_f32_16x16x32_bf16 v[86:89], v[196:199], v[232:235], v[86:89]
	v_mfma_f32_16x16x32_bf16 v[74:77], v[182:185], v[244:247], v[74:77]
	v_mfma_f32_16x16x32_bf16 v[70:73], v[196:199], v[244:247], v[70:73]
	v_mfma_f32_16x16x32_bf16 v[122:125], v[186:189], v[220:223], v[122:125]
	v_mfma_f32_16x16x32_bf16 v[118:121], v[212:215], v[220:223], v[118:121]
	v_mfma_f32_16x16x32_bf16 v[106:109], v[186:189], v[228:231], v[106:109]
	v_mfma_f32_16x16x32_bf16 v[102:105], v[212:215], v[228:231], v[102:105]
	v_mfma_f32_16x16x32_bf16 v[90:93], v[186:189], v[236:239], v[90:93]
	v_mfma_f32_16x16x32_bf16 v[86:89], v[212:215], v[236:239], v[86:89]
	v_mfma_f32_16x16x32_bf16 v[74:77], v[186:189], v[248:251], v[74:77]
	v_mfma_f32_16x16x32_bf16 v[70:73], v[212:215], v[248:251], v[70:73]
	s_setprio 0
	s_barrier
	s_add_i32 s72, s63, s15
	v_lshl_add_u64 v[156:157], s[60:61], 0, v[160:161]
	s_mov_b32 m0, s72
	s_nop 0
	global_load_lds_dwordx4 v[156:157], off
	s_add_i32 m0, s72, 0x2000
	s_add_u32 s72, s60, 0x80000
	v_lshl_add_u64 v[178:179], s[60:61], 0, v[164:165]
	s_addc_u32 s73, s61, 0
	s_add_i32 s74, s64, s15
	global_load_lds_dwordx4 v[178:179], off
	v_lshl_add_u64 v[4:5], s[72:73], 0, v[160:161]
	s_mov_b32 m0, s74
	s_nop 0
	global_load_lds_dwordx4 v[4:5], off
	v_lshl_add_u64 v[4:5], s[72:73], 0, v[164:165]
	s_add_i32 m0, s74, 0x2000
	s_and_b64 s[72:73], s[10:11], s[58:59]
	s_and_b64 s[72:73], s[72:73], exec
	s_cselect_b32 s72, s38, s54
	s_cselect_b32 s73, s39, s55
	s_add_u32 s72, s72, s2
	s_addc_u32 s73, s73, 0
	global_load_lds_dwordx4 v[4:5], off
	v_lshl_add_u64 v[192:193], s[72:73], 0, v[158:159]
	s_mov_b32 m0, s42
	v_lshl_add_u64 v[202:203], s[72:73], 0, v[162:163]
	global_load_lds_dwordx4 v[192:193], off
	s_mov_b32 m0, s43
	s_nop 0
	global_load_lds_dwordx4 v[202:203], off
	ds_read_b128 v[216:219], v210 offset:16384
	ds_read_b128 v[220:223], v210 offset:17408
	ds_read_b128 v[224:227], v210 offset:18432
	ds_read_b128 v[228:231], v210 offset:19456
	ds_read_b128 v[232:235], v210 offset:20480
	ds_read_b128 v[236:239], v210 offset:21504
	ds_read_b128 v[244:247], v210 offset:22528
	ds_read_b128 v[248:251], v210 offset:23552
	s_waitcnt vmcnt(8)
	s_waitcnt lgkmcnt(0)
	s_barrier
	s_setprio 1
	s_waitcnt lgkmcnt(0)
	v_mfma_f32_16x16x32_bf16 v[66:69], v[140:143], v[216:219], v[66:69]
	v_mfma_f32_16x16x32_bf16 v[62:65], v[148:151], v[216:219], v[62:65]
	v_mfma_f32_16x16x32_bf16 v[50:53], v[140:143], v[224:227], v[50:53]
	v_mfma_f32_16x16x32_bf16 v[46:49], v[148:151], v[224:227], v[46:49]
	v_mfma_f32_16x16x32_bf16 v[34:37], v[140:143], v[232:235], v[34:37]
	v_mfma_f32_16x16x32_bf16 v[30:33], v[148:151], v[232:235], v[30:33]
	v_mfma_f32_16x16x32_bf16 v[18:21], v[140:143], v[244:247], v[18:21]
	v_mfma_f32_16x16x32_bf16 v[14:17], v[148:151], v[244:247], v[14:17]
	v_mfma_f32_16x16x32_bf16 v[66:69], v[144:147], v[220:223], v[66:69]
	v_mfma_f32_16x16x32_bf16 v[62:65], v[152:155], v[220:223], v[62:65]
	v_mfma_f32_16x16x32_bf16 v[50:53], v[144:147], v[228:231], v[50:53]
	v_mfma_f32_16x16x32_bf16 v[46:49], v[152:155], v[228:231], v[46:49]
	v_mfma_f32_16x16x32_bf16 v[34:37], v[144:147], v[236:239], v[34:37]
	v_mfma_f32_16x16x32_bf16 v[30:33], v[152:155], v[236:239], v[30:33]
	v_mfma_f32_16x16x32_bf16 v[18:21], v[144:147], v[248:251], v[18:21]
	v_mfma_f32_16x16x32_bf16 v[14:17], v[152:155], v[248:251], v[14:17]
	s_setprio 0
	s_setprio 1
	v_mfma_f32_16x16x32_bf16 v[58:61], v[182:185], v[216:219], v[58:61]
	v_mfma_f32_16x16x32_bf16 v[54:57], v[196:199], v[216:219], v[54:57]
	v_mfma_f32_16x16x32_bf16 v[42:45], v[182:185], v[224:227], v[42:45]
	v_mfma_f32_16x16x32_bf16 v[38:41], v[196:199], v[224:227], v[38:41]
	v_mfma_f32_16x16x32_bf16 v[26:29], v[182:185], v[232:235], v[26:29]
	v_mfma_f32_16x16x32_bf16 v[22:25], v[196:199], v[232:235], v[22:25]
	v_mfma_f32_16x16x32_bf16 v[10:13], v[182:185], v[244:247], v[10:13]
	v_mfma_f32_16x16x32_bf16 v[4:7], v[196:199], v[244:247], v[6:9]
	v_mfma_f32_16x16x32_bf16 v[58:61], v[186:189], v[220:223], v[58:61]
	v_mfma_f32_16x16x32_bf16 v[54:57], v[212:215], v[220:223], v[54:57]
	v_mfma_f32_16x16x32_bf16 v[42:45], v[186:189], v[228:231], v[42:45]
	v_mfma_f32_16x16x32_bf16 v[38:41], v[212:215], v[228:231], v[38:41]
	v_mfma_f32_16x16x32_bf16 v[26:29], v[186:189], v[236:239], v[26:29]
	v_mfma_f32_16x16x32_bf16 v[22:25], v[212:215], v[236:239], v[22:25]
	v_mfma_f32_16x16x32_bf16 v[10:13], v[186:189], v[248:251], v[10:13]
	v_mfma_f32_16x16x32_bf16 v[4:7], v[212:215], v[248:251], v[4:7]
	s_setprio 0
	s_barrier
	s_add_u32 s72, s72, 0x80000
	s_addc_u32 s73, s73, 0
	s_mov_b32 m0, s48
	v_lshl_add_u64 v[8:9], s[72:73], 0, v[158:159]
	global_load_lds_dwordx4 v[8:9], off
	v_lshl_add_u64 v[8:9], s[72:73], 0, v[162:163]
	s_mov_b32 m0, s49
	s_nop 0
	global_load_lds_dwordx4 v[8:9], off
	s_add_i32 s2, 0, 0x18000
	v_add_u32_e32 v3, s2, v177
	s_add_i32 s74, 0, 0x1c000
	ds_read_b128 v[140:143], v3
	ds_read_b128 v[144:147], v3 offset:1024
	ds_read_b128 v[148:151], v3 offset:2048
	ds_read_b128 v[152:155], v3 offset:3072
	v_add_u32_e32 v3, s74, v177
	ds_read_b128 v[182:185], v3
	ds_read_b128 v[186:189], v3 offset:1024
	ds_read_b128 v[196:199], v3 offset:2048
	ds_read_b128 v[212:215], v3 offset:3072
	ds_read_b128 v[216:219], v210 offset:32768
	ds_read_b128 v[220:223], v210 offset:33792
	ds_read_b128 v[224:227], v210 offset:34816
	ds_read_b128 v[228:231], v210 offset:35840
	ds_read_b128 v[232:235], v210 offset:36864
	ds_read_b128 v[236:239], v210 offset:37888
	ds_read_b128 v[244:247], v210 offset:38912
	ds_read_b128 v[248:251], v210 offset:39936
	s_waitcnt vmcnt(8)
	s_waitcnt lgkmcnt(0)
	s_barrier
	s_setprio 1
	s_waitcnt lgkmcnt(0)
	v_mfma_f32_16x16x32_bf16 v[130:133], v[140:143], v[216:219], v[130:133]
	v_mfma_f32_16x16x32_bf16 v[126:129], v[148:151], v[216:219], v[126:129]
	v_mfma_f32_16x16x32_bf16 v[114:117], v[140:143], v[224:227], v[114:117]
	v_mfma_f32_16x16x32_bf16 v[110:113], v[148:151], v[224:227], v[110:113]
	v_mfma_f32_16x16x32_bf16 v[98:101], v[140:143], v[232:235], v[98:101]
	v_mfma_f32_16x16x32_bf16 v[94:97], v[148:151], v[232:235], v[94:97]
	v_mfma_f32_16x16x32_bf16 v[82:85], v[140:143], v[244:247], v[82:85]
	v_mfma_f32_16x16x32_bf16 v[78:81], v[148:151], v[244:247], v[78:81]
	v_mfma_f32_16x16x32_bf16 v[130:133], v[144:147], v[220:223], v[130:133]
	v_mfma_f32_16x16x32_bf16 v[126:129], v[152:155], v[220:223], v[126:129]
	v_mfma_f32_16x16x32_bf16 v[114:117], v[144:147], v[228:231], v[114:117]
	v_mfma_f32_16x16x32_bf16 v[110:113], v[152:155], v[228:231], v[110:113]
	v_mfma_f32_16x16x32_bf16 v[98:101], v[144:147], v[236:239], v[98:101]
	v_mfma_f32_16x16x32_bf16 v[94:97], v[152:155], v[236:239], v[94:97]
	v_mfma_f32_16x16x32_bf16 v[82:85], v[144:147], v[248:251], v[82:85]
	v_mfma_f32_16x16x32_bf16 v[78:81], v[152:155], v[248:251], v[78:81]
	s_setprio 0
	s_setprio 1
	v_mfma_f32_16x16x32_bf16 v[122:125], v[182:185], v[216:219], v[122:125]
	v_mfma_f32_16x16x32_bf16 v[118:121], v[196:199], v[216:219], v[118:121]
	v_mfma_f32_16x16x32_bf16 v[106:109], v[182:185], v[224:227], v[106:109]
	v_mfma_f32_16x16x32_bf16 v[102:105], v[196:199], v[224:227], v[102:105]
	v_mfma_f32_16x16x32_bf16 v[90:93], v[182:185], v[232:235], v[90:93]
	v_mfma_f32_16x16x32_bf16 v[86:89], v[196:199], v[232:235], v[86:89]
	v_mfma_f32_16x16x32_bf16 v[74:77], v[182:185], v[244:247], v[74:77]
	v_mfma_f32_16x16x32_bf16 v[70:73], v[196:199], v[244:247], v[70:73]
	v_mfma_f32_16x16x32_bf16 v[122:125], v[186:189], v[220:223], v[122:125]
	v_mfma_f32_16x16x32_bf16 v[118:121], v[212:215], v[220:223], v[118:121]
	v_mfma_f32_16x16x32_bf16 v[106:109], v[186:189], v[228:231], v[106:109]
	v_mfma_f32_16x16x32_bf16 v[102:105], v[212:215], v[228:231], v[102:105]
	v_mfma_f32_16x16x32_bf16 v[90:93], v[186:189], v[236:239], v[90:93]
	v_mfma_f32_16x16x32_bf16 v[86:89], v[212:215], v[236:239], v[86:89]
	v_mfma_f32_16x16x32_bf16 v[74:77], v[186:189], v[248:251], v[74:77]
	v_mfma_f32_16x16x32_bf16 v[70:73], v[212:215], v[248:251], v[70:73]
	s_setprio 0
	s_barrier
	s_add_i32 s2, s2, s15
	v_lshl_add_u64 v[8:9], v[156:157], 0, s[28:29]
	s_mov_b32 m0, s2
	s_nop 0
	global_load_lds_dwordx4 v[8:9], off
	s_add_i32 m0, s2, 0x2000
	s_add_u32 s60, s60, 0x80080
	v_lshl_add_u64 v[8:9], v[178:179], 0, s[28:29]
	s_addc_u32 s61, s61, 0
	s_add_i32 s2, s74, s15
	global_load_lds_dwordx4 v[8:9], off
	v_lshl_add_u64 v[8:9], s[60:61], 0, v[160:161]
	s_mov_b32 m0, s2
	s_nop 0
	global_load_lds_dwordx4 v[8:9], off
	v_lshl_add_u64 v[8:9], s[60:61], 0, v[164:165]
	s_add_i32 m0, s2, 0x2000
	s_nop 0
	global_load_lds_dwordx4 v[8:9], off
	v_lshl_add_u64 v[8:9], v[192:193], 0, s[28:29]
	s_mov_b32 m0, s51
	s_nop 0
	global_load_lds_dwordx4 v[8:9], off
	v_lshl_add_u64 v[8:9], v[202:203], 0, s[28:29]
	s_mov_b32 m0, s52
	s_nop 0
	global_load_lds_dwordx4 v[8:9], off
	ds_read_b128 v[216:219], v210 offset:49152
	ds_read_b128 v[220:223], v210 offset:50176
	ds_read_b128 v[224:227], v210 offset:51200
	ds_read_b128 v[228:231], v210 offset:52224
	ds_read_b128 v[232:235], v210 offset:53248
	ds_read_b128 v[236:239], v210 offset:54272
	ds_read_b128 v[244:247], v210 offset:55296
	ds_read_b128 v[248:251], v210 offset:56320
	s_waitcnt vmcnt(8)
	s_waitcnt lgkmcnt(0)
	s_barrier
	s_setprio 1
	s_waitcnt lgkmcnt(0)
	v_mfma_f32_16x16x32_bf16 v[66:69], v[140:143], v[216:219], v[66:69]
	v_mfma_f32_16x16x32_bf16 v[62:65], v[148:151], v[216:219], v[62:65]
	v_mfma_f32_16x16x32_bf16 v[50:53], v[140:143], v[224:227], v[50:53]
	v_mfma_f32_16x16x32_bf16 v[46:49], v[148:151], v[224:227], v[46:49]
	v_mfma_f32_16x16x32_bf16 v[34:37], v[140:143], v[232:235], v[34:37]
	v_mfma_f32_16x16x32_bf16 v[30:33], v[148:151], v[232:235], v[30:33]
	v_mfma_f32_16x16x32_bf16 v[18:21], v[140:143], v[244:247], v[18:21]
	v_mfma_f32_16x16x32_bf16 v[14:17], v[148:151], v[244:247], v[14:17]
	v_mfma_f32_16x16x32_bf16 v[66:69], v[144:147], v[220:223], v[66:69]
	v_mfma_f32_16x16x32_bf16 v[62:65], v[152:155], v[220:223], v[62:65]
	v_mfma_f32_16x16x32_bf16 v[50:53], v[144:147], v[228:231], v[50:53]
	v_mfma_f32_16x16x32_bf16 v[46:49], v[152:155], v[228:231], v[46:49]
	v_mfma_f32_16x16x32_bf16 v[34:37], v[144:147], v[236:239], v[34:37]
	v_mfma_f32_16x16x32_bf16 v[30:33], v[152:155], v[236:239], v[30:33]
	v_mfma_f32_16x16x32_bf16 v[18:21], v[144:147], v[248:251], v[18:21]
	v_mfma_f32_16x16x32_bf16 v[14:17], v[152:155], v[248:251], v[14:17]
	s_setprio 0
	s_setprio 1
	v_mfma_f32_16x16x32_bf16 v[58:61], v[182:185], v[216:219], v[58:61]
	v_mfma_f32_16x16x32_bf16 v[54:57], v[196:199], v[216:219], v[54:57]
	v_mfma_f32_16x16x32_bf16 v[42:45], v[182:185], v[224:227], v[42:45]
	v_mfma_f32_16x16x32_bf16 v[38:41], v[196:199], v[224:227], v[38:41]
	v_mfma_f32_16x16x32_bf16 v[26:29], v[182:185], v[232:235], v[26:29]
	v_mfma_f32_16x16x32_bf16 v[22:25], v[196:199], v[232:235], v[22:25]
	v_mfma_f32_16x16x32_bf16 v[8:11], v[182:185], v[244:247], v[10:13]
	v_mfma_f32_16x16x32_bf16 v[4:7], v[196:199], v[244:247], v[4:7]
	v_mfma_f32_16x16x32_bf16 v[58:61], v[186:189], v[220:223], v[58:61]
	v_mfma_f32_16x16x32_bf16 v[54:57], v[212:215], v[220:223], v[54:57]
	v_mfma_f32_16x16x32_bf16 v[42:45], v[186:189], v[228:231], v[42:45]
	v_mfma_f32_16x16x32_bf16 v[38:41], v[212:215], v[228:231], v[38:41]
	v_mfma_f32_16x16x32_bf16 v[26:29], v[186:189], v[236:239], v[26:29]
	v_mfma_f32_16x16x32_bf16 v[22:25], v[212:215], v[236:239], v[22:25]
	v_mfma_f32_16x16x32_bf16 v[10:13], v[186:189], v[248:251], v[8:11]
	v_mfma_f32_16x16x32_bf16 v[6:9], v[212:215], v[248:251], v[4:7]
	s_setprio 0
	s_barrier
	s_add_i32 s2, s71, 4
	s_and_b32 s2, s2, 6
	s_cmp_lg_u32 s2, 0
	s_cselect_b64 s[60:61], -1, 0
	s_or_b64 s[58:59], s[58:59], s[60:61]
	s_and_b64 vcc, exec, s[58:59]
	s_cbranch_vccnz .LBB0_711
	ds_read2st64_b32 v[4:5], v138 offset1:1
	ds_read2st64_b32 v[140:141], v138 offset0:2 offset1:3
	ds_read2st64_b32 v[142:143], v138 offset0:8 offset1:9
	ds_read2st64_b32 v[144:145], v138 offset0:10 offset1:11
	s_waitcnt lgkmcnt(0)
	v_pk_mul_f32 v[132:133], v[132:133], v[4:5] op_sel_hi:[1,0]
	v_pk_mul_f32 v[130:131], v[130:131], v[4:5] op_sel_hi:[1,0]
	v_pk_mul_f32 v[128:129], v[128:129], v[4:5] op_sel_hi:[1,0]
	v_pk_mul_f32 v[126:127], v[126:127], v[4:5] op_sel_hi:[1,0]
	v_pk_mul_f32 v[124:125], v[124:125], v[4:5] op_sel_hi:[1,0]
	v_pk_mul_f32 v[122:123], v[122:123], v[4:5] op_sel_hi:[1,0]
	v_pk_mul_f32 v[120:121], v[120:121], v[4:5] op_sel_hi:[1,0]
	v_pk_mul_f32 v[118:119], v[118:119], v[4:5] op_sel_hi:[1,0]
	v_mov_b32_e32 v4, v5
	v_pk_mul_f32 v[116:117], v[116:117], v[4:5] op_sel_hi:[1,0]
	v_pk_mul_f32 v[114:115], v[114:115], v[4:5] op_sel_hi:[1,0]
	v_pk_mul_f32 v[112:113], v[112:113], v[4:5] op_sel_hi:[1,0]
	v_pk_mul_f32 v[110:111], v[110:111], v[4:5] op_sel_hi:[1,0]
	v_pk_mul_f32 v[108:109], v[108:109], v[4:5] op_sel_hi:[1,0]
	v_pk_mul_f32 v[106:107], v[106:107], v[4:5] op_sel_hi:[1,0]
	v_pk_mul_f32 v[104:105], v[104:105], v[4:5] op_sel_hi:[1,0]
	v_pk_mul_f32 v[102:103], v[102:103], v[4:5] op_sel_hi:[1,0]
	v_mov_b32_e32 v4, v141
	v_pk_mul_f32 v[84:85], v[84:85], v[4:5] op_sel_hi:[1,0]
	v_pk_mul_f32 v[82:83], v[82:83], v[4:5] op_sel_hi:[1,0]
	v_pk_mul_f32 v[80:81], v[80:81], v[4:5] op_sel_hi:[1,0]
	v_pk_mul_f32 v[78:79], v[78:79], v[4:5] op_sel_hi:[1,0]
	v_pk_mul_f32 v[76:77], v[76:77], v[4:5] op_sel_hi:[1,0]
	v_pk_mul_f32 v[74:75], v[74:75], v[4:5] op_sel_hi:[1,0]
	v_pk_mul_f32 v[72:73], v[72:73], v[4:5] op_sel_hi:[1,0]
	v_pk_mul_f32 v[70:71], v[70:71], v[4:5] op_sel_hi:[1,0]
	v_mov_b32_e32 v4, v143
	v_pk_mul_f32 v[52:53], v[52:53], v[4:5] op_sel_hi:[1,0]
	v_pk_mul_f32 v[50:51], v[50:51], v[4:5] op_sel_hi:[1,0]
	v_pk_mul_f32 v[48:49], v[48:49], v[4:5] op_sel_hi:[1,0]
	v_pk_mul_f32 v[46:47], v[46:47], v[4:5] op_sel_hi:[1,0]
	v_pk_mul_f32 v[44:45], v[44:45], v[4:5] op_sel_hi:[1,0]
	v_pk_mul_f32 v[42:43], v[42:43], v[4:5] op_sel_hi:[1,0]
	v_pk_mul_f32 v[40:41], v[40:41], v[4:5] op_sel_hi:[1,0]
	v_pk_mul_f32 v[38:39], v[38:39], v[4:5] op_sel_hi:[1,0]
	v_mov_b32_e32 v4, v145
	v_pk_mul_f32 v[100:101], v[100:101], v[140:141] op_sel_hi:[1,0]
	v_pk_mul_f32 v[98:99], v[98:99], v[140:141] op_sel_hi:[1,0]
	v_pk_mul_f32 v[96:97], v[96:97], v[140:141] op_sel_hi:[1,0]
	v_pk_mul_f32 v[94:95], v[94:95], v[140:141] op_sel_hi:[1,0]
	v_pk_mul_f32 v[92:93], v[92:93], v[140:141] op_sel_hi:[1,0]
	v_pk_mul_f32 v[90:91], v[90:91], v[140:141] op_sel_hi:[1,0]
	v_pk_mul_f32 v[88:89], v[88:89], v[140:141] op_sel_hi:[1,0]
	v_pk_mul_f32 v[86:87], v[86:87], v[140:141] op_sel_hi:[1,0]
	v_pk_mul_f32 v[68:69], v[68:69], v[142:143] op_sel_hi:[1,0]
	v_pk_mul_f32 v[66:67], v[66:67], v[142:143] op_sel_hi:[1,0]
	v_pk_mul_f32 v[64:65], v[64:65], v[142:143] op_sel_hi:[1,0]
	v_pk_mul_f32 v[62:63], v[62:63], v[142:143] op_sel_hi:[1,0]
	v_pk_mul_f32 v[60:61], v[60:61], v[142:143] op_sel_hi:[1,0]
	v_pk_mul_f32 v[58:59], v[58:59], v[142:143] op_sel_hi:[1,0]
	v_pk_mul_f32 v[56:57], v[56:57], v[142:143] op_sel_hi:[1,0]
	v_pk_mul_f32 v[54:55], v[54:55], v[142:143] op_sel_hi:[1,0]
	v_pk_mul_f32 v[36:37], v[36:37], v[144:145] op_sel_hi:[1,0]
	v_pk_mul_f32 v[34:35], v[34:35], v[144:145] op_sel_hi:[1,0]
	v_pk_mul_f32 v[32:33], v[32:33], v[144:145] op_sel_hi:[1,0]
	v_pk_mul_f32 v[30:31], v[30:31], v[144:145] op_sel_hi:[1,0]
	v_pk_mul_f32 v[28:29], v[28:29], v[144:145] op_sel_hi:[1,0]
	v_pk_mul_f32 v[26:27], v[26:27], v[144:145] op_sel_hi:[1,0]
	v_pk_mul_f32 v[24:25], v[24:25], v[144:145] op_sel_hi:[1,0]
	v_pk_mul_f32 v[22:23], v[22:23], v[144:145] op_sel_hi:[1,0]
	v_pk_mul_f32 v[20:21], v[20:21], v[4:5] op_sel_hi:[1,0]
	v_pk_mul_f32 v[18:19], v[18:19], v[4:5] op_sel_hi:[1,0]
	v_pk_mul_f32 v[16:17], v[16:17], v[4:5] op_sel_hi:[1,0]
	v_pk_mul_f32 v[14:15], v[14:15], v[4:5] op_sel_hi:[1,0]
	v_pk_mul_f32 v[12:13], v[12:13], v[4:5] op_sel_hi:[1,0]
	v_pk_mul_f32 v[10:11], v[10:11], v[4:5] op_sel_hi:[1,0]
	v_pk_mul_f32 v[8:9], v[8:9], v[4:5] op_sel_hi:[1,0]
	v_pk_mul_f32 v[6:7], v[6:7], v[4:5] op_sel_hi:[1,0]
	s_branch .LBB0_711

.LBB0_812:
	s_mov_b64 s[56:57], s[38:39]
	s_add_u32 s74, s71, s56
	s_addc_u32 s75, s72, s57
	s_add_u32 s38, s56, 0x100
	s_addc_u32 s39, s57, 0
	s_cmp_eq_u32 s73, 12
	s_cselect_b64 s[40:41], -1, 0
	s_and_b64 s[54:55], s[40:41], exec
	s_cselect_b32 s75, s27, s75
	s_cselect_b32 s74, s29, s74
	s_cselect_b32 s54, 0, s38
	s_add_i32 s81, s68, s43
	s_add_i32 m0, s48, 0xc000
	s_add_i32 s80, s48, 0xe000
	s_add_i32 s82, s81, 0x2000
	s_add_u32 s76, s74, 0x80000
	s_addc_u32 s77, s75, 0
	s_and_b64 s[40:41], s[6:7], s[40:41]
	s_and_b64 s[40:41], s[40:41], exec
	s_cselect_b32 s41, s30, s14
	s_cselect_b32 s40, s31, s15
	s_add_u32 s78, s41, s54
	ds_read_b128 v[66:69], v135
	ds_read_b128 v[70:73], v135 offset:1024
	ds_read_b128 v[74:77], v135 offset:2048
	ds_read_b128 v[78:81], v135 offset:3072
	s_addc_u32 s79, s40, 0
	s_add_i32 s83, 0, 0x18000
	s_add_u32 s54, s78, 0x80000
	s_addc_u32 s55, s79, 0
	s_add_i32 s84, s83, s43
	s_add_i32 s85, s84, 0x2000
	s_add_u32 s40, s74, 0x80080
	s_addc_u32 s41, s75, 0
	s_cmp_lg_u32 s73, 12
	v_lshl_add_u64 v[138:139], v[128:129], 0, s[56:57]
	ds_read_b128 v[82:85], v136
	ds_read_b128 v[86:89], v136 offset:1024
	ds_read_b128 v[90:93], v136 offset:2048
	ds_read_b128 v[94:97], v136 offset:3072
	ds_read_b128 v[98:101], v136 offset:4096
	ds_read_b128 v[102:105], v136 offset:5120
	ds_read_b128 v[106:109], v136 offset:6144
	ds_read_b128 v[110:113], v136 offset:7168
	global_load_lds_dwordx4 v[138:139], off
	v_lshl_add_u64 v[138:139], v[130:131], 0, s[56:57]
	s_mov_b32 m0, s80
	s_nop 0
	global_load_lds_dwordx4 v[138:139], off
	s_waitcnt vmcnt(8)
	s_waitcnt lgkmcnt(0)
	s_barrier
	s_setprio 1
	s_waitcnt lgkmcnt(0)
	v_mfma_f32_16x16x32_bf16 v[62:65], v[66:69], v[82:85], v[62:65]
	v_mfma_f32_16x16x32_bf16 v[54:57], v[74:77], v[82:85], v[54:57]
	v_mfma_f32_16x16x32_bf16 v[46:49], v[66:69], v[90:93], v[46:49]
	v_mfma_f32_16x16x32_bf16 v[42:45], v[74:77], v[90:93], v[42:45]
	v_mfma_f32_16x16x32_bf16 v[38:41], v[66:69], v[98:101], v[38:41]
	v_mfma_f32_16x16x32_bf16 v[30:33], v[74:77], v[98:101], v[30:33]
	v_mfma_f32_16x16x32_bf16 v[22:25], v[66:69], v[106:109], v[22:25]
	v_mfma_f32_16x16x32_bf16 v[18:21], v[74:77], v[106:109], v[18:21]
	v_mfma_f32_16x16x32_bf16 v[62:65], v[70:73], v[86:89], v[62:65]
	v_mfma_f32_16x16x32_bf16 v[54:57], v[78:81], v[86:89], v[54:57]
	v_mfma_f32_16x16x32_bf16 v[46:49], v[70:73], v[94:97], v[46:49]
	v_mfma_f32_16x16x32_bf16 v[42:45], v[78:81], v[94:97], v[42:45]
	v_mfma_f32_16x16x32_bf16 v[38:41], v[70:73], v[102:105], v[38:41]
	v_mfma_f32_16x16x32_bf16 v[30:33], v[78:81], v[102:105], v[30:33]
	v_mfma_f32_16x16x32_bf16 v[22:25], v[70:73], v[110:113], v[22:25]
	v_mfma_f32_16x16x32_bf16 v[18:21], v[78:81], v[110:113], v[18:21]
	s_setprio 0
	s_setprio 1
	s_setprio 0
	s_barrier
	s_mov_b32 m0, s81
	v_lshl_add_u64 v[138:139], s[74:75], 0, v[114:115]
	global_load_lds_dwordx4 v[138:139], off
	v_lshl_add_u64 v[140:141], s[74:75], 0, v[116:117]
	s_mov_b32 m0, s82
	v_lshl_add_u64 v[142:143], s[76:77], 0, v[114:115]
	global_load_lds_dwordx4 v[140:141], off
	s_mov_b32 m0, s49
	v_lshl_add_u64 v[144:145], s[78:79], 0, v[116:117]
	global_load_lds_dwordx4 v[142:143], off
	v_lshl_add_u64 v[142:143], s[76:77], 0, v[116:117]
	s_mov_b32 m0, s50
	s_nop 0
	global_load_lds_dwordx4 v[142:143], off
	v_lshl_add_u64 v[142:143], s[78:79], 0, v[114:115]
	s_mov_b32 m0, s48
	s_nop 0
	global_load_lds_dwordx4 v[142:143], off
	s_mov_b32 m0, s51
	s_nop 0
	global_load_lds_dwordx4 v[144:145], off
	ds_read_b128 v[82:85], v136 offset:16384
	ds_read_b128 v[86:89], v136 offset:17408
	ds_read_b128 v[90:93], v136 offset:18432
	ds_read_b128 v[94:97], v136 offset:19456
	ds_read_b128 v[98:101], v136 offset:20480
	ds_read_b128 v[102:105], v136 offset:21504
	ds_read_b128 v[106:109], v136 offset:22528
	ds_read_b128 v[110:113], v136 offset:23552
	s_waitcnt vmcnt(8)
	s_waitcnt lgkmcnt(0)
	s_barrier
	s_setprio 1
	s_waitcnt lgkmcnt(0)
	v_mfma_f32_16x16x32_bf16 v[58:61], v[66:69], v[82:85], v[58:61]
	v_mfma_f32_16x16x32_bf16 v[50:53], v[74:77], v[82:85], v[50:53]
	v_mfma_f32_16x16x32_bf16 v[34:37], v[66:69], v[90:93], v[34:37]
	v_mfma_f32_16x16x32_bf16 v[26:29], v[74:77], v[90:93], v[26:29]
	v_mfma_f32_16x16x32_bf16 v[14:17], v[66:69], v[98:101], v[14:17]
	v_mfma_f32_16x16x32_bf16 v[10:13], v[74:77], v[98:101], v[10:13]
	v_mfma_f32_16x16x32_bf16 v[6:9], v[66:69], v[106:109], v[6:9]
	v_mfma_f32_16x16x32_bf16 v[2:5], v[74:77], v[106:109], v[2:5]
	v_mfma_f32_16x16x32_bf16 v[58:61], v[70:73], v[86:89], v[58:61]
	v_mfma_f32_16x16x32_bf16 v[50:53], v[78:81], v[86:89], v[50:53]
	v_mfma_f32_16x16x32_bf16 v[34:37], v[70:73], v[94:97], v[34:37]
	v_mfma_f32_16x16x32_bf16 v[26:29], v[78:81], v[94:97], v[26:29]
	v_mfma_f32_16x16x32_bf16 v[14:17], v[70:73], v[102:105], v[14:17]
	v_mfma_f32_16x16x32_bf16 v[10:13], v[78:81], v[102:105], v[10:13]
	v_mfma_f32_16x16x32_bf16 v[6:9], v[70:73], v[110:113], v[6:9]
	v_mfma_f32_16x16x32_bf16 v[2:5], v[78:81], v[110:113], v[2:5]
	s_setprio 0
	s_setprio 1
	s_setprio 0
	s_barrier
	s_mov_b32 m0, s52
	v_lshl_add_u64 v[146:147], s[54:55], 0, v[114:115]
	global_load_lds_dwordx4 v[146:147], off
	v_lshl_add_u64 v[146:147], s[54:55], 0, v[116:117]
	s_mov_b32 m0, s53
	s_nop 0
	global_load_lds_dwordx4 v[146:147], off
	v_add_u32_e32 v78, s83, v133
	ds_read_b128 v[66:69], v78
	ds_read_b128 v[70:73], v78 offset:1024
	ds_read_b128 v[74:77], v78 offset:2048
	ds_read_b128 v[78:81], v78 offset:3072
	ds_read_b128 v[82:85], v136 offset:32768
	ds_read_b128 v[86:89], v136 offset:33792
	ds_read_b128 v[90:93], v136 offset:34816
	ds_read_b128 v[94:97], v136 offset:35840
	ds_read_b128 v[98:101], v136 offset:36864
	ds_read_b128 v[102:105], v136 offset:37888
	ds_read_b128 v[106:109], v136 offset:38912
	ds_read_b128 v[110:113], v136 offset:39936
	s_waitcnt vmcnt(8)
	s_waitcnt lgkmcnt(0)
	s_barrier
	s_setprio 1
	s_waitcnt lgkmcnt(0)
	v_mfma_f32_16x16x32_bf16 v[62:65], v[66:69], v[82:85], v[62:65]
	v_mfma_f32_16x16x32_bf16 v[54:57], v[74:77], v[82:85], v[54:57]
	v_mfma_f32_16x16x32_bf16 v[46:49], v[66:69], v[90:93], v[46:49]
	v_mfma_f32_16x16x32_bf16 v[42:45], v[74:77], v[90:93], v[42:45]
	v_mfma_f32_16x16x32_bf16 v[38:41], v[66:69], v[98:101], v[38:41]
	v_mfma_f32_16x16x32_bf16 v[30:33], v[74:77], v[98:101], v[30:33]
	v_mfma_f32_16x16x32_bf16 v[22:25], v[66:69], v[106:109], v[22:25]
	v_mfma_f32_16x16x32_bf16 v[18:21], v[74:77], v[106:109], v[18:21]
	v_mfma_f32_16x16x32_bf16 v[62:65], v[70:73], v[86:89], v[62:65]
	v_mfma_f32_16x16x32_bf16 v[54:57], v[78:81], v[86:89], v[54:57]
	v_mfma_f32_16x16x32_bf16 v[46:49], v[70:73], v[94:97], v[46:49]
	v_mfma_f32_16x16x32_bf16 v[42:45], v[78:81], v[94:97], v[42:45]
	v_mfma_f32_16x16x32_bf16 v[38:41], v[70:73], v[102:105], v[38:41]
	v_mfma_f32_16x16x32_bf16 v[30:33], v[78:81], v[102:105], v[30:33]
	v_mfma_f32_16x16x32_bf16 v[22:25], v[70:73], v[110:113], v[22:25]
	v_mfma_f32_16x16x32_bf16 v[18:21], v[78:81], v[110:113], v[18:21]
	s_setprio 0
	s_setprio 1
	s_setprio 0
	s_barrier
	s_mov_b32 m0, s84
	v_lshl_add_u64 v[138:139], v[138:139], 0, s[12:13]
	global_load_lds_dwordx4 v[138:139], off
	v_lshl_add_u64 v[138:139], v[140:141], 0, s[12:13]
	s_mov_b32 m0, s85
	s_nop 0
	global_load_lds_dwordx4 v[138:139], off
	v_lshl_add_u64 v[138:139], s[40:41], 0, v[114:115]
	s_mov_b32 m0, s65
	s_nop 0
	global_load_lds_dwordx4 v[138:139], off
	v_lshl_add_u64 v[138:139], s[40:41], 0, v[116:117]
	s_mov_b32 m0, s66
	s_nop 0
	global_load_lds_dwordx4 v[138:139], off
	v_lshl_add_u64 v[138:139], v[142:143], 0, s[12:13]
	s_mov_b32 m0, s63
	s_nop 0
	global_load_lds_dwordx4 v[138:139], off
	v_lshl_add_u64 v[138:139], v[144:145], 0, s[12:13]
	s_mov_b32 m0, s64
	s_nop 0
	global_load_lds_dwordx4 v[138:139], off
	ds_read_b128 v[106:109], v136 offset:49152
	ds_read_b128 v[110:113], v136 offset:50176
	ds_read_b128 v[98:101], v136 offset:51200
	ds_read_b128 v[102:105], v136 offset:52224
	ds_read_b128 v[90:93], v136 offset:53248
	ds_read_b128 v[94:97], v136 offset:54272
	ds_read_b128 v[82:85], v136 offset:55296
	ds_read_b128 v[86:89], v136 offset:56320
	s_waitcnt vmcnt(8)
	s_waitcnt lgkmcnt(0)
	s_barrier
	s_cbranch_scc1 .LBB0_811
	v_mov_b32_e32 v137, v1
	v_mov_b32_e32 v138, v132
	s_andn2_b64 vcc, exec, s[16:17]
	s_cbranch_vccnz .LBB0_810
	v_add_u32_e32 v140, s70, v137
	v_ashrrev_i32_e32 v141, 31, v140
	v_lshl_add_u32 v138, v138, 2, s62
	v_lshlrev_b64 v[140:141], 8, v[140:141]
	v_ashrrev_i32_e32 v139, 31, v138
	v_lshl_add_u64 v[140:141], s[36:37], 0, v[140:141]
	v_lshl_add_u64 v[138:139], v[138:139], 2, v[140:141]
	v_add_co_u32_e32 v142, vcc, 0x1000, v138
	global_store_dwordx4 v[138:139], v[62:65], off
	global_store_dwordx4 v[138:139], v[54:57], off offset:64
	v_addc_co_u32_e32 v143, vcc, 0, v139, vcc
	v_lshl_add_u64 v[140:141], v[138:139], 0, s[20:21]
	global_store_dwordx4 v[142:143], v[46:49], off
	global_store_dwordx4 v[140:141], v[42:45], off offset:64
	v_add_co_u32_e32 v142, vcc, 0x2000, v138
	v_lshl_add_u64 v[140:141], v[138:139], 0, s[22:23]
	s_nop 0
	v_addc_co_u32_e32 v143, vcc, 0, v139, vcc
	global_store_dwordx4 v[142:143], v[38:41], off
	global_store_dwordx4 v[140:141], v[30:33], off offset:64
	v_lshl_add_u64 v[140:141], v[138:139], 0, s[24:25]
	v_add_co_u32_e32 v138, vcc, 0x3000, v138
	s_nop 1
	v_addc_co_u32_e32 v139, vcc, 0, v139, vcc
	global_store_dwordx4 v[138:139], v[22:25], off
	global_store_dwordx4 v[140:141], v[18:21], off offset:64
	s_branch .LBB0_810

.LBB0_1005:
	s_add_u32 s40, s64, s10
	s_addc_u32 s41, s65, s11
	s_add_u32 s38, s10, 0x100
	s_addc_u32 s39, s11, 0
	s_cmpk_eq_i32 s10, 0xf00
	s_cselect_b64 vcc, -1, 0
	s_and_b64 s[2:3], vcc, exec
	s_cselect_b32 s41, s31, s41
	s_cselect_b32 s40, s37, s40
	s_cselect_b32 s67, 0, s38
	v_lshl_add_u64 v[226:227], v[146:147], 0, s[10:11]
	s_add_i32 m0, s49, 0xc000
	s_nop 0
	global_load_lds_dwordx4 v[226:227], off
	v_lshl_add_u64 v[226:227], v[144:145], 0, s[10:11]
	s_add_i32 m0, s49, 0xe000
	s_nop 0
	global_load_lds_dwordx4 v[226:227], off
	ds_read_b128 v[152:155], v158
	ds_read_b128 v[166:169], v158 offset:1024
	ds_read_b128 v[170:173], v158 offset:2048
	ds_read_b128 v[174:177], v158 offset:3072
	ds_read_b128 v[178:181], v159
	ds_read_b128 v[182:185], v159 offset:1024
	ds_read_b128 v[186:189], v159 offset:2048
	ds_read_b128 v[190:193], v159 offset:3072
	ds_read_b128 v[194:197], v160
	ds_read_b128 v[198:201], v160 offset:1024
	ds_read_b128 v[202:205], v160 offset:2048
	ds_read_b128 v[206:209], v160 offset:3072
	ds_read_b128 v[210:213], v160 offset:4096
	ds_read_b128 v[214:217], v160 offset:5120
	ds_read_b128 v[218:221], v160 offset:6144
	ds_read_b128 v[222:225], v160 offset:7168
	s_waitcnt vmcnt(8)
	s_waitcnt lgkmcnt(0)
	s_barrier
	s_setprio 1
	s_waitcnt lgkmcnt(0)
	v_mfma_f32_16x16x32_bf16 v[126:129], v[152:155], v[194:197], v[126:129]
	v_mfma_f32_16x16x32_bf16 v[122:125], v[170:173], v[194:197], v[122:125]
	v_mfma_f32_16x16x32_bf16 v[110:113], v[152:155], v[202:205], v[110:113]
	v_mfma_f32_16x16x32_bf16 v[106:109], v[170:173], v[202:205], v[106:109]
	v_mfma_f32_16x16x32_bf16 v[94:97], v[152:155], v[210:213], v[94:97]
	v_mfma_f32_16x16x32_bf16 v[90:93], v[170:173], v[210:213], v[90:93]
	v_mfma_f32_16x16x32_bf16 v[78:81], v[152:155], v[218:221], v[78:81]
	v_mfma_f32_16x16x32_bf16 v[74:77], v[170:173], v[218:221], v[74:77]
	v_mfma_f32_16x16x32_bf16 v[126:129], v[166:169], v[198:201], v[126:129]
	v_mfma_f32_16x16x32_bf16 v[122:125], v[174:177], v[198:201], v[122:125]
	v_mfma_f32_16x16x32_bf16 v[110:113], v[166:169], v[206:209], v[110:113]
	v_mfma_f32_16x16x32_bf16 v[106:109], v[174:177], v[206:209], v[106:109]
	v_mfma_f32_16x16x32_bf16 v[94:97], v[166:169], v[214:217], v[94:97]
	v_mfma_f32_16x16x32_bf16 v[90:93], v[174:177], v[214:217], v[90:93]
	v_mfma_f32_16x16x32_bf16 v[78:81], v[166:169], v[222:225], v[78:81]
	v_mfma_f32_16x16x32_bf16 v[74:77], v[174:177], v[222:225], v[74:77]
	s_setprio 0
	s_setprio 1
	v_mfma_f32_16x16x32_bf16 v[118:121], v[178:181], v[194:197], v[118:121]
	v_mfma_f32_16x16x32_bf16 v[114:117], v[186:189], v[194:197], v[114:117]
	v_mfma_f32_16x16x32_bf16 v[102:105], v[178:181], v[202:205], v[102:105]
	v_mfma_f32_16x16x32_bf16 v[98:101], v[186:189], v[202:205], v[98:101]
	v_mfma_f32_16x16x32_bf16 v[86:89], v[178:181], v[210:213], v[86:89]
	v_mfma_f32_16x16x32_bf16 v[82:85], v[186:189], v[210:213], v[82:85]
	v_mfma_f32_16x16x32_bf16 v[70:73], v[178:181], v[218:221], v[70:73]
	v_mfma_f32_16x16x32_bf16 v[66:69], v[186:189], v[218:221], v[66:69]
	v_mfma_f32_16x16x32_bf16 v[118:121], v[182:185], v[198:201], v[118:121]
	v_mfma_f32_16x16x32_bf16 v[114:117], v[190:193], v[198:201], v[114:117]
	v_mfma_f32_16x16x32_bf16 v[102:105], v[182:185], v[206:209], v[102:105]
	v_mfma_f32_16x16x32_bf16 v[98:101], v[190:193], v[206:209], v[98:101]
	v_mfma_f32_16x16x32_bf16 v[86:89], v[182:185], v[214:217], v[86:89]
	v_mfma_f32_16x16x32_bf16 v[82:85], v[190:193], v[214:217], v[82:85]
	v_mfma_f32_16x16x32_bf16 v[70:73], v[182:185], v[222:225], v[70:73]
	v_mfma_f32_16x16x32_bf16 v[66:69], v[190:193], v[222:225], v[66:69]
	s_setprio 0
	s_barrier
	s_add_i32 s2, s61, s48
	v_lshl_add_u64 v[226:227], s[40:41], 0, v[132:133]
	s_mov_b32 m0, s2
	s_nop 0
	global_load_lds_dwordx4 v[226:227], off
	s_add_i32 m0, s2, 0x2000
	s_add_u32 s2, s40, 0x80000
	v_lshl_add_u64 v[228:229], s[40:41], 0, v[134:135]
	s_addc_u32 s3, s41, 0
	s_add_i32 s10, s62, s48
	global_load_lds_dwordx4 v[228:229], off
	v_lshl_add_u64 v[230:231], s[2:3], 0, v[132:133]
	s_mov_b32 m0, s10
	v_cndmask_b32_e32 v130, v148, v164, vcc
	global_load_lds_dwordx4 v[230:231], off
	s_add_i32 m0, s10, 0x2000
	v_lshl_add_u64 v[230:231], s[2:3], 0, v[134:135]
	s_add_u32 s2, s16, s67
	global_load_lds_dwordx4 v[230:231], off
	s_addc_u32 s3, s17, 0
	s_mov_b32 m0, s49
	v_lshl_add_u64 v[230:231], s[2:3], 0, v[130:131]
	global_load_lds_dwordx4 v130, s[2:3]
	v_cndmask_b32_e32 v130, v140, v163, vcc
	s_mov_b32 m0, s50
	v_lshl_add_u64 v[232:233], s[2:3], 0, v[130:131]
	global_load_lds_dwordx4 v130, s[2:3]
	ds_read_b128 v[194:197], v160 offset:16384
	ds_read_b128 v[198:201], v160 offset:17408
	ds_read_b128 v[202:205], v160 offset:18432
	ds_read_b128 v[206:209], v160 offset:19456
	ds_read_b128 v[210:213], v160 offset:20480
	ds_read_b128 v[214:217], v160 offset:21504
	ds_read_b128 v[218:221], v160 offset:22528
	ds_read_b128 v[222:225], v160 offset:23552
	s_waitcnt vmcnt(8)
	s_waitcnt lgkmcnt(0)
	s_barrier
	s_setprio 1
	s_waitcnt lgkmcnt(0)
	v_mfma_f32_16x16x32_bf16 v[62:65], v[152:155], v[194:197], v[62:65]
	v_mfma_f32_16x16x32_bf16 v[58:61], v[170:173], v[194:197], v[58:61]
	v_mfma_f32_16x16x32_bf16 v[46:49], v[152:155], v[202:205], v[46:49]
	v_mfma_f32_16x16x32_bf16 v[42:45], v[170:173], v[202:205], v[42:45]
	v_mfma_f32_16x16x32_bf16 v[30:33], v[152:155], v[210:213], v[30:33]
	v_mfma_f32_16x16x32_bf16 v[26:29], v[170:173], v[210:213], v[26:29]
	v_mfma_f32_16x16x32_bf16 v[14:17], v[152:155], v[218:221], v[14:17]
	v_mfma_f32_16x16x32_bf16 v[10:13], v[170:173], v[218:221], v[10:13]
	v_mfma_f32_16x16x32_bf16 v[62:65], v[166:169], v[198:201], v[62:65]
	v_mfma_f32_16x16x32_bf16 v[58:61], v[174:177], v[198:201], v[58:61]
	v_mfma_f32_16x16x32_bf16 v[46:49], v[166:169], v[206:209], v[46:49]
	v_mfma_f32_16x16x32_bf16 v[42:45], v[174:177], v[206:209], v[42:45]
	v_mfma_f32_16x16x32_bf16 v[30:33], v[166:169], v[214:217], v[30:33]
	v_mfma_f32_16x16x32_bf16 v[26:29], v[174:177], v[214:217], v[26:29]
	v_mfma_f32_16x16x32_bf16 v[14:17], v[166:169], v[222:225], v[14:17]
	v_mfma_f32_16x16x32_bf16 v[10:13], v[174:177], v[222:225], v[10:13]
	s_setprio 0
	s_setprio 1
	v_mfma_f32_16x16x32_bf16 v[54:57], v[178:181], v[194:197], v[54:57]
	v_mfma_f32_16x16x32_bf16 v[50:53], v[186:189], v[194:197], v[50:53]
	v_mfma_f32_16x16x32_bf16 v[38:41], v[178:181], v[202:205], v[38:41]
	v_mfma_f32_16x16x32_bf16 v[34:37], v[186:189], v[202:205], v[34:37]
	v_mfma_f32_16x16x32_bf16 v[22:25], v[178:181], v[210:213], v[22:25]
	v_mfma_f32_16x16x32_bf16 v[18:21], v[186:189], v[210:213], v[18:21]
	v_mfma_f32_16x16x32_bf16 v[6:9], v[178:181], v[218:221], v[6:9]
	v_mfma_f32_16x16x32_bf16 v[2:5], v[186:189], v[218:221], v[2:5]
	v_mfma_f32_16x16x32_bf16 v[54:57], v[182:185], v[198:201], v[54:57]
	v_mfma_f32_16x16x32_bf16 v[50:53], v[190:193], v[198:201], v[50:53]
	v_mfma_f32_16x16x32_bf16 v[38:41], v[182:185], v[206:209], v[38:41]
	v_mfma_f32_16x16x32_bf16 v[34:37], v[190:193], v[206:209], v[34:37]
	v_mfma_f32_16x16x32_bf16 v[22:25], v[182:185], v[214:217], v[22:25]
	v_mfma_f32_16x16x32_bf16 v[18:21], v[190:193], v[214:217], v[18:21]
	v_mfma_f32_16x16x32_bf16 v[6:9], v[182:185], v[222:225], v[6:9]
	v_mfma_f32_16x16x32_bf16 v[2:5], v[190:193], v[222:225], v[2:5]
	s_setprio 0
	s_barrier
	s_add_i32 s10, 0, 0x18000
	v_add_u32_e32 v130, s10, v156
	s_add_i32 s11, 0, 0x1c000
	ds_read_b128 v[152:155], v130
	ds_read_b128 v[166:169], v130 offset:1024
	ds_read_b128 v[170:173], v130 offset:2048
	ds_read_b128 v[174:177], v130 offset:3072
	v_add_u32_e32 v130, s11, v156
	ds_read_b128 v[178:181], v130
	ds_read_b128 v[182:185], v130 offset:1024
	ds_read_b128 v[186:189], v130 offset:2048
	ds_read_b128 v[190:193], v130 offset:3072
	s_mov_b32 m0, s51
	v_cndmask_b32_e32 v130, v138, v161, vcc
	ds_read_b128 v[194:197], v160 offset:32768
	ds_read_b128 v[198:201], v160 offset:33792
	ds_read_b128 v[202:205], v160 offset:34816
	ds_read_b128 v[206:209], v160 offset:35840
	ds_read_b128 v[210:213], v160 offset:36864
	ds_read_b128 v[214:217], v160 offset:37888
	ds_read_b128 v[218:221], v160 offset:38912
	ds_read_b128 v[222:225], v160 offset:39936
	global_load_lds_dwordx4 v130, s[2:3]
	v_cndmask_b32_e32 v130, v142, v162, vcc
	s_mov_b32 m0, s52
	s_nop 0
	global_load_lds_dwordx4 v130, s[2:3]
	s_waitcnt vmcnt(8)
	s_waitcnt lgkmcnt(0)
	s_barrier
	s_setprio 1
	s_waitcnt lgkmcnt(0)
	v_mfma_f32_16x16x32_bf16 v[126:129], v[152:155], v[194:197], v[126:129]
	v_mfma_f32_16x16x32_bf16 v[122:125], v[170:173], v[194:197], v[122:125]
	v_mfma_f32_16x16x32_bf16 v[110:113], v[152:155], v[202:205], v[110:113]
	v_mfma_f32_16x16x32_bf16 v[106:109], v[170:173], v[202:205], v[106:109]
	v_mfma_f32_16x16x32_bf16 v[94:97], v[152:155], v[210:213], v[94:97]
	v_mfma_f32_16x16x32_bf16 v[90:93], v[170:173], v[210:213], v[90:93]
	v_mfma_f32_16x16x32_bf16 v[78:81], v[152:155], v[218:221], v[78:81]
	v_mfma_f32_16x16x32_bf16 v[74:77], v[170:173], v[218:221], v[74:77]
	v_mfma_f32_16x16x32_bf16 v[126:129], v[166:169], v[198:201], v[126:129]
	v_mfma_f32_16x16x32_bf16 v[122:125], v[174:177], v[198:201], v[122:125]
	v_mfma_f32_16x16x32_bf16 v[110:113], v[166:169], v[206:209], v[110:113]
	v_mfma_f32_16x16x32_bf16 v[106:109], v[174:177], v[206:209], v[106:109]
	v_mfma_f32_16x16x32_bf16 v[94:97], v[166:169], v[214:217], v[94:97]
	v_mfma_f32_16x16x32_bf16 v[90:93], v[174:177], v[214:217], v[90:93]
	v_mfma_f32_16x16x32_bf16 v[78:81], v[166:169], v[222:225], v[78:81]
	v_mfma_f32_16x16x32_bf16 v[74:77], v[174:177], v[222:225], v[74:77]
	s_setprio 0
	s_setprio 1
	v_mfma_f32_16x16x32_bf16 v[118:121], v[178:181], v[194:197], v[118:121]
	v_mfma_f32_16x16x32_bf16 v[114:117], v[186:189], v[194:197], v[114:117]
	v_mfma_f32_16x16x32_bf16 v[102:105], v[178:181], v[202:205], v[102:105]
	v_mfma_f32_16x16x32_bf16 v[98:101], v[186:189], v[202:205], v[98:101]
	v_mfma_f32_16x16x32_bf16 v[86:89], v[178:181], v[210:213], v[86:89]
	v_mfma_f32_16x16x32_bf16 v[82:85], v[186:189], v[210:213], v[82:85]
	v_mfma_f32_16x16x32_bf16 v[70:73], v[178:181], v[218:221], v[70:73]
	v_mfma_f32_16x16x32_bf16 v[66:69], v[186:189], v[218:221], v[66:69]
	v_mfma_f32_16x16x32_bf16 v[118:121], v[182:185], v[198:201], v[118:121]
	v_mfma_f32_16x16x32_bf16 v[114:117], v[190:193], v[198:201], v[114:117]
	v_mfma_f32_16x16x32_bf16 v[102:105], v[182:185], v[206:209], v[102:105]
	v_mfma_f32_16x16x32_bf16 v[98:101], v[190:193], v[206:209], v[98:101]
	v_mfma_f32_16x16x32_bf16 v[86:89], v[182:185], v[214:217], v[86:89]
	v_mfma_f32_16x16x32_bf16 v[82:85], v[190:193], v[214:217], v[82:85]
	v_mfma_f32_16x16x32_bf16 v[70:73], v[182:185], v[222:225], v[70:73]
	v_mfma_f32_16x16x32_bf16 v[66:69], v[190:193], v[222:225], v[66:69]
	s_setprio 0
	s_barrier
	s_add_i32 s2, s10, s48
	v_lshl_add_u64 v[226:227], v[226:227], 0, s[20:21]
	s_mov_b32 m0, s2
	s_nop 0
	global_load_lds_dwordx4 v[226:227], off
	s_add_i32 m0, s2, 0x2000
	s_add_u32 s2, s40, 0x80080
	v_lshl_add_u64 v[226:227], v[228:229], 0, s[20:21]
	s_addc_u32 s3, s41, 0
	s_add_i32 s10, s11, s48
	global_load_lds_dwordx4 v[226:227], off
	v_lshl_add_u64 v[226:227], s[2:3], 0, v[132:133]
	s_mov_b32 m0, s10
	s_nop 0
	global_load_lds_dwordx4 v[226:227], off
	v_lshl_add_u64 v[226:227], s[2:3], 0, v[134:135]
	s_add_i32 m0, s10, 0x2000
	s_nop 0
	global_load_lds_dwordx4 v[226:227], off
	v_lshl_add_u64 v[226:227], v[230:231], 0, s[20:21]
	s_mov_b32 m0, s58
	s_nop 0
	global_load_lds_dwordx4 v[226:227], off
	v_lshl_add_u64 v[226:227], v[232:233], 0, s[20:21]
	s_mov_b32 m0, s59
	s_nop 0
	global_load_lds_dwordx4 v[226:227], off
	ds_read_b128 v[194:197], v160 offset:49152
	ds_read_b128 v[198:201], v160 offset:50176
	ds_read_b128 v[202:205], v160 offset:51200
	ds_read_b128 v[206:209], v160 offset:52224
	ds_read_b128 v[210:213], v160 offset:53248
	ds_read_b128 v[214:217], v160 offset:54272
	ds_read_b128 v[218:221], v160 offset:55296
	ds_read_b128 v[222:225], v160 offset:56320
	s_waitcnt vmcnt(8)
	s_waitcnt lgkmcnt(0)
	s_barrier
	s_setprio 1
	s_waitcnt lgkmcnt(0)
	v_mfma_f32_16x16x32_bf16 v[62:65], v[152:155], v[194:197], v[62:65]
	v_mfma_f32_16x16x32_bf16 v[58:61], v[170:173], v[194:197], v[58:61]
	v_mfma_f32_16x16x32_bf16 v[46:49], v[152:155], v[202:205], v[46:49]
	v_mfma_f32_16x16x32_bf16 v[42:45], v[170:173], v[202:205], v[42:45]
	v_mfma_f32_16x16x32_bf16 v[30:33], v[152:155], v[210:213], v[30:33]
	v_mfma_f32_16x16x32_bf16 v[26:29], v[170:173], v[210:213], v[26:29]
	v_mfma_f32_16x16x32_bf16 v[14:17], v[152:155], v[218:221], v[14:17]
	v_mfma_f32_16x16x32_bf16 v[10:13], v[170:173], v[218:221], v[10:13]
	v_mfma_f32_16x16x32_bf16 v[62:65], v[166:169], v[198:201], v[62:65]
	v_mfma_f32_16x16x32_bf16 v[58:61], v[174:177], v[198:201], v[58:61]
	v_mfma_f32_16x16x32_bf16 v[46:49], v[166:169], v[206:209], v[46:49]
	v_mfma_f32_16x16x32_bf16 v[42:45], v[174:177], v[206:209], v[42:45]
	v_mfma_f32_16x16x32_bf16 v[30:33], v[166:169], v[214:217], v[30:33]
	v_mfma_f32_16x16x32_bf16 v[26:29], v[174:177], v[214:217], v[26:29]
	v_mfma_f32_16x16x32_bf16 v[14:17], v[166:169], v[222:225], v[14:17]
	v_mfma_f32_16x16x32_bf16 v[10:13], v[174:177], v[222:225], v[10:13]
	s_setprio 0
	s_setprio 1
	v_mfma_f32_16x16x32_bf16 v[54:57], v[178:181], v[194:197], v[54:57]
	v_mfma_f32_16x16x32_bf16 v[50:53], v[186:189], v[194:197], v[50:53]
	v_mfma_f32_16x16x32_bf16 v[38:41], v[178:181], v[202:205], v[38:41]
	v_mfma_f32_16x16x32_bf16 v[34:37], v[186:189], v[202:205], v[34:37]
	v_mfma_f32_16x16x32_bf16 v[22:25], v[178:181], v[210:213], v[22:25]
	v_mfma_f32_16x16x32_bf16 v[18:21], v[186:189], v[210:213], v[18:21]
	v_mfma_f32_16x16x32_bf16 v[6:9], v[178:181], v[218:221], v[6:9]
	v_mfma_f32_16x16x32_bf16 v[2:5], v[186:189], v[218:221], v[2:5]
	v_mfma_f32_16x16x32_bf16 v[54:57], v[182:185], v[198:201], v[54:57]
	v_mfma_f32_16x16x32_bf16 v[50:53], v[190:193], v[198:201], v[50:53]
	v_mfma_f32_16x16x32_bf16 v[38:41], v[182:185], v[206:209], v[38:41]
	v_mfma_f32_16x16x32_bf16 v[34:37], v[190:193], v[206:209], v[34:37]
	v_mfma_f32_16x16x32_bf16 v[22:25], v[182:185], v[214:217], v[22:25]
	v_mfma_f32_16x16x32_bf16 v[18:21], v[190:193], v[214:217], v[18:21]
	v_mfma_f32_16x16x32_bf16 v[6:9], v[182:185], v[222:225], v[6:9]
	v_mfma_f32_16x16x32_bf16 v[2:5], v[190:193], v[222:225], v[2:5]
	s_setprio 0
	s_barrier
	s_add_i32 s66, s66, 2
	s_cmp_gt_u32 s66, 29
	s_mov_b64 s[10:11], s[38:39]
	s_cbranch_scc0 .LBB0_1005
	s_and_b64 vcc, exec, s[24:25]
	s_cbranch_vccz .LBB0_1008
	s_barrier

.LBB0_1122:
	s_lshl_b32 s2, s87, 7
	v_add_u32_e32 v142, s80, v205
	v_add_u32_e32 v158, s81, v205
	s_add_u32 s64, s38, s2
	ds_read_b128 v[130:133], v142
	ds_read_b128 v[134:137], v142 offset:1024
	ds_read_b128 v[138:141], v142 offset:2048
	ds_read_b128 v[142:145], v142 offset:3072
	ds_read_b128 v[146:149], v158
	ds_read_b128 v[150:153], v158 offset:1024
	ds_read_b128 v[154:157], v158 offset:2048
	ds_read_b128 v[158:161], v158 offset:3072
	s_addc_u32 s65, s39, 0
	s_add_u32 s66, s64, 0x100
	s_addc_u32 s67, s65, 0
	s_and_b64 s[64:65], s[60:61], exec
	s_cselect_b32 s65, s35, s67
	s_cselect_b32 s64, s83, s66
	s_add_i32 s68, s2, 0x100
	s_and_b64 s[66:67], s[60:61], exec
	s_cselect_b32 s68, 0, s68
	s_add_u32 s2, s36, s2
	s_addc_u32 s67, s37, 0
	s_add_u32 s66, s2, 0x20080
	s_addc_u32 s67, s67, 0
	v_lshl_add_u64 v[210:211], s[66:67], 0, v[194:195]
	s_add_i32 m0, s50, 0xc000
	ds_read_b128 v[162:165], v209
	ds_read_b128 v[166:169], v209 offset:1024
	ds_read_b128 v[170:173], v209 offset:2048
	ds_read_b128 v[174:177], v209 offset:3072
	ds_read_b128 v[178:181], v209 offset:4096
	ds_read_b128 v[182:185], v209 offset:5120
	ds_read_b128 v[186:189], v209 offset:6144
	ds_read_b128 v[190:193], v209 offset:7168
	global_load_lds_dwordx4 v[210:211], off
	v_lshl_add_u64 v[210:211], s[66:67], 0, v[198:199]
	s_add_i32 m0, s50, 0xe000
	s_nop 0
	global_load_lds_dwordx4 v[210:211], off
	s_waitcnt vmcnt(8)
	s_waitcnt lgkmcnt(0)
	s_barrier
	s_setprio 1
	s_waitcnt lgkmcnt(0)
	v_mfma_f32_16x16x32_bf16 v[86:89], v[130:133], v[162:165], v[86:89]
	v_mfma_f32_16x16x32_bf16 v[82:85], v[138:141], v[162:165], v[82:85]
	v_mfma_f32_16x16x32_bf16 v[78:81], v[130:133], v[170:173], v[78:81]
	v_mfma_f32_16x16x32_bf16 v[74:77], v[138:141], v[170:173], v[74:77]
	v_mfma_f32_16x16x32_bf16 v[70:73], v[130:133], v[178:181], v[70:73]
	v_mfma_f32_16x16x32_bf16 v[66:69], v[138:141], v[178:181], v[66:69]
	v_mfma_f32_16x16x32_bf16 v[62:65], v[130:133], v[186:189], v[62:65]
	v_mfma_f32_16x16x32_bf16 v[58:61], v[138:141], v[186:189], v[58:61]
	v_mfma_f32_16x16x32_bf16 v[86:89], v[134:137], v[166:169], v[86:89]
	v_mfma_f32_16x16x32_bf16 v[82:85], v[142:145], v[166:169], v[82:85]
	v_mfma_f32_16x16x32_bf16 v[78:81], v[134:137], v[174:177], v[78:81]
	v_mfma_f32_16x16x32_bf16 v[74:77], v[142:145], v[174:177], v[74:77]
	v_mfma_f32_16x16x32_bf16 v[70:73], v[134:137], v[182:185], v[70:73]
	v_mfma_f32_16x16x32_bf16 v[66:69], v[142:145], v[182:185], v[66:69]
	v_mfma_f32_16x16x32_bf16 v[62:65], v[134:137], v[190:193], v[62:65]
	v_mfma_f32_16x16x32_bf16 v[58:61], v[142:145], v[190:193], v[58:61]
	s_setprio 0
	s_setprio 1
	v_mfma_f32_16x16x32_bf16 v[54:57], v[146:149], v[162:165], v[54:57]
	v_mfma_f32_16x16x32_bf16 v[50:53], v[154:157], v[162:165], v[50:53]
	v_mfma_f32_16x16x32_bf16 v[46:49], v[146:149], v[170:173], v[46:49]
	v_mfma_f32_16x16x32_bf16 v[42:45], v[154:157], v[170:173], v[42:45]
	v_mfma_f32_16x16x32_bf16 v[34:37], v[146:149], v[178:181], v[34:37]
	v_mfma_f32_16x16x32_bf16 v[26:29], v[154:157], v[178:181], v[26:29]
	v_mfma_f32_16x16x32_bf16 v[18:21], v[146:149], v[186:189], v[18:21]
	v_mfma_f32_16x16x32_bf16 v[10:13], v[154:157], v[186:189], v[10:13]
	v_mfma_f32_16x16x32_bf16 v[54:57], v[150:153], v[166:169], v[54:57]
	v_mfma_f32_16x16x32_bf16 v[50:53], v[158:161], v[166:169], v[50:53]
	v_mfma_f32_16x16x32_bf16 v[46:49], v[150:153], v[174:177], v[46:49]
	v_mfma_f32_16x16x32_bf16 v[42:45], v[158:161], v[174:177], v[42:45]
	v_mfma_f32_16x16x32_bf16 v[34:37], v[150:153], v[182:185], v[34:37]
	v_mfma_f32_16x16x32_bf16 v[26:29], v[158:161], v[182:185], v[26:29]
	v_mfma_f32_16x16x32_bf16 v[18:21], v[150:153], v[190:193], v[18:21]
	v_mfma_f32_16x16x32_bf16 v[10:13], v[158:161], v[190:193], v[10:13]
	s_setprio 0
	s_barrier
	s_add_i32 s2, s80, s49
	v_lshl_add_u64 v[210:211], s[64:65], 0, v[196:197]
	s_mov_b32 m0, s2
	s_nop 0
	global_load_lds_dwordx4 v[210:211], off
	s_add_i32 m0, s2, 0x2000
	s_add_u32 s66, s64, 0x20000
	v_lshl_add_u64 v[212:213], s[64:65], 0, v[200:201]
	s_addc_u32 s67, s65, 0
	s_add_i32 s2, s81, s49
	global_load_lds_dwordx4 v[212:213], off
	v_lshl_add_u64 v[214:215], s[66:67], 0, v[196:197]
	s_mov_b32 m0, s2
	s_nop 0
	global_load_lds_dwordx4 v[214:215], off
	s_add_i32 m0, s2, 0x2000
	s_add_u32 s62, s62, s68
	v_lshl_add_u64 v[214:215], s[66:67], 0, v[200:201]
	s_addc_u32 s63, s63, 0
	global_load_lds_dwordx4 v[214:215], off
	v_lshl_add_u64 v[214:215], s[62:63], 0, v[194:195]
	s_mov_b32 m0, s50
	v_lshl_add_u64 v[216:217], s[62:63], 0, v[198:199]
	global_load_lds_dwordx4 v[214:215], off
	s_mov_b32 m0, s51
	s_nop 0
	global_load_lds_dwordx4 v[216:217], off
	ds_read_b128 v[162:165], v209 offset:16384
	ds_read_b128 v[166:169], v209 offset:17408
	ds_read_b128 v[170:173], v209 offset:18432
	ds_read_b128 v[174:177], v209 offset:19456
	ds_read_b128 v[178:181], v209 offset:20480
	ds_read_b128 v[182:185], v209 offset:21504
	ds_read_b128 v[186:189], v209 offset:22528
	ds_read_b128 v[190:193], v209 offset:23552
	s_waitcnt vmcnt(8)
	s_waitcnt lgkmcnt(0)
	s_barrier
	s_setprio 1
	s_waitcnt lgkmcnt(0)
	v_mfma_f32_16x16x32_bf16 v[126:129], v[130:133], v[162:165], v[126:129]
	v_mfma_f32_16x16x32_bf16 v[122:125], v[138:141], v[162:165], v[122:125]
	v_mfma_f32_16x16x32_bf16 v[110:113], v[130:133], v[170:173], v[110:113]
	v_mfma_f32_16x16x32_bf16 v[106:109], v[138:141], v[170:173], v[106:109]
	v_mfma_f32_16x16x32_bf16 v[94:97], v[130:133], v[178:181], v[94:97]
	v_mfma_f32_16x16x32_bf16 v[90:93], v[138:141], v[178:181], v[90:93]
	v_mfma_f32_16x16x32_bf16 v[22:25], v[130:133], v[186:189], v[22:25]
	v_mfma_f32_16x16x32_bf16 v[14:17], v[138:141], v[186:189], v[14:17]
	v_mfma_f32_16x16x32_bf16 v[126:129], v[134:137], v[166:169], v[126:129]
	v_mfma_f32_16x16x32_bf16 v[122:125], v[142:145], v[166:169], v[122:125]
	v_mfma_f32_16x16x32_bf16 v[110:113], v[134:137], v[174:177], v[110:113]
	v_mfma_f32_16x16x32_bf16 v[106:109], v[142:145], v[174:177], v[106:109]
	v_mfma_f32_16x16x32_bf16 v[94:97], v[134:137], v[182:185], v[94:97]
	v_mfma_f32_16x16x32_bf16 v[90:93], v[142:145], v[182:185], v[90:93]
	v_mfma_f32_16x16x32_bf16 v[22:25], v[134:137], v[190:193], v[22:25]
	v_mfma_f32_16x16x32_bf16 v[14:17], v[142:145], v[190:193], v[14:17]
	s_setprio 0
	s_setprio 1
	v_mfma_f32_16x16x32_bf16 v[118:121], v[146:149], v[162:165], v[118:121]
	v_mfma_f32_16x16x32_bf16 v[114:117], v[154:157], v[162:165], v[114:117]
	v_mfma_f32_16x16x32_bf16 v[102:105], v[146:149], v[170:173], v[102:105]
	v_mfma_f32_16x16x32_bf16 v[98:101], v[154:157], v[170:173], v[98:101]
	v_mfma_f32_16x16x32_bf16 v[38:41], v[146:149], v[178:181], v[38:41]
	v_mfma_f32_16x16x32_bf16 v[30:33], v[154:157], v[178:181], v[30:33]
	v_mfma_f32_16x16x32_bf16 v[6:9], v[146:149], v[186:189], v[6:9]
	v_mfma_f32_16x16x32_bf16 v[2:5], v[154:157], v[186:189], v[2:5]
	v_mfma_f32_16x16x32_bf16 v[118:121], v[150:153], v[166:169], v[118:121]
	v_mfma_f32_16x16x32_bf16 v[114:117], v[158:161], v[166:169], v[114:117]
	v_mfma_f32_16x16x32_bf16 v[102:105], v[150:153], v[174:177], v[102:105]
	v_mfma_f32_16x16x32_bf16 v[98:101], v[158:161], v[174:177], v[98:101]
	v_mfma_f32_16x16x32_bf16 v[38:41], v[150:153], v[182:185], v[38:41]
	v_mfma_f32_16x16x32_bf16 v[30:33], v[158:161], v[182:185], v[30:33]
	v_mfma_f32_16x16x32_bf16 v[6:9], v[150:153], v[190:193], v[6:9]
	v_mfma_f32_16x16x32_bf16 v[2:5], v[158:161], v[190:193], v[2:5]
	s_setprio 0
	s_barrier
	s_add_u32 s62, s62, 0x20000
	s_addc_u32 s63, s63, 0
	s_mov_b32 m0, s52
	v_lshl_add_u64 v[218:219], s[62:63], 0, v[194:195]
	global_load_lds_dwordx4 v[218:219], off
	v_lshl_add_u64 v[218:219], s[62:63], 0, v[198:199]
	s_mov_b32 m0, s53
	s_nop 0
	global_load_lds_dwordx4 v[218:219], off
	s_add_i32 s2, 0, 0x18000
	s_add_i32 s66, 0, 0x1c000
	v_add_u32_e32 v130, s2, v205
	v_add_u32_e32 v142, s66, v205
	ds_read_b128 v[146:149], v130
	ds_read_b128 v[150:153], v130 offset:1024
	ds_read_b128 v[154:157], v130 offset:2048
	ds_read_b128 v[158:161], v130 offset:3072
	ds_read_b128 v[130:133], v142
	ds_read_b128 v[134:137], v142 offset:1024
	ds_read_b128 v[138:141], v142 offset:2048
	ds_read_b128 v[142:145], v142 offset:3072
	ds_read_b128 v[162:165], v209 offset:32768
	ds_read_b128 v[166:169], v209 offset:33792
	ds_read_b128 v[170:173], v209 offset:34816
	ds_read_b128 v[174:177], v209 offset:35840
	ds_read_b128 v[178:181], v209 offset:36864
	ds_read_b128 v[182:185], v209 offset:37888
	ds_read_b128 v[186:189], v209 offset:38912
	ds_read_b128 v[190:193], v209 offset:39936
	s_waitcnt vmcnt(8)
	s_waitcnt lgkmcnt(0)
	s_barrier
	s_setprio 1
	s_waitcnt lgkmcnt(0)
	v_mfma_f32_16x16x32_bf16 v[86:89], v[146:149], v[162:165], v[86:89]
	v_mfma_f32_16x16x32_bf16 v[82:85], v[154:157], v[162:165], v[82:85]
	v_mfma_f32_16x16x32_bf16 v[78:81], v[146:149], v[170:173], v[78:81]
	v_mfma_f32_16x16x32_bf16 v[74:77], v[154:157], v[170:173], v[74:77]
	v_mfma_f32_16x16x32_bf16 v[70:73], v[146:149], v[178:181], v[70:73]
	v_mfma_f32_16x16x32_bf16 v[66:69], v[154:157], v[178:181], v[66:69]
	v_mfma_f32_16x16x32_bf16 v[62:65], v[146:149], v[186:189], v[62:65]
	v_mfma_f32_16x16x32_bf16 v[58:61], v[154:157], v[186:189], v[58:61]
	v_mfma_f32_16x16x32_bf16 v[86:89], v[150:153], v[166:169], v[86:89]
	v_mfma_f32_16x16x32_bf16 v[82:85], v[158:161], v[166:169], v[82:85]
	v_mfma_f32_16x16x32_bf16 v[78:81], v[150:153], v[174:177], v[78:81]
	v_mfma_f32_16x16x32_bf16 v[74:77], v[158:161], v[174:177], v[74:77]
	v_mfma_f32_16x16x32_bf16 v[70:73], v[150:153], v[182:185], v[70:73]
	v_mfma_f32_16x16x32_bf16 v[66:69], v[158:161], v[182:185], v[66:69]
	v_mfma_f32_16x16x32_bf16 v[62:65], v[150:153], v[190:193], v[62:65]
	v_mfma_f32_16x16x32_bf16 v[58:61], v[158:161], v[190:193], v[58:61]
	s_setprio 0
	s_setprio 1
	v_mfma_f32_16x16x32_bf16 v[54:57], v[130:133], v[162:165], v[54:57]
	v_mfma_f32_16x16x32_bf16 v[50:53], v[138:141], v[162:165], v[50:53]
	v_mfma_f32_16x16x32_bf16 v[46:49], v[130:133], v[170:173], v[46:49]
	v_mfma_f32_16x16x32_bf16 v[42:45], v[138:141], v[170:173], v[42:45]
	v_mfma_f32_16x16x32_bf16 v[34:37], v[130:133], v[178:181], v[34:37]
	v_mfma_f32_16x16x32_bf16 v[26:29], v[138:141], v[178:181], v[26:29]
	v_mfma_f32_16x16x32_bf16 v[18:21], v[130:133], v[186:189], v[18:21]
	v_mfma_f32_16x16x32_bf16 v[10:13], v[138:141], v[186:189], v[10:13]
	v_mfma_f32_16x16x32_bf16 v[54:57], v[134:137], v[166:169], v[54:57]
	v_mfma_f32_16x16x32_bf16 v[50:53], v[142:145], v[166:169], v[50:53]
	v_mfma_f32_16x16x32_bf16 v[46:49], v[134:137], v[174:177], v[46:49]
	v_mfma_f32_16x16x32_bf16 v[42:45], v[142:145], v[174:177], v[42:45]
	v_mfma_f32_16x16x32_bf16 v[34:37], v[134:137], v[182:185], v[34:37]
	v_mfma_f32_16x16x32_bf16 v[26:29], v[142:145], v[182:185], v[26:29]
	v_mfma_f32_16x16x32_bf16 v[18:21], v[134:137], v[190:193], v[18:21]
	v_mfma_f32_16x16x32_bf16 v[10:13], v[142:145], v[190:193], v[10:13]
	s_setprio 0
	s_barrier
	s_add_i32 s2, s2, s49
	v_lshl_add_u64 v[210:211], v[210:211], 0, s[12:13]
	s_mov_b32 m0, s2
	s_nop 0
	global_load_lds_dwordx4 v[210:211], off
	s_add_i32 m0, s2, 0x2000
	s_add_u32 s62, s64, 0x20080
	v_lshl_add_u64 v[210:211], v[212:213], 0, s[12:13]
	s_addc_u32 s63, s65, 0
	s_add_i32 s2, s66, s49
	global_load_lds_dwordx4 v[210:211], off
	v_lshl_add_u64 v[210:211], s[62:63], 0, v[196:197]
	s_mov_b32 m0, s2
	s_andn2_b64 vcc, exec, s[60:61]
	global_load_lds_dwordx4 v[210:211], off
	v_lshl_add_u64 v[210:211], s[62:63], 0, v[200:201]
	s_add_i32 m0, s2, 0x2000
	s_nop 0
	global_load_lds_dwordx4 v[210:211], off
	v_lshl_add_u64 v[210:211], v[214:215], 0, s[12:13]
	s_mov_b32 m0, s73
	s_nop 0
	global_load_lds_dwordx4 v[210:211], off
	v_lshl_add_u64 v[210:211], v[216:217], 0, s[12:13]
	s_mov_b32 m0, s74
	s_nop 0
	global_load_lds_dwordx4 v[210:211], off
	ds_read_b128 v[186:189], v209 offset:49152
	ds_read_b128 v[190:193], v209 offset:50176
	ds_read_b128 v[178:181], v209 offset:51200
	ds_read_b128 v[182:185], v209 offset:52224
	ds_read_b128 v[170:173], v209 offset:53248
	ds_read_b128 v[174:177], v209 offset:54272
	ds_read_b128 v[162:165], v209 offset:55296
	ds_read_b128 v[166:169], v209 offset:56320
	s_waitcnt vmcnt(8)
	s_waitcnt lgkmcnt(0)
	s_barrier
	s_cbranch_vccnz .LBB0_1104
	v_pk_mul_f32 v[214:215], v[86:87], s[20:21] op_sel_hi:[1,0]
	v_pk_mul_f32 v[216:217], v[82:83], s[20:21] op_sel_hi:[1,0]
	v_mov_b32_e32 v218, 0
	v_mov_b32_e32 v219, 0
	v_cvt_pk_fp8_f32 v218, v214, v215
	v_cvt_pk_fp8_f32 v219, v216, v217
	v_pk_mul_f32 v[214:215], v[88:89], s[20:21] op_sel_hi:[1,0]
	v_pk_mul_f32 v[216:217], v[84:85], s[20:21] op_sel_hi:[1,0]
	v_cvt_pk_fp8_f32 v218, v214, v215 op_sel:[0,0,1]
	v_cvt_pk_fp8_f32 v219, v216, v217 op_sel:[0,0,1]
	v_pk_mul_f32 v[214:215], v[54:55], s[20:21] op_sel_hi:[1,0]
	v_pk_mul_f32 v[216:217], v[50:51], s[20:21] op_sel_hi:[1,0]
	v_mov_b32_e32 v220, 0
	v_mov_b32_e32 v221, 0
	v_mov_b32_e32 v210, v1
	v_mov_b32_e32 v211, v204
	v_cvt_pk_fp8_f32 v220, v214, v215
	v_cvt_pk_fp8_f32 v221, v216, v217
	v_pk_mul_f32 v[214:215], v[56:57], s[20:21] op_sel_hi:[1,0]
	v_add_u32_e32 v210, s85, v210
	v_lshl_add_u32 v212, v211, 3, s86
	v_ashrrev_i32_e32 v211, 31, v210
	v_pk_mul_f32 v[216:217], v[52:53], s[20:21] op_sel_hi:[1,0]
	v_lshlrev_b64 v[210:211], 11, v[210:211]
	v_cvt_pk_fp8_f32 v220, v214, v215 op_sel:[0,0,1]
	v_cvt_pk_fp8_f32 v221, v216, v217 op_sel:[0,0,1]
	v_ashrrev_i32_e32 v213, 31, v212
	v_lshl_add_u64 v[210:211], s[10:11], 0, v[210:211]
	v_lshl_add_u64 v[210:211], v[210:211], 0, v[212:213]
	global_store_dwordx2 v[210:211], v[218:219], off
	global_store_dwordx2 v[210:211], v[220:221], off offset:128
	v_pk_mul_f32 v[214:215], v[78:79], s[20:21] op_sel_hi:[1,0]
	v_pk_mul_f32 v[216:217], v[74:75], s[20:21] op_sel_hi:[1,0]
	v_mov_b32_e32 v218, 0
	v_mov_b32_e32 v219, 0
	v_cvt_pk_fp8_f32 v218, v214, v215
	v_cvt_pk_fp8_f32 v219, v216, v217
	v_pk_mul_f32 v[214:215], v[80:81], s[20:21] op_sel_hi:[1,0]
	v_pk_mul_f32 v[216:217], v[76:77], s[20:21] op_sel_hi:[1,0]
	v_cvt_pk_fp8_f32 v218, v214, v215 op_sel:[0,0,1]
	v_cvt_pk_fp8_f32 v219, v216, v217 op_sel:[0,0,1]
	v_pk_mul_f32 v[214:215], v[46:47], s[20:21] op_sel_hi:[1,0]
	v_pk_mul_f32 v[216:217], v[42:43], s[20:21] op_sel_hi:[1,0]
	v_mov_b32_e32 v220, 0
	v_mov_b32_e32 v221, 0
	v_cvt_pk_fp8_f32 v220, v214, v215
	v_cvt_pk_fp8_f32 v221, v216, v217
	v_pk_mul_f32 v[214:215], v[48:49], s[20:21] op_sel_hi:[1,0]
	v_pk_mul_f32 v[216:217], v[44:45], s[20:21] op_sel_hi:[1,0]
	v_cvt_pk_fp8_f32 v220, v214, v215 op_sel:[0,0,1]
	v_cvt_pk_fp8_f32 v221, v216, v217 op_sel:[0,0,1]
	s_mov_b32 s2, 0x8000
	v_add_co_u32_e32 v214, vcc, s2, v210
	s_mov_b64 s[60:61], 0x8000
	s_nop 0
	v_addc_co_u32_e32 v215, vcc, 0, v211, vcc
	v_lshl_add_u64 v[212:213], v[210:211], 0, s[60:61]
	global_store_dwordx2 v[214:215], v[218:219], off
	global_store_dwordx2 v[212:213], v[220:221], off offset:128
	v_pk_mul_f32 v[214:215], v[70:71], s[20:21] op_sel_hi:[1,0]
	v_pk_mul_f32 v[216:217], v[66:67], s[20:21] op_sel_hi:[1,0]
	v_mov_b32_e32 v218, 0
	v_mov_b32_e32 v219, 0
	v_cvt_pk_fp8_f32 v218, v214, v215
	v_cvt_pk_fp8_f32 v219, v216, v217
	v_pk_mul_f32 v[214:215], v[72:73], s[20:21] op_sel_hi:[1,0]
	v_pk_mul_f32 v[216:217], v[68:69], s[20:21] op_sel_hi:[1,0]
	v_cvt_pk_fp8_f32 v218, v214, v215 op_sel:[0,0,1]
	v_cvt_pk_fp8_f32 v219, v216, v217 op_sel:[0,0,1]
	v_pk_mul_f32 v[214:215], v[34:35], s[20:21] op_sel_hi:[1,0]
	v_pk_mul_f32 v[216:217], v[26:27], s[20:21] op_sel_hi:[1,0]
	v_mov_b32_e32 v220, 0
	v_mov_b32_e32 v221, 0
	v_cvt_pk_fp8_f32 v220, v214, v215
	v_cvt_pk_fp8_f32 v221, v216, v217
	v_pk_mul_f32 v[214:215], v[36:37], s[20:21] op_sel_hi:[1,0]
	v_pk_mul_f32 v[216:217], v[28:29], s[20:21] op_sel_hi:[1,0]
	v_cvt_pk_fp8_f32 v220, v214, v215 op_sel:[0,0,1]
	v_cvt_pk_fp8_f32 v221, v216, v217 op_sel:[0,0,1]
	s_mov_b32 s2, 0x10000
	v_add_co_u32_e32 v214, vcc, s2, v210
	v_lshl_add_u64 v[212:213], v[210:211], 0, s[24:25]
	s_nop 0
	v_addc_co_u32_e32 v215, vcc, 0, v211, vcc
	global_store_dwordx2 v[214:215], v[218:219], off
	global_store_dwordx2 v[212:213], v[220:221], off offset:128
	v_pk_mul_f32 v[214:215], v[62:63], s[20:21] op_sel_hi:[1,0]
	v_pk_mul_f32 v[216:217], v[58:59], s[20:21] op_sel_hi:[1,0]
	v_mov_b32_e32 v218, 0
	v_mov_b32_e32 v219, 0
	v_cvt_pk_fp8_f32 v218, v214, v215
	v_cvt_pk_fp8_f32 v219, v216, v217
	v_pk_mul_f32 v[214:215], v[64:65], s[20:21] op_sel_hi:[1,0]
	v_pk_mul_f32 v[216:217], v[60:61], s[20:21] op_sel_hi:[1,0]
	v_cvt_pk_fp8_f32 v218, v214, v215 op_sel:[0,0,1]
	v_cvt_pk_fp8_f32 v219, v216, v217 op_sel:[0,0,1]
	v_pk_mul_f32 v[214:215], v[18:19], s[20:21] op_sel_hi:[1,0]
	v_pk_mul_f32 v[216:217], v[10:11], s[20:21] op_sel_hi:[1,0]
	v_mov_b32_e32 v220, 0
	v_mov_b32_e32 v221, 0
	v_cvt_pk_fp8_f32 v220, v214, v215
	v_cvt_pk_fp8_f32 v221, v216, v217
	v_pk_mul_f32 v[214:215], v[20:21], s[20:21] op_sel_hi:[1,0]
	v_pk_mul_f32 v[216:217], v[12:13], s[20:21] op_sel_hi:[1,0]
	v_cvt_pk_fp8_f32 v220, v214, v215 op_sel:[0,0,1]
	v_cvt_pk_fp8_f32 v221, v216, v217 op_sel:[0,0,1]
	s_mov_b32 s2, 0x18000
	v_lshl_add_u64 v[212:213], v[210:211], 0, s[28:29]
	v_add_co_u32_e32 v210, vcc, s2, v210
	s_nop 1
	v_addc_co_u32_e32 v211, vcc, 0, v211, vcc
	global_store_dwordx2 v[210:211], v[218:219], off
	global_store_dwordx2 v[212:213], v[220:221], off offset:128
	s_branch .LBB0_1104

.LBB0_1294:
	s_mov_b64 s[56:57], s[40:41]
	s_add_u32 s2, s71, s56
	s_addc_u32 s22, s72, s57
	s_add_u32 s40, s56, 0x100
	s_addc_u32 s41, s57, 0
	s_cmp_eq_u32 s73, 28
	s_cselect_b64 s[8:9], -1, 0
	s_and_b64 s[12:13], s[8:9], exec
	s_cselect_b32 s61, s67, s22
	s_cselect_b32 s60, s68, s2
	s_cselect_b32 s2, 0, s40
	s_add_i32 s22, s86, s42
	s_add_i32 m0, s51, 0xc000
	s_add_i32 s13, s51, 0xe000
	s_add_i32 s23, s22, 0x2000
	s_add_u32 s62, s60, 0x80000
	s_addc_u32 s63, s61, 0
	s_add_i32 s24, s87, s42
	s_add_i32 s25, s24, 0x2000
	s_and_b64 s[8:9], s[6:7], s[8:9]
	ds_read_b128 v[130:133], v229
	ds_read_b128 v[134:137], v229 offset:1024
	ds_read_b128 v[138:141], v229 offset:2048
	ds_read_b128 v[142:145], v229 offset:3072
	ds_read_b128 v[146:149], v230
	ds_read_b128 v[150:153], v230 offset:1024
	ds_read_b128 v[154:157], v230 offset:2048
	ds_read_b128 v[158:161], v230 offset:3072
	s_and_b64 s[8:9], s[8:9], exec
	s_cselect_b32 s9, s30, s36
	s_cselect_b32 s8, s31, s37
	s_add_u32 s64, s9, s2
	s_addc_u32 s65, s8, 0
	s_add_i32 s82, 0, 0x18000
	s_add_i32 s83, 0, 0x1c000
	s_add_u32 s58, s64, 0x80000
	s_addc_u32 s59, s65, 0
	s_add_i32 s8, s82, s42
	s_add_i32 s2, s8, 0x2000
	s_add_u32 s54, s60, 0x80080
	s_addc_u32 s55, s61, 0
	s_add_i32 s12, s83, s42
	s_add_i32 s9, s12, 0x2000
	s_cmp_lg_u32 s73, 28
	v_lshl_add_u64 v[224:225], v[220:221], 0, s[56:57]
	ds_read_b128 v[162:165], v231
	ds_read_b128 v[166:169], v231 offset:1024
	ds_read_b128 v[170:173], v231 offset:2048
	ds_read_b128 v[174:177], v231 offset:3072
	ds_read_b128 v[178:181], v231 offset:4096
	ds_read_b128 v[182:185], v231 offset:5120
	ds_read_b128 v[186:189], v231 offset:6144
	ds_read_b128 v[190:193], v231 offset:7168
	global_load_lds_dwordx4 v[224:225], off
	v_lshl_add_u64 v[224:225], v[222:223], 0, s[56:57]
	s_mov_b32 m0, s13
	s_nop 0
	global_load_lds_dwordx4 v[224:225], off
	s_waitcnt vmcnt(8)
	s_waitcnt lgkmcnt(0)
	s_barrier
	s_setprio 1
	s_waitcnt lgkmcnt(0)
	v_mfma_f32_16x16x32_bf16 v[62:65], v[130:133], v[162:165], v[62:65]
	v_mfma_f32_16x16x32_bf16 v[58:61], v[138:141], v[162:165], v[58:61]
	v_mfma_f32_16x16x32_bf16 v[54:57], v[130:133], v[170:173], v[54:57]
	v_mfma_f32_16x16x32_bf16 v[50:53], v[138:141], v[170:173], v[50:53]
	v_mfma_f32_16x16x32_bf16 v[46:49], v[130:133], v[178:181], v[46:49]
	v_mfma_f32_16x16x32_bf16 v[42:45], v[138:141], v[178:181], v[42:45]
	v_mfma_f32_16x16x32_bf16 v[38:41], v[130:133], v[186:189], v[38:41]
	v_mfma_f32_16x16x32_bf16 v[34:37], v[138:141], v[186:189], v[34:37]
	v_mfma_f32_16x16x32_bf16 v[62:65], v[134:137], v[166:169], v[62:65]
	v_mfma_f32_16x16x32_bf16 v[58:61], v[142:145], v[166:169], v[58:61]
	v_mfma_f32_16x16x32_bf16 v[54:57], v[134:137], v[174:177], v[54:57]
	v_mfma_f32_16x16x32_bf16 v[50:53], v[142:145], v[174:177], v[50:53]
	v_mfma_f32_16x16x32_bf16 v[46:49], v[134:137], v[182:185], v[46:49]
	v_mfma_f32_16x16x32_bf16 v[42:45], v[142:145], v[182:185], v[42:45]
	v_mfma_f32_16x16x32_bf16 v[38:41], v[134:137], v[190:193], v[38:41]
	v_mfma_f32_16x16x32_bf16 v[34:37], v[142:145], v[190:193], v[34:37]
	s_setprio 0
	s_setprio 1
	v_mfma_f32_16x16x32_bf16 v[30:33], v[146:149], v[162:165], v[30:33]
	v_mfma_f32_16x16x32_bf16 v[26:29], v[154:157], v[162:165], v[26:29]
	v_mfma_f32_16x16x32_bf16 v[22:25], v[146:149], v[170:173], v[22:25]
	v_mfma_f32_16x16x32_bf16 v[18:21], v[154:157], v[170:173], v[18:21]
	v_mfma_f32_16x16x32_bf16 v[14:17], v[146:149], v[178:181], v[14:17]
	v_mfma_f32_16x16x32_bf16 v[10:13], v[154:157], v[178:181], v[10:13]
	v_mfma_f32_16x16x32_bf16 v[6:9], v[146:149], v[186:189], v[6:9]
	v_mfma_f32_16x16x32_bf16 v[2:5], v[154:157], v[186:189], v[2:5]
	v_mfma_f32_16x16x32_bf16 v[30:33], v[150:153], v[166:169], v[30:33]
	v_mfma_f32_16x16x32_bf16 v[26:29], v[158:161], v[166:169], v[26:29]
	v_mfma_f32_16x16x32_bf16 v[22:25], v[150:153], v[174:177], v[22:25]
	v_mfma_f32_16x16x32_bf16 v[18:21], v[158:161], v[174:177], v[18:21]
	v_mfma_f32_16x16x32_bf16 v[14:17], v[150:153], v[182:185], v[14:17]
	v_mfma_f32_16x16x32_bf16 v[10:13], v[158:161], v[182:185], v[10:13]
	v_mfma_f32_16x16x32_bf16 v[6:9], v[150:153], v[190:193], v[6:9]
	v_mfma_f32_16x16x32_bf16 v[2:5], v[158:161], v[190:193], v[2:5]
	s_setprio 0
	s_barrier
	s_mov_b32 m0, s22
	v_lshl_add_u64 v[224:225], s[60:61], 0, v[196:197]
	global_load_lds_dwordx4 v[224:225], off
	v_lshl_add_u64 v[232:233], s[60:61], 0, v[200:201]
	s_mov_b32 m0, s23
	v_lshl_add_u64 v[234:235], s[62:63], 0, v[196:197]
	global_load_lds_dwordx4 v[232:233], off
	s_mov_b32 m0, s24
	v_lshl_add_u64 v[236:237], s[64:65], 0, v[198:199]
	global_load_lds_dwordx4 v[234:235], off
	v_lshl_add_u64 v[234:235], s[62:63], 0, v[200:201]
	s_mov_b32 m0, s25
	s_nop 0
	global_load_lds_dwordx4 v[234:235], off
	v_lshl_add_u64 v[234:235], s[64:65], 0, v[194:195]
	s_mov_b32 m0, s51
	s_nop 0
	global_load_lds_dwordx4 v[234:235], off
	s_mov_b32 m0, s52
	s_nop 0
	global_load_lds_dwordx4 v[236:237], off
	ds_read_b128 v[162:165], v231 offset:16384
	ds_read_b128 v[166:169], v231 offset:17408
	ds_read_b128 v[170:173], v231 offset:18432
	ds_read_b128 v[174:177], v231 offset:19456
	ds_read_b128 v[178:181], v231 offset:20480
	ds_read_b128 v[182:185], v231 offset:21504
	ds_read_b128 v[186:189], v231 offset:22528
	ds_read_b128 v[190:193], v231 offset:23552
	s_waitcnt vmcnt(8)
	s_waitcnt lgkmcnt(0)
	s_barrier
	s_setprio 1
	s_waitcnt lgkmcnt(0)
	v_mfma_f32_16x16x32_bf16 v[126:129], v[130:133], v[162:165], v[126:129]
	v_mfma_f32_16x16x32_bf16 v[122:125], v[138:141], v[162:165], v[122:125]
	v_mfma_f32_16x16x32_bf16 v[114:117], v[130:133], v[170:173], v[114:117]
	v_mfma_f32_16x16x32_bf16 v[106:109], v[138:141], v[170:173], v[106:109]
	v_mfma_f32_16x16x32_bf16 v[102:105], v[130:133], v[178:181], v[102:105]
	v_mfma_f32_16x16x32_bf16 v[94:97], v[138:141], v[178:181], v[94:97]
	v_mfma_f32_16x16x32_bf16 v[86:89], v[130:133], v[186:189], v[86:89]
	v_mfma_f32_16x16x32_bf16 v[78:81], v[138:141], v[186:189], v[78:81]
	v_mfma_f32_16x16x32_bf16 v[126:129], v[134:137], v[166:169], v[126:129]
	v_mfma_f32_16x16x32_bf16 v[122:125], v[142:145], v[166:169], v[122:125]
	v_mfma_f32_16x16x32_bf16 v[114:117], v[134:137], v[174:177], v[114:117]
	v_mfma_f32_16x16x32_bf16 v[106:109], v[142:145], v[174:177], v[106:109]
	v_mfma_f32_16x16x32_bf16 v[102:105], v[134:137], v[182:185], v[102:105]
	v_mfma_f32_16x16x32_bf16 v[94:97], v[142:145], v[182:185], v[94:97]
	v_mfma_f32_16x16x32_bf16 v[86:89], v[134:137], v[190:193], v[86:89]
	v_mfma_f32_16x16x32_bf16 v[78:81], v[142:145], v[190:193], v[78:81]
	s_setprio 0
	s_setprio 1
	v_mfma_f32_16x16x32_bf16 v[118:121], v[146:149], v[162:165], v[118:121]
	v_mfma_f32_16x16x32_bf16 v[110:113], v[154:157], v[162:165], v[110:113]
	v_mfma_f32_16x16x32_bf16 v[98:101], v[146:149], v[170:173], v[98:101]
	v_mfma_f32_16x16x32_bf16 v[90:93], v[154:157], v[170:173], v[90:93]
	v_mfma_f32_16x16x32_bf16 v[82:85], v[146:149], v[178:181], v[82:85]
	v_mfma_f32_16x16x32_bf16 v[74:77], v[154:157], v[178:181], v[74:77]
	v_mfma_f32_16x16x32_bf16 v[70:73], v[146:149], v[186:189], v[70:73]
	v_mfma_f32_16x16x32_bf16 v[66:69], v[154:157], v[186:189], v[66:69]
	v_mfma_f32_16x16x32_bf16 v[118:121], v[150:153], v[166:169], v[118:121]
	v_mfma_f32_16x16x32_bf16 v[110:113], v[158:161], v[166:169], v[110:113]
	v_mfma_f32_16x16x32_bf16 v[98:101], v[150:153], v[174:177], v[98:101]
	v_mfma_f32_16x16x32_bf16 v[90:93], v[158:161], v[174:177], v[90:93]
	v_mfma_f32_16x16x32_bf16 v[82:85], v[150:153], v[182:185], v[82:85]
	v_mfma_f32_16x16x32_bf16 v[74:77], v[158:161], v[182:185], v[74:77]
	v_mfma_f32_16x16x32_bf16 v[70:73], v[150:153], v[190:193], v[70:73]
	v_mfma_f32_16x16x32_bf16 v[66:69], v[158:161], v[190:193], v[66:69]
	s_setprio 0
	s_barrier
	s_mov_b32 m0, s53
	v_lshl_add_u64 v[238:239], s[58:59], 0, v[194:195]
	global_load_lds_dwordx4 v[238:239], off
	v_lshl_add_u64 v[238:239], s[58:59], 0, v[198:199]
	s_mov_b32 m0, s74
	s_nop 0
	global_load_lds_dwordx4 v[238:239], off
	v_add_u32_e32 v130, s82, v227
	v_add_u32_e32 v142, s83, v227
	ds_read_b128 v[146:149], v130
	ds_read_b128 v[150:153], v130 offset:1024
	ds_read_b128 v[154:157], v130 offset:2048
	ds_read_b128 v[158:161], v130 offset:3072
	ds_read_b128 v[130:133], v142
	ds_read_b128 v[134:137], v142 offset:1024
	ds_read_b128 v[138:141], v142 offset:2048
	ds_read_b128 v[142:145], v142 offset:3072
	ds_read_b128 v[162:165], v231 offset:32768
	ds_read_b128 v[166:169], v231 offset:33792
	ds_read_b128 v[170:173], v231 offset:34816
	ds_read_b128 v[174:177], v231 offset:35840
	ds_read_b128 v[178:181], v231 offset:36864
	ds_read_b128 v[182:185], v231 offset:37888
	ds_read_b128 v[186:189], v231 offset:38912
	ds_read_b128 v[190:193], v231 offset:39936
	s_waitcnt vmcnt(8)
	s_waitcnt lgkmcnt(0)
	s_barrier
	s_setprio 1
	s_waitcnt lgkmcnt(0)
	v_mfma_f32_16x16x32_bf16 v[62:65], v[146:149], v[162:165], v[62:65]
	v_mfma_f32_16x16x32_bf16 v[58:61], v[154:157], v[162:165], v[58:61]
	v_mfma_f32_16x16x32_bf16 v[54:57], v[146:149], v[170:173], v[54:57]
	v_mfma_f32_16x16x32_bf16 v[50:53], v[154:157], v[170:173], v[50:53]
	v_mfma_f32_16x16x32_bf16 v[46:49], v[146:149], v[178:181], v[46:49]
	v_mfma_f32_16x16x32_bf16 v[42:45], v[154:157], v[178:181], v[42:45]
	v_mfma_f32_16x16x32_bf16 v[38:41], v[146:149], v[186:189], v[38:41]
	v_mfma_f32_16x16x32_bf16 v[34:37], v[154:157], v[186:189], v[34:37]
	v_mfma_f32_16x16x32_bf16 v[62:65], v[150:153], v[166:169], v[62:65]
	v_mfma_f32_16x16x32_bf16 v[58:61], v[158:161], v[166:169], v[58:61]
	v_mfma_f32_16x16x32_bf16 v[54:57], v[150:153], v[174:177], v[54:57]
	v_mfma_f32_16x16x32_bf16 v[50:53], v[158:161], v[174:177], v[50:53]
	v_mfma_f32_16x16x32_bf16 v[46:49], v[150:153], v[182:185], v[46:49]
	v_mfma_f32_16x16x32_bf16 v[42:45], v[158:161], v[182:185], v[42:45]
	v_mfma_f32_16x16x32_bf16 v[38:41], v[150:153], v[190:193], v[38:41]
	v_mfma_f32_16x16x32_bf16 v[34:37], v[158:161], v[190:193], v[34:37]
	s_setprio 0
	s_setprio 1
	v_mfma_f32_16x16x32_bf16 v[30:33], v[130:133], v[162:165], v[30:33]
	v_mfma_f32_16x16x32_bf16 v[26:29], v[138:141], v[162:165], v[26:29]
	v_mfma_f32_16x16x32_bf16 v[22:25], v[130:133], v[170:173], v[22:25]
	v_mfma_f32_16x16x32_bf16 v[18:21], v[138:141], v[170:173], v[18:21]
	v_mfma_f32_16x16x32_bf16 v[14:17], v[130:133], v[178:181], v[14:17]
	v_mfma_f32_16x16x32_bf16 v[10:13], v[138:141], v[178:181], v[10:13]
	v_mfma_f32_16x16x32_bf16 v[6:9], v[130:133], v[186:189], v[6:9]
	v_mfma_f32_16x16x32_bf16 v[2:5], v[138:141], v[186:189], v[2:5]
	v_mfma_f32_16x16x32_bf16 v[30:33], v[134:137], v[166:169], v[30:33]
	v_mfma_f32_16x16x32_bf16 v[26:29], v[142:145], v[166:169], v[26:29]
	v_mfma_f32_16x16x32_bf16 v[22:25], v[134:137], v[174:177], v[22:25]
	v_mfma_f32_16x16x32_bf16 v[18:21], v[142:145], v[174:177], v[18:21]
	v_mfma_f32_16x16x32_bf16 v[14:17], v[134:137], v[182:185], v[14:17]
	v_mfma_f32_16x16x32_bf16 v[10:13], v[142:145], v[182:185], v[10:13]
	v_mfma_f32_16x16x32_bf16 v[6:9], v[134:137], v[190:193], v[6:9]
	v_mfma_f32_16x16x32_bf16 v[2:5], v[142:145], v[190:193], v[2:5]
	s_setprio 0
	s_barrier
	s_mov_b32 m0, s8
	v_lshl_add_u64 v[224:225], v[224:225], 0, s[18:19]
	global_load_lds_dwordx4 v[224:225], off
	v_lshl_add_u64 v[224:225], v[232:233], 0, s[18:19]
	s_mov_b32 m0, s2
	s_nop 0
	global_load_lds_dwordx4 v[224:225], off
	v_lshl_add_u64 v[224:225], s[54:55], 0, v[196:197]
	s_mov_b32 m0, s12
	s_nop 0
	global_load_lds_dwordx4 v[224:225], off
	v_lshl_add_u64 v[224:225], s[54:55], 0, v[200:201]
	s_mov_b32 m0, s9
	s_nop 0
	global_load_lds_dwordx4 v[224:225], off
	v_lshl_add_u64 v[224:225], v[234:235], 0, s[18:19]
	s_mov_b32 m0, s78
	s_nop 0
	global_load_lds_dwordx4 v[224:225], off
	v_lshl_add_u64 v[224:225], v[236:237], 0, s[18:19]
	s_mov_b32 m0, s79
	s_nop 0
	global_load_lds_dwordx4 v[224:225], off
	ds_read_b128 v[186:189], v231 offset:49152
	ds_read_b128 v[190:193], v231 offset:50176
	ds_read_b128 v[178:181], v231 offset:51200
	ds_read_b128 v[182:185], v231 offset:52224
	ds_read_b128 v[170:173], v231 offset:53248
	ds_read_b128 v[174:177], v231 offset:54272
	ds_read_b128 v[162:165], v231 offset:55296
	ds_read_b128 v[166:169], v231 offset:56320
	s_waitcnt vmcnt(8)
	s_waitcnt lgkmcnt(0)
	s_barrier
	s_cbranch_scc1 .LBB0_1293
	v_mov_b32_e32 v202, v1
	v_mov_b32_e32 v224, v209
	s_mov_b64 s[54:55], -1
	v_add_u32_e32 v202, s69, v202
	v_lshlrev_b32_e32 v224, 3, v224
	s_and_b64 vcc, exec, s[38:39]
	v_add_u32_e32 v234, 16, v202
	v_add_u32_e32 v233, 32, v202
	v_add_u32_e32 v232, 48, v202
	s_cbranch_vccz .LBB0_1297
	v_add_u32_e32 v236, s70, v224
	v_ashrrev_i32_e32 v237, 31, v236
	v_mov_b64_e32 v[240:241], s[14:15]
	v_mad_i64_i32 v[238:239], s[8:9], v202, s88, v[240:241]
	v_lshlrev_b64 v[244:245], 1, v[236:237]
	v_lshl_add_u64 v[246:247], v[238:239], 0, v[244:245]
	v_cvt_pk_bf16_f32 v236, v62, v63
	v_cvt_pk_bf16_f32 v237, v64, v65
	v_cvt_pk_bf16_f32 v238, v58, v59
	v_cvt_pk_bf16_f32 v239, v60, v61
	global_store_dwordx4 v[246:247], v[236:239], off
	s_mov_b64 s[54:55], 0
	s_nop 0
	v_cvt_pk_bf16_f32 v236, v30, v31
	v_cvt_pk_bf16_f32 v237, v32, v33
	v_cvt_pk_bf16_f32 v238, v26, v27
	v_cvt_pk_bf16_f32 v239, v28, v29
	global_store_dwordx4 v[246:247], v[236:239], off offset:256
	s_nop 1
	v_mad_i64_i32 v[236:237], s[8:9], v234, s88, v[240:241]
	v_lshl_add_u64 v[246:247], v[236:237], 0, v[244:245]
	v_cvt_pk_bf16_f32 v236, v54, v55
	v_cvt_pk_bf16_f32 v237, v56, v57
	v_cvt_pk_bf16_f32 v238, v50, v51
	v_cvt_pk_bf16_f32 v239, v52, v53
	global_store_dwordx4 v[246:247], v[236:239], off
	s_nop 1
	v_cvt_pk_bf16_f32 v236, v22, v23
	v_cvt_pk_bf16_f32 v237, v24, v25
	v_cvt_pk_bf16_f32 v238, v18, v19
	v_cvt_pk_bf16_f32 v239, v20, v21
	global_store_dwordx4 v[246:247], v[236:239], off offset:256
	s_nop 1
	v_mad_i64_i32 v[236:237], s[8:9], v233, s88, v[240:241]
	v_lshl_add_u64 v[246:247], v[236:237], 0, v[244:245]
	v_cvt_pk_bf16_f32 v236, v46, v47
	v_cvt_pk_bf16_f32 v237, v48, v49
	v_cvt_pk_bf16_f32 v238, v42, v43
	v_cvt_pk_bf16_f32 v239, v44, v45
	global_store_dwordx4 v[246:247], v[236:239], off
	s_nop 1
	v_cvt_pk_bf16_f32 v236, v14, v15
	v_cvt_pk_bf16_f32 v237, v16, v17
	v_cvt_pk_bf16_f32 v238, v10, v11
	v_cvt_pk_bf16_f32 v239, v12, v13
	global_store_dwordx4 v[246:247], v[236:239], off offset:256
	s_nop 1
	v_mad_i64_i32 v[236:237], s[8:9], v232, s88, v[240:241]
	v_lshl_add_u64 v[240:241], v[236:237], 0, v[244:245]
	v_cvt_pk_bf16_f32 v236, v38, v39
	v_cvt_pk_bf16_f32 v237, v40, v41
	v_cvt_pk_bf16_f32 v238, v34, v35
	v_cvt_pk_bf16_f32 v239, v36, v37
	global_store_dwordx4 v[240:241], v[236:239], off
	s_nop 1
	v_cvt_pk_bf16_f32 v236, v6, v7
	v_cvt_pk_bf16_f32 v237, v8, v9
	v_cvt_pk_bf16_f32 v238, v2, v3
	v_cvt_pk_bf16_f32 v239, v4, v5
	global_store_dwordx4 v[240:241], v[236:239], off offset:256

.LBB0_1547:
	s_add_u32 s2, s66, s54
	s_addc_u32 s69, s67, s55
	s_add_u32 s56, s54, 0x100
	s_addc_u32 s57, s55, 0
	s_cmp_eq_u32 s68, 28
	s_cselect_b64 s[60:61], -1, 0
	s_and_b64 s[58:59], s[60:61], exec
	s_cselect_b32 s59, s31, s69
	s_cselect_b32 s58, s35, s2
	s_cselect_b32 s2, 0, s56
	v_lshl_add_u64 v[178:179], v[130:131], 0, s[54:55]
	s_add_i32 m0, s13, 0xc000
	s_nop 0
	global_load_lds_dwordx4 v[178:179], off
	v_lshl_add_u64 v[178:179], v[132:133], 0, s[54:55]
	s_add_i32 m0, s13, 0xe000
	s_nop 0
	global_load_lds_dwordx4 v[178:179], off
	ds_read_b128 v[134:137], v189
	ds_read_b128 v[138:141], v189 offset:1024
	ds_read_b128 v[142:145], v189 offset:2048
	ds_read_b128 v[146:149], v189 offset:3072
	ds_read_b128 v[150:153], v190
	ds_read_b128 v[170:173], v190 offset:1024
	ds_read_b128 v[174:177], v190 offset:2048
	ds_read_b128 v[194:197], v190 offset:3072
	ds_read_b128 v[198:201], v191
	ds_read_b128 v[202:205], v191 offset:1024
	ds_read_b128 v[206:209], v191 offset:2048
	ds_read_b128 v[210:213], v191 offset:3072
	ds_read_b128 v[214:217], v191 offset:4096
	ds_read_b128 v[218:221], v191 offset:5120
	ds_read_b128 v[222:225], v191 offset:6144
	ds_read_b128 v[226:229], v191 offset:7168
	s_waitcnt vmcnt(8)
	s_waitcnt lgkmcnt(0)
	s_barrier
	s_setprio 1
	s_waitcnt lgkmcnt(0)
	v_mfma_f32_16x16x32_bf16 v[126:129], v[134:137], v[198:201], v[126:129]
	v_mfma_f32_16x16x32_bf16 v[122:125], v[142:145], v[198:201], v[122:125]
	v_mfma_f32_16x16x32_bf16 v[110:113], v[134:137], v[206:209], v[110:113]
	v_mfma_f32_16x16x32_bf16 v[106:109], v[142:145], v[206:209], v[106:109]
	v_mfma_f32_16x16x32_bf16 v[94:97], v[134:137], v[214:217], v[94:97]
	v_mfma_f32_16x16x32_bf16 v[90:93], v[142:145], v[214:217], v[90:93]
	v_mfma_f32_16x16x32_bf16 v[78:81], v[134:137], v[222:225], v[78:81]
	v_mfma_f32_16x16x32_bf16 v[74:77], v[142:145], v[222:225], v[74:77]
	v_mfma_f32_16x16x32_bf16 v[126:129], v[138:141], v[202:205], v[126:129]
	v_mfma_f32_16x16x32_bf16 v[122:125], v[146:149], v[202:205], v[122:125]
	v_mfma_f32_16x16x32_bf16 v[110:113], v[138:141], v[210:213], v[110:113]
	v_mfma_f32_16x16x32_bf16 v[106:109], v[146:149], v[210:213], v[106:109]
	v_mfma_f32_16x16x32_bf16 v[94:97], v[138:141], v[218:221], v[94:97]
	v_mfma_f32_16x16x32_bf16 v[90:93], v[146:149], v[218:221], v[90:93]
	v_mfma_f32_16x16x32_bf16 v[78:81], v[138:141], v[226:229], v[78:81]
	v_mfma_f32_16x16x32_bf16 v[74:77], v[146:149], v[226:229], v[74:77]
	s_setprio 0
	s_setprio 1
	v_mfma_f32_16x16x32_bf16 v[118:121], v[150:153], v[198:201], v[118:121]
	v_mfma_f32_16x16x32_bf16 v[114:117], v[174:177], v[198:201], v[114:117]
	v_mfma_f32_16x16x32_bf16 v[102:105], v[150:153], v[206:209], v[102:105]
	v_mfma_f32_16x16x32_bf16 v[98:101], v[174:177], v[206:209], v[98:101]
	v_mfma_f32_16x16x32_bf16 v[86:89], v[150:153], v[214:217], v[86:89]
	v_mfma_f32_16x16x32_bf16 v[82:85], v[174:177], v[214:217], v[82:85]
	v_mfma_f32_16x16x32_bf16 v[70:73], v[150:153], v[222:225], v[70:73]
	v_mfma_f32_16x16x32_bf16 v[66:69], v[174:177], v[222:225], v[66:69]
	v_mfma_f32_16x16x32_bf16 v[118:121], v[170:173], v[202:205], v[118:121]
	v_mfma_f32_16x16x32_bf16 v[114:117], v[194:197], v[202:205], v[114:117]
	v_mfma_f32_16x16x32_bf16 v[102:105], v[170:173], v[210:213], v[102:105]
	v_mfma_f32_16x16x32_bf16 v[98:101], v[194:197], v[210:213], v[98:101]
	v_mfma_f32_16x16x32_bf16 v[86:89], v[170:173], v[218:221], v[86:89]
	v_mfma_f32_16x16x32_bf16 v[82:85], v[194:197], v[218:221], v[82:85]
	v_mfma_f32_16x16x32_bf16 v[70:73], v[170:173], v[226:229], v[70:73]
	v_mfma_f32_16x16x32_bf16 v[66:69], v[194:197], v[226:229], v[66:69]
	s_setprio 0
	s_barrier
	s_add_i32 s54, s63, s42
	v_lshl_add_u64 v[178:179], s[58:59], 0, v[156:157]
	s_mov_b32 m0, s54
	s_nop 0
	global_load_lds_dwordx4 v[178:179], off
	s_add_i32 m0, s54, 0x2000
	s_add_u32 s54, s58, 0x80000
	v_lshl_add_u64 v[182:183], s[58:59], 0, v[160:161]
	s_addc_u32 s55, s59, 0
	s_add_i32 s69, s64, s42
	global_load_lds_dwordx4 v[182:183], off
	v_lshl_add_u64 v[186:187], s[54:55], 0, v[156:157]
	s_mov_b32 m0, s69
	s_nop 0
	global_load_lds_dwordx4 v[186:187], off
	v_lshl_add_u64 v[186:187], s[54:55], 0, v[160:161]
	s_add_i32 m0, s69, 0x2000
	s_and_b64 s[54:55], s[8:9], s[60:61]
	s_and_b64 s[54:55], s[54:55], exec
	s_cselect_b32 s54, s36, s40
	s_cselect_b32 s55, s37, s41
	s_add_u32 s54, s54, s2
	s_addc_u32 s55, s55, 0
	global_load_lds_dwordx4 v[186:187], off
	v_lshl_add_u64 v[186:187], s[54:55], 0, v[154:155]
	s_mov_b32 m0, s13
	v_lshl_add_u64 v[230:231], s[54:55], 0, v[158:159]
	global_load_lds_dwordx4 v[186:187], off
	s_mov_b32 m0, s43
	s_nop 0
	global_load_lds_dwordx4 v[230:231], off
	ds_read_b128 v[198:201], v191 offset:16384
	ds_read_b128 v[202:205], v191 offset:17408
	ds_read_b128 v[206:209], v191 offset:18432
	ds_read_b128 v[210:213], v191 offset:19456
	ds_read_b128 v[214:217], v191 offset:20480
	ds_read_b128 v[218:221], v191 offset:21504
	ds_read_b128 v[222:225], v191 offset:22528
	ds_read_b128 v[226:229], v191 offset:23552
	s_waitcnt vmcnt(8)
	s_waitcnt lgkmcnt(0)
	s_barrier
	s_setprio 1
	s_waitcnt lgkmcnt(0)
	v_mfma_f32_16x16x32_bf16 v[62:65], v[134:137], v[198:201], v[62:65]
	v_mfma_f32_16x16x32_bf16 v[58:61], v[142:145], v[198:201], v[58:61]
	v_mfma_f32_16x16x32_bf16 v[46:49], v[134:137], v[206:209], v[46:49]
	v_mfma_f32_16x16x32_bf16 v[42:45], v[142:145], v[206:209], v[42:45]
	v_mfma_f32_16x16x32_bf16 v[30:33], v[134:137], v[214:217], v[30:33]
	v_mfma_f32_16x16x32_bf16 v[26:29], v[142:145], v[214:217], v[26:29]
	v_mfma_f32_16x16x32_bf16 v[14:17], v[134:137], v[222:225], v[14:17]
	v_mfma_f32_16x16x32_bf16 v[10:13], v[142:145], v[222:225], v[10:13]
	v_mfma_f32_16x16x32_bf16 v[62:65], v[138:141], v[202:205], v[62:65]
	v_mfma_f32_16x16x32_bf16 v[58:61], v[146:149], v[202:205], v[58:61]
	v_mfma_f32_16x16x32_bf16 v[46:49], v[138:141], v[210:213], v[46:49]
	v_mfma_f32_16x16x32_bf16 v[42:45], v[146:149], v[210:213], v[42:45]
	v_mfma_f32_16x16x32_bf16 v[30:33], v[138:141], v[218:221], v[30:33]
	v_mfma_f32_16x16x32_bf16 v[26:29], v[146:149], v[218:221], v[26:29]
	v_mfma_f32_16x16x32_bf16 v[14:17], v[138:141], v[226:229], v[14:17]
	v_mfma_f32_16x16x32_bf16 v[10:13], v[146:149], v[226:229], v[10:13]
	s_setprio 0
	s_setprio 1
	v_mfma_f32_16x16x32_bf16 v[54:57], v[150:153], v[198:201], v[54:57]
	v_mfma_f32_16x16x32_bf16 v[50:53], v[174:177], v[198:201], v[50:53]
	v_mfma_f32_16x16x32_bf16 v[38:41], v[150:153], v[206:209], v[38:41]
	v_mfma_f32_16x16x32_bf16 v[34:37], v[174:177], v[206:209], v[34:37]
	v_mfma_f32_16x16x32_bf16 v[22:25], v[150:153], v[214:217], v[22:25]
	v_mfma_f32_16x16x32_bf16 v[18:21], v[174:177], v[214:217], v[18:21]
	v_mfma_f32_16x16x32_bf16 v[6:9], v[150:153], v[222:225], v[6:9]
	v_mfma_f32_16x16x32_bf16 v[2:5], v[174:177], v[222:225], v[2:5]
	v_mfma_f32_16x16x32_bf16 v[54:57], v[170:173], v[202:205], v[54:57]
	v_mfma_f32_16x16x32_bf16 v[50:53], v[194:197], v[202:205], v[50:53]
	v_mfma_f32_16x16x32_bf16 v[38:41], v[170:173], v[210:213], v[38:41]
	v_mfma_f32_16x16x32_bf16 v[34:37], v[194:197], v[210:213], v[34:37]
	v_mfma_f32_16x16x32_bf16 v[22:25], v[170:173], v[218:221], v[22:25]
	v_mfma_f32_16x16x32_bf16 v[18:21], v[194:197], v[218:221], v[18:21]
	v_mfma_f32_16x16x32_bf16 v[6:9], v[170:173], v[226:229], v[6:9]
	v_mfma_f32_16x16x32_bf16 v[2:5], v[194:197], v[226:229], v[2:5]
	s_setprio 0
	s_barrier
	s_add_u32 s54, s54, 0x80000
	s_addc_u32 s55, s55, 0
	s_mov_b32 m0, s48
	v_lshl_add_u64 v[232:233], s[54:55], 0, v[154:155]
	global_load_lds_dwordx4 v[232:233], off
	v_lshl_add_u64 v[232:233], s[54:55], 0, v[158:159]
	s_mov_b32 m0, s49
	s_nop 0
	global_load_lds_dwordx4 v[232:233], off
	s_add_i32 s2, 0, 0x18000
	s_add_i32 s60, 0, 0x1c000
	v_add_u32_e32 v146, s2, v181
	v_add_u32_e32 v180, s60, v181
	ds_read_b128 v[134:137], v146
	ds_read_b128 v[138:141], v146 offset:1024
	ds_read_b128 v[142:145], v146 offset:2048
	ds_read_b128 v[146:149], v146 offset:3072
	ds_read_b128 v[150:153], v180
	ds_read_b128 v[170:173], v180 offset:1024
	ds_read_b128 v[174:177], v180 offset:2048
	ds_read_b128 v[194:197], v180 offset:3072
	ds_read_b128 v[198:201], v191 offset:32768
	ds_read_b128 v[202:205], v191 offset:33792
	ds_read_b128 v[206:209], v191 offset:34816
	ds_read_b128 v[210:213], v191 offset:35840
	ds_read_b128 v[214:217], v191 offset:36864
	ds_read_b128 v[218:221], v191 offset:37888
	ds_read_b128 v[222:225], v191 offset:38912
	ds_read_b128 v[226:229], v191 offset:39936
	s_waitcnt vmcnt(8)
	s_waitcnt lgkmcnt(0)
	s_barrier
	s_setprio 1
	s_waitcnt lgkmcnt(0)
	v_mfma_f32_16x16x32_bf16 v[126:129], v[134:137], v[198:201], v[126:129]
	v_mfma_f32_16x16x32_bf16 v[122:125], v[142:145], v[198:201], v[122:125]
	v_mfma_f32_16x16x32_bf16 v[110:113], v[134:137], v[206:209], v[110:113]
	v_mfma_f32_16x16x32_bf16 v[106:109], v[142:145], v[206:209], v[106:109]
	v_mfma_f32_16x16x32_bf16 v[94:97], v[134:137], v[214:217], v[94:97]
	v_mfma_f32_16x16x32_bf16 v[90:93], v[142:145], v[214:217], v[90:93]
	v_mfma_f32_16x16x32_bf16 v[78:81], v[134:137], v[222:225], v[78:81]
	v_mfma_f32_16x16x32_bf16 v[74:77], v[142:145], v[222:225], v[74:77]
	v_mfma_f32_16x16x32_bf16 v[126:129], v[138:141], v[202:205], v[126:129]
	v_mfma_f32_16x16x32_bf16 v[122:125], v[146:149], v[202:205], v[122:125]
	v_mfma_f32_16x16x32_bf16 v[110:113], v[138:141], v[210:213], v[110:113]
	v_mfma_f32_16x16x32_bf16 v[106:109], v[146:149], v[210:213], v[106:109]
	v_mfma_f32_16x16x32_bf16 v[94:97], v[138:141], v[218:221], v[94:97]
	v_mfma_f32_16x16x32_bf16 v[90:93], v[146:149], v[218:221], v[90:93]
	v_mfma_f32_16x16x32_bf16 v[78:81], v[138:141], v[226:229], v[78:81]
	v_mfma_f32_16x16x32_bf16 v[74:77], v[146:149], v[226:229], v[74:77]
	s_setprio 0
	s_setprio 1
	v_mfma_f32_16x16x32_bf16 v[118:121], v[150:153], v[198:201], v[118:121]
	v_mfma_f32_16x16x32_bf16 v[114:117], v[174:177], v[198:201], v[114:117]
	v_mfma_f32_16x16x32_bf16 v[102:105], v[150:153], v[206:209], v[102:105]
	v_mfma_f32_16x16x32_bf16 v[98:101], v[174:177], v[206:209], v[98:101]
	v_mfma_f32_16x16x32_bf16 v[86:89], v[150:153], v[214:217], v[86:89]
	v_mfma_f32_16x16x32_bf16 v[82:85], v[174:177], v[214:217], v[82:85]
	v_mfma_f32_16x16x32_bf16 v[70:73], v[150:153], v[222:225], v[70:73]
	v_mfma_f32_16x16x32_bf16 v[66:69], v[174:177], v[222:225], v[66:69]
	v_mfma_f32_16x16x32_bf16 v[118:121], v[170:173], v[202:205], v[118:121]
	v_mfma_f32_16x16x32_bf16 v[114:117], v[194:197], v[202:205], v[114:117]
	v_mfma_f32_16x16x32_bf16 v[102:105], v[170:173], v[210:213], v[102:105]
	v_mfma_f32_16x16x32_bf16 v[98:101], v[194:197], v[210:213], v[98:101]
	v_mfma_f32_16x16x32_bf16 v[86:89], v[170:173], v[218:221], v[86:89]
	v_mfma_f32_16x16x32_bf16 v[82:85], v[194:197], v[218:221], v[82:85]
	v_mfma_f32_16x16x32_bf16 v[70:73], v[170:173], v[226:229], v[70:73]
	v_mfma_f32_16x16x32_bf16 v[66:69], v[194:197], v[226:229], v[66:69]
	s_setprio 0
	s_barrier
	s_add_i32 s2, s2, s42
	v_lshl_add_u64 v[178:179], v[178:179], 0, s[26:27]
	s_mov_b32 m0, s2
	s_nop 0
	global_load_lds_dwordx4 v[178:179], off
	s_add_i32 m0, s2, 0x2000
	s_add_u32 s54, s58, 0x80080
	v_lshl_add_u64 v[178:179], v[182:183], 0, s[26:27]
	s_addc_u32 s55, s59, 0
	s_add_i32 s2, s60, s42
	global_load_lds_dwordx4 v[178:179], off
	v_lshl_add_u64 v[178:179], s[54:55], 0, v[156:157]
	s_mov_b32 m0, s2
	s_nop 0
	global_load_lds_dwordx4 v[178:179], off
	v_lshl_add_u64 v[178:179], s[54:55], 0, v[160:161]
	s_add_i32 m0, s2, 0x2000
	s_nop 0
	global_load_lds_dwordx4 v[178:179], off
	v_lshl_add_u64 v[178:179], v[186:187], 0, s[26:27]
	s_mov_b32 m0, s51
	s_nop 0
	global_load_lds_dwordx4 v[178:179], off
	v_lshl_add_u64 v[178:179], v[230:231], 0, s[26:27]
	s_mov_b32 m0, s52
	s_nop 0
	global_load_lds_dwordx4 v[178:179], off
	ds_read_b128 v[198:201], v191 offset:49152
	ds_read_b128 v[202:205], v191 offset:50176
	ds_read_b128 v[206:209], v191 offset:51200
	ds_read_b128 v[210:213], v191 offset:52224
	ds_read_b128 v[214:217], v191 offset:53248
	ds_read_b128 v[218:221], v191 offset:54272
	ds_read_b128 v[222:225], v191 offset:55296
	ds_read_b128 v[226:229], v191 offset:56320
	s_waitcnt vmcnt(8)
	s_waitcnt lgkmcnt(0)
	s_barrier
	s_setprio 1
	s_waitcnt lgkmcnt(0)
	v_mfma_f32_16x16x32_bf16 v[62:65], v[134:137], v[198:201], v[62:65]
	v_mfma_f32_16x16x32_bf16 v[58:61], v[142:145], v[198:201], v[58:61]
	v_mfma_f32_16x16x32_bf16 v[46:49], v[134:137], v[206:209], v[46:49]
	v_mfma_f32_16x16x32_bf16 v[42:45], v[142:145], v[206:209], v[42:45]
	v_mfma_f32_16x16x32_bf16 v[30:33], v[134:137], v[214:217], v[30:33]
	v_mfma_f32_16x16x32_bf16 v[26:29], v[142:145], v[214:217], v[26:29]
	v_mfma_f32_16x16x32_bf16 v[14:17], v[134:137], v[222:225], v[14:17]
	v_mfma_f32_16x16x32_bf16 v[10:13], v[142:145], v[222:225], v[10:13]
	v_mfma_f32_16x16x32_bf16 v[62:65], v[138:141], v[202:205], v[62:65]
	v_mfma_f32_16x16x32_bf16 v[58:61], v[146:149], v[202:205], v[58:61]
	v_mfma_f32_16x16x32_bf16 v[46:49], v[138:141], v[210:213], v[46:49]
	v_mfma_f32_16x16x32_bf16 v[42:45], v[146:149], v[210:213], v[42:45]
	v_mfma_f32_16x16x32_bf16 v[30:33], v[138:141], v[218:221], v[30:33]
	v_mfma_f32_16x16x32_bf16 v[26:29], v[146:149], v[218:221], v[26:29]
	v_mfma_f32_16x16x32_bf16 v[14:17], v[138:141], v[226:229], v[14:17]
	v_mfma_f32_16x16x32_bf16 v[10:13], v[146:149], v[226:229], v[10:13]
	s_setprio 0
	s_setprio 1
	v_mfma_f32_16x16x32_bf16 v[54:57], v[150:153], v[198:201], v[54:57]
	v_mfma_f32_16x16x32_bf16 v[50:53], v[174:177], v[198:201], v[50:53]
	v_mfma_f32_16x16x32_bf16 v[38:41], v[150:153], v[206:209], v[38:41]
	v_mfma_f32_16x16x32_bf16 v[34:37], v[174:177], v[206:209], v[34:37]
	v_mfma_f32_16x16x32_bf16 v[22:25], v[150:153], v[214:217], v[22:25]
	v_mfma_f32_16x16x32_bf16 v[18:21], v[174:177], v[214:217], v[18:21]
	v_mfma_f32_16x16x32_bf16 v[6:9], v[150:153], v[222:225], v[6:9]
	v_mfma_f32_16x16x32_bf16 v[2:5], v[174:177], v[222:225], v[2:5]
	v_mfma_f32_16x16x32_bf16 v[54:57], v[170:173], v[202:205], v[54:57]
	v_mfma_f32_16x16x32_bf16 v[50:53], v[194:197], v[202:205], v[50:53]
	v_mfma_f32_16x16x32_bf16 v[38:41], v[170:173], v[210:213], v[38:41]
	v_mfma_f32_16x16x32_bf16 v[34:37], v[194:197], v[210:213], v[34:37]
	v_mfma_f32_16x16x32_bf16 v[22:25], v[170:173], v[218:221], v[22:25]
	v_mfma_f32_16x16x32_bf16 v[18:21], v[194:197], v[218:221], v[18:21]
	v_mfma_f32_16x16x32_bf16 v[6:9], v[170:173], v[226:229], v[6:9]
	v_mfma_f32_16x16x32_bf16 v[2:5], v[194:197], v[226:229], v[2:5]
	s_setprio 0
	s_barrier
	s_add_i32 s68, s68, 2
	s_cmp_gt_u32 s68, 29
	s_mov_b64 s[54:55], s[56:57]
	s_cbranch_scc0 .LBB0_1547
	s_and_b64 vcc, exec, s[28:29]
	s_cbranch_vccz .LBB0_1550
	s_barrier

.LBB0_1954:
	s_lshl_b32 s2, s89, 7
	v_add_u32_e32 v142, s82, v205
	v_add_u32_e32 v158, s83, v205
	s_add_u32 s66, s40, s2
	ds_read_b128 v[130:133], v142
	ds_read_b128 v[134:137], v142 offset:1024
	ds_read_b128 v[138:141], v142 offset:2048
	ds_read_b128 v[142:145], v142 offset:3072
	ds_read_b128 v[146:149], v158
	ds_read_b128 v[150:153], v158 offset:1024
	ds_read_b128 v[154:157], v158 offset:2048
	ds_read_b128 v[158:161], v158 offset:3072
	s_addc_u32 s67, s41, 0
	s_add_u32 s68, s66, 0x100
	s_addc_u32 s69, s67, 0
	s_and_b64 s[66:67], s[62:63], exec
	s_cselect_b32 s67, s37, s69
	s_cselect_b32 s66, s85, s68
	s_add_i32 s70, s2, 0x100
	s_and_b64 s[68:69], s[62:63], exec
	s_cselect_b32 s70, 0, s70
	s_add_u32 s2, s38, s2
	s_addc_u32 s69, s39, 0
	s_add_u32 s68, s2, 0x20080
	s_addc_u32 s69, s69, 0
	v_lshl_add_u64 v[210:211], s[68:69], 0, v[194:195]
	s_add_i32 m0, s50, 0xc000
	ds_read_b128 v[162:165], v209
	ds_read_b128 v[166:169], v209 offset:1024
	ds_read_b128 v[170:173], v209 offset:2048
	ds_read_b128 v[174:177], v209 offset:3072
	ds_read_b128 v[178:181], v209 offset:4096
	ds_read_b128 v[182:185], v209 offset:5120
	ds_read_b128 v[186:189], v209 offset:6144
	ds_read_b128 v[190:193], v209 offset:7168
	global_load_lds_dwordx4 v[210:211], off
	v_lshl_add_u64 v[210:211], s[68:69], 0, v[198:199]
	s_add_i32 m0, s50, 0xe000
	s_nop 0
	global_load_lds_dwordx4 v[210:211], off
	s_waitcnt vmcnt(8)
	s_waitcnt lgkmcnt(0)
	s_barrier
	s_setprio 1
	s_waitcnt lgkmcnt(0)
	v_mfma_f32_16x16x32_bf16 v[86:89], v[130:133], v[162:165], v[86:89]
	v_mfma_f32_16x16x32_bf16 v[82:85], v[138:141], v[162:165], v[82:85]
	v_mfma_f32_16x16x32_bf16 v[78:81], v[130:133], v[170:173], v[78:81]
	v_mfma_f32_16x16x32_bf16 v[74:77], v[138:141], v[170:173], v[74:77]
	v_mfma_f32_16x16x32_bf16 v[70:73], v[130:133], v[178:181], v[70:73]
	v_mfma_f32_16x16x32_bf16 v[66:69], v[138:141], v[178:181], v[66:69]
	v_mfma_f32_16x16x32_bf16 v[62:65], v[130:133], v[186:189], v[62:65]
	v_mfma_f32_16x16x32_bf16 v[58:61], v[138:141], v[186:189], v[58:61]
	v_mfma_f32_16x16x32_bf16 v[86:89], v[134:137], v[166:169], v[86:89]
	v_mfma_f32_16x16x32_bf16 v[82:85], v[142:145], v[166:169], v[82:85]
	v_mfma_f32_16x16x32_bf16 v[78:81], v[134:137], v[174:177], v[78:81]
	v_mfma_f32_16x16x32_bf16 v[74:77], v[142:145], v[174:177], v[74:77]
	v_mfma_f32_16x16x32_bf16 v[70:73], v[134:137], v[182:185], v[70:73]
	v_mfma_f32_16x16x32_bf16 v[66:69], v[142:145], v[182:185], v[66:69]
	v_mfma_f32_16x16x32_bf16 v[62:65], v[134:137], v[190:193], v[62:65]
	v_mfma_f32_16x16x32_bf16 v[58:61], v[142:145], v[190:193], v[58:61]
	s_setprio 0
	s_setprio 1
	v_mfma_f32_16x16x32_bf16 v[54:57], v[146:149], v[162:165], v[54:57]
	v_mfma_f32_16x16x32_bf16 v[50:53], v[154:157], v[162:165], v[50:53]
	v_mfma_f32_16x16x32_bf16 v[46:49], v[146:149], v[170:173], v[46:49]
	v_mfma_f32_16x16x32_bf16 v[42:45], v[154:157], v[170:173], v[42:45]
	v_mfma_f32_16x16x32_bf16 v[34:37], v[146:149], v[178:181], v[34:37]
	v_mfma_f32_16x16x32_bf16 v[30:33], v[154:157], v[178:181], v[30:33]
	v_mfma_f32_16x16x32_bf16 v[18:21], v[146:149], v[186:189], v[18:21]
	v_mfma_f32_16x16x32_bf16 v[14:17], v[154:157], v[186:189], v[14:17]
	v_mfma_f32_16x16x32_bf16 v[54:57], v[150:153], v[166:169], v[54:57]
	v_mfma_f32_16x16x32_bf16 v[50:53], v[158:161], v[166:169], v[50:53]
	v_mfma_f32_16x16x32_bf16 v[46:49], v[150:153], v[174:177], v[46:49]
	v_mfma_f32_16x16x32_bf16 v[42:45], v[158:161], v[174:177], v[42:45]
	v_mfma_f32_16x16x32_bf16 v[34:37], v[150:153], v[182:185], v[34:37]
	v_mfma_f32_16x16x32_bf16 v[30:33], v[158:161], v[182:185], v[30:33]
	v_mfma_f32_16x16x32_bf16 v[18:21], v[150:153], v[190:193], v[18:21]
	v_mfma_f32_16x16x32_bf16 v[14:17], v[158:161], v[190:193], v[14:17]
	s_setprio 0
	s_barrier
	s_add_i32 s2, s82, s49
	v_lshl_add_u64 v[210:211], s[66:67], 0, v[196:197]
	s_mov_b32 m0, s2
	s_nop 0
	global_load_lds_dwordx4 v[210:211], off
	s_add_i32 m0, s2, 0x2000
	s_add_u32 s68, s66, 0x20000
	v_lshl_add_u64 v[212:213], s[66:67], 0, v[200:201]
	s_addc_u32 s69, s67, 0
	s_add_i32 s2, s83, s49
	global_load_lds_dwordx4 v[212:213], off
	v_lshl_add_u64 v[214:215], s[68:69], 0, v[196:197]
	s_mov_b32 m0, s2
	s_nop 0
	global_load_lds_dwordx4 v[214:215], off
	s_add_i32 m0, s2, 0x2000
	s_add_u32 s64, s64, s70
	v_lshl_add_u64 v[214:215], s[68:69], 0, v[200:201]
	s_addc_u32 s65, s65, 0
	global_load_lds_dwordx4 v[214:215], off
	v_lshl_add_u64 v[214:215], s[64:65], 0, v[194:195]
	s_mov_b32 m0, s50
	v_lshl_add_u64 v[216:217], s[64:65], 0, v[198:199]
	global_load_lds_dwordx4 v[214:215], off
	s_mov_b32 m0, s51
	s_nop 0
	global_load_lds_dwordx4 v[216:217], off
	ds_read_b128 v[162:165], v209 offset:16384
	ds_read_b128 v[166:169], v209 offset:17408
	ds_read_b128 v[170:173], v209 offset:18432
	ds_read_b128 v[174:177], v209 offset:19456
	ds_read_b128 v[178:181], v209 offset:20480
	ds_read_b128 v[182:185], v209 offset:21504
	ds_read_b128 v[186:189], v209 offset:22528
	ds_read_b128 v[190:193], v209 offset:23552
	s_waitcnt vmcnt(8)
	s_waitcnt lgkmcnt(0)
	s_barrier
	s_setprio 1
	s_waitcnt lgkmcnt(0)
	v_mfma_f32_16x16x32_bf16 v[126:129], v[130:133], v[162:165], v[126:129]
	v_mfma_f32_16x16x32_bf16 v[122:125], v[138:141], v[162:165], v[122:125]
	v_mfma_f32_16x16x32_bf16 v[110:113], v[130:133], v[170:173], v[110:113]
	v_mfma_f32_16x16x32_bf16 v[106:109], v[138:141], v[170:173], v[106:109]
	v_mfma_f32_16x16x32_bf16 v[94:97], v[130:133], v[178:181], v[94:97]
	v_mfma_f32_16x16x32_bf16 v[90:93], v[138:141], v[178:181], v[90:93]
	v_mfma_f32_16x16x32_bf16 v[22:25], v[130:133], v[186:189], v[22:25]
	v_mfma_f32_16x16x32_bf16 v[10:13], v[138:141], v[186:189], v[10:13]
	v_mfma_f32_16x16x32_bf16 v[126:129], v[134:137], v[166:169], v[126:129]
	v_mfma_f32_16x16x32_bf16 v[122:125], v[142:145], v[166:169], v[122:125]
	v_mfma_f32_16x16x32_bf16 v[110:113], v[134:137], v[174:177], v[110:113]
	v_mfma_f32_16x16x32_bf16 v[106:109], v[142:145], v[174:177], v[106:109]
	v_mfma_f32_16x16x32_bf16 v[94:97], v[134:137], v[182:185], v[94:97]
	v_mfma_f32_16x16x32_bf16 v[90:93], v[142:145], v[182:185], v[90:93]
	v_mfma_f32_16x16x32_bf16 v[22:25], v[134:137], v[190:193], v[22:25]
	v_mfma_f32_16x16x32_bf16 v[10:13], v[142:145], v[190:193], v[10:13]
	s_setprio 0
	s_setprio 1
	v_mfma_f32_16x16x32_bf16 v[118:121], v[146:149], v[162:165], v[118:121]
	v_mfma_f32_16x16x32_bf16 v[114:117], v[154:157], v[162:165], v[114:117]
	v_mfma_f32_16x16x32_bf16 v[102:105], v[146:149], v[170:173], v[102:105]
	v_mfma_f32_16x16x32_bf16 v[98:101], v[154:157], v[170:173], v[98:101]
	v_mfma_f32_16x16x32_bf16 v[38:41], v[146:149], v[178:181], v[38:41]
	v_mfma_f32_16x16x32_bf16 v[26:29], v[154:157], v[178:181], v[26:29]
	v_mfma_f32_16x16x32_bf16 v[6:9], v[146:149], v[186:189], v[6:9]
	v_mfma_f32_16x16x32_bf16 v[2:5], v[154:157], v[186:189], v[2:5]
	v_mfma_f32_16x16x32_bf16 v[118:121], v[150:153], v[166:169], v[118:121]
	v_mfma_f32_16x16x32_bf16 v[114:117], v[158:161], v[166:169], v[114:117]
	v_mfma_f32_16x16x32_bf16 v[102:105], v[150:153], v[174:177], v[102:105]
	v_mfma_f32_16x16x32_bf16 v[98:101], v[158:161], v[174:177], v[98:101]
	v_mfma_f32_16x16x32_bf16 v[38:41], v[150:153], v[182:185], v[38:41]
	v_mfma_f32_16x16x32_bf16 v[26:29], v[158:161], v[182:185], v[26:29]
	v_mfma_f32_16x16x32_bf16 v[6:9], v[150:153], v[190:193], v[6:9]
	v_mfma_f32_16x16x32_bf16 v[2:5], v[158:161], v[190:193], v[2:5]
	s_setprio 0
	s_barrier
	s_add_u32 s64, s64, 0x20000
	s_addc_u32 s65, s65, 0
	s_mov_b32 m0, s52
	v_lshl_add_u64 v[218:219], s[64:65], 0, v[194:195]
	global_load_lds_dwordx4 v[218:219], off
	v_lshl_add_u64 v[218:219], s[64:65], 0, v[198:199]
	s_mov_b32 m0, s53
	s_nop 0
	global_load_lds_dwordx4 v[218:219], off
	s_add_i32 s2, 0, 0x18000
	s_add_i32 s68, 0, 0x1c000
	v_add_u32_e32 v130, s2, v205
	v_add_u32_e32 v142, s68, v205
	ds_read_b128 v[146:149], v130
	ds_read_b128 v[150:153], v130 offset:1024
	ds_read_b128 v[154:157], v130 offset:2048
	ds_read_b128 v[158:161], v130 offset:3072
	ds_read_b128 v[130:133], v142
	ds_read_b128 v[134:137], v142 offset:1024
	ds_read_b128 v[138:141], v142 offset:2048
	ds_read_b128 v[142:145], v142 offset:3072
	ds_read_b128 v[162:165], v209 offset:32768
	ds_read_b128 v[166:169], v209 offset:33792
	ds_read_b128 v[170:173], v209 offset:34816
	ds_read_b128 v[174:177], v209 offset:35840
	ds_read_b128 v[178:181], v209 offset:36864
	ds_read_b128 v[182:185], v209 offset:37888
	ds_read_b128 v[186:189], v209 offset:38912
	ds_read_b128 v[190:193], v209 offset:39936
	s_waitcnt vmcnt(8)
	s_waitcnt lgkmcnt(0)
	s_barrier
	s_setprio 1
	s_waitcnt lgkmcnt(0)
	v_mfma_f32_16x16x32_bf16 v[86:89], v[146:149], v[162:165], v[86:89]
	v_mfma_f32_16x16x32_bf16 v[82:85], v[154:157], v[162:165], v[82:85]
	v_mfma_f32_16x16x32_bf16 v[78:81], v[146:149], v[170:173], v[78:81]
	v_mfma_f32_16x16x32_bf16 v[74:77], v[154:157], v[170:173], v[74:77]
	v_mfma_f32_16x16x32_bf16 v[70:73], v[146:149], v[178:181], v[70:73]
	v_mfma_f32_16x16x32_bf16 v[66:69], v[154:157], v[178:181], v[66:69]
	v_mfma_f32_16x16x32_bf16 v[62:65], v[146:149], v[186:189], v[62:65]
	v_mfma_f32_16x16x32_bf16 v[58:61], v[154:157], v[186:189], v[58:61]
	v_mfma_f32_16x16x32_bf16 v[86:89], v[150:153], v[166:169], v[86:89]
	v_mfma_f32_16x16x32_bf16 v[82:85], v[158:161], v[166:169], v[82:85]
	v_mfma_f32_16x16x32_bf16 v[78:81], v[150:153], v[174:177], v[78:81]
	v_mfma_f32_16x16x32_bf16 v[74:77], v[158:161], v[174:177], v[74:77]
	v_mfma_f32_16x16x32_bf16 v[70:73], v[150:153], v[182:185], v[70:73]
	v_mfma_f32_16x16x32_bf16 v[66:69], v[158:161], v[182:185], v[66:69]
	v_mfma_f32_16x16x32_bf16 v[62:65], v[150:153], v[190:193], v[62:65]
	v_mfma_f32_16x16x32_bf16 v[58:61], v[158:161], v[190:193], v[58:61]
	s_setprio 0
	s_setprio 1
	v_mfma_f32_16x16x32_bf16 v[54:57], v[130:133], v[162:165], v[54:57]
	v_mfma_f32_16x16x32_bf16 v[50:53], v[138:141], v[162:165], v[50:53]
	v_mfma_f32_16x16x32_bf16 v[46:49], v[130:133], v[170:173], v[46:49]
	v_mfma_f32_16x16x32_bf16 v[42:45], v[138:141], v[170:173], v[42:45]
	v_mfma_f32_16x16x32_bf16 v[34:37], v[130:133], v[178:181], v[34:37]
	v_mfma_f32_16x16x32_bf16 v[30:33], v[138:141], v[178:181], v[30:33]
	v_mfma_f32_16x16x32_bf16 v[18:21], v[130:133], v[186:189], v[18:21]
	v_mfma_f32_16x16x32_bf16 v[14:17], v[138:141], v[186:189], v[14:17]
	v_mfma_f32_16x16x32_bf16 v[54:57], v[134:137], v[166:169], v[54:57]
	v_mfma_f32_16x16x32_bf16 v[50:53], v[142:145], v[166:169], v[50:53]
	v_mfma_f32_16x16x32_bf16 v[46:49], v[134:137], v[174:177], v[46:49]
	v_mfma_f32_16x16x32_bf16 v[42:45], v[142:145], v[174:177], v[42:45]
	v_mfma_f32_16x16x32_bf16 v[34:37], v[134:137], v[182:185], v[34:37]
	v_mfma_f32_16x16x32_bf16 v[30:33], v[142:145], v[182:185], v[30:33]
	v_mfma_f32_16x16x32_bf16 v[18:21], v[134:137], v[190:193], v[18:21]
	v_mfma_f32_16x16x32_bf16 v[14:17], v[142:145], v[190:193], v[14:17]
	s_setprio 0
	s_barrier
	s_add_i32 s2, s2, s49
	v_lshl_add_u64 v[210:211], v[210:211], 0, s[12:13]
	s_mov_b32 m0, s2
	s_nop 0
	global_load_lds_dwordx4 v[210:211], off
	s_add_i32 m0, s2, 0x2000
	s_add_u32 s64, s66, 0x20080
	v_lshl_add_u64 v[210:211], v[212:213], 0, s[12:13]
	s_addc_u32 s65, s67, 0
	s_add_i32 s2, s68, s49
	global_load_lds_dwordx4 v[210:211], off
	v_lshl_add_u64 v[210:211], s[64:65], 0, v[196:197]
	s_mov_b32 m0, s2
	s_andn2_b64 vcc, exec, s[62:63]
	global_load_lds_dwordx4 v[210:211], off
	v_lshl_add_u64 v[210:211], s[64:65], 0, v[200:201]
	s_add_i32 m0, s2, 0x2000
	s_nop 0
	global_load_lds_dwordx4 v[210:211], off
	v_lshl_add_u64 v[210:211], v[214:215], 0, s[12:13]
	s_mov_b32 m0, s75
	s_nop 0
	global_load_lds_dwordx4 v[210:211], off
	v_lshl_add_u64 v[210:211], v[216:217], 0, s[12:13]
	s_mov_b32 m0, s76
	s_nop 0
	global_load_lds_dwordx4 v[210:211], off
	ds_read_b128 v[186:189], v209 offset:49152
	ds_read_b128 v[190:193], v209 offset:50176
	ds_read_b128 v[178:181], v209 offset:51200
	ds_read_b128 v[182:185], v209 offset:52224
	ds_read_b128 v[170:173], v209 offset:53248
	ds_read_b128 v[174:177], v209 offset:54272
	ds_read_b128 v[162:165], v209 offset:55296
	ds_read_b128 v[166:169], v209 offset:56320
	s_waitcnt vmcnt(8)
	s_waitcnt lgkmcnt(0)
	s_barrier
	s_cbranch_vccnz .LBB0_1936
	v_pk_mul_f32 v[214:215], v[86:87], s[20:21] op_sel_hi:[1,0]
	v_pk_mul_f32 v[216:217], v[82:83], s[20:21] op_sel_hi:[1,0]
	v_mov_b32_e32 v218, 0
	v_mov_b32_e32 v219, 0
	v_cvt_pk_fp8_f32 v218, v214, v215
	v_cvt_pk_fp8_f32 v219, v216, v217
	v_pk_mul_f32 v[214:215], v[88:89], s[20:21] op_sel_hi:[1,0]
	v_pk_mul_f32 v[216:217], v[84:85], s[20:21] op_sel_hi:[1,0]
	v_cvt_pk_fp8_f32 v218, v214, v215 op_sel:[0,0,1]
	v_cvt_pk_fp8_f32 v219, v216, v217 op_sel:[0,0,1]
	v_pk_mul_f32 v[214:215], v[54:55], s[20:21] op_sel_hi:[1,0]
	v_pk_mul_f32 v[216:217], v[50:51], s[20:21] op_sel_hi:[1,0]
	v_mov_b32_e32 v220, 0
	v_mov_b32_e32 v221, 0
	v_mov_b32_e32 v210, v1
	v_mov_b32_e32 v211, v204
	v_cvt_pk_fp8_f32 v220, v214, v215
	v_cvt_pk_fp8_f32 v221, v216, v217
	v_pk_mul_f32 v[214:215], v[56:57], s[20:21] op_sel_hi:[1,0]
	v_add_u32_e32 v210, s87, v210
	v_lshl_add_u32 v212, v211, 3, s88
	v_ashrrev_i32_e32 v211, 31, v210
	v_pk_mul_f32 v[216:217], v[52:53], s[20:21] op_sel_hi:[1,0]
	v_lshlrev_b64 v[210:211], 11, v[210:211]
	v_cvt_pk_fp8_f32 v220, v214, v215 op_sel:[0,0,1]
	v_cvt_pk_fp8_f32 v221, v216, v217 op_sel:[0,0,1]
	v_ashrrev_i32_e32 v213, 31, v212
	v_lshl_add_u64 v[210:211], s[10:11], 0, v[210:211]
	v_lshl_add_u64 v[210:211], v[210:211], 0, v[212:213]
	global_store_dwordx2 v[210:211], v[218:219], off
	global_store_dwordx2 v[210:211], v[220:221], off offset:128
	v_pk_mul_f32 v[214:215], v[78:79], s[20:21] op_sel_hi:[1,0]
	v_pk_mul_f32 v[216:217], v[74:75], s[20:21] op_sel_hi:[1,0]
	v_mov_b32_e32 v218, 0
	v_mov_b32_e32 v219, 0
	v_cvt_pk_fp8_f32 v218, v214, v215
	v_cvt_pk_fp8_f32 v219, v216, v217
	v_pk_mul_f32 v[214:215], v[80:81], s[20:21] op_sel_hi:[1,0]
	v_pk_mul_f32 v[216:217], v[76:77], s[20:21] op_sel_hi:[1,0]
	v_cvt_pk_fp8_f32 v218, v214, v215 op_sel:[0,0,1]
	v_cvt_pk_fp8_f32 v219, v216, v217 op_sel:[0,0,1]
	v_pk_mul_f32 v[214:215], v[46:47], s[20:21] op_sel_hi:[1,0]
	v_pk_mul_f32 v[216:217], v[42:43], s[20:21] op_sel_hi:[1,0]
	v_mov_b32_e32 v220, 0
	v_mov_b32_e32 v221, 0
	v_cvt_pk_fp8_f32 v220, v214, v215
	v_cvt_pk_fp8_f32 v221, v216, v217
	v_pk_mul_f32 v[214:215], v[48:49], s[20:21] op_sel_hi:[1,0]
	v_pk_mul_f32 v[216:217], v[44:45], s[20:21] op_sel_hi:[1,0]
	v_cvt_pk_fp8_f32 v220, v214, v215 op_sel:[0,0,1]
	v_cvt_pk_fp8_f32 v221, v216, v217 op_sel:[0,0,1]
	s_mov_b32 s2, 0x8000
	v_add_co_u32_e32 v214, vcc, s2, v210
	v_lshl_add_u64 v[212:213], v[210:211], 0, s[24:25]
	s_nop 0
	v_addc_co_u32_e32 v215, vcc, 0, v211, vcc
	global_store_dwordx2 v[214:215], v[218:219], off
	global_store_dwordx2 v[212:213], v[220:221], off offset:128
	v_pk_mul_f32 v[214:215], v[70:71], s[20:21] op_sel_hi:[1,0]
	v_pk_mul_f32 v[216:217], v[66:67], s[20:21] op_sel_hi:[1,0]
	v_mov_b32_e32 v218, 0
	v_mov_b32_e32 v219, 0
	v_cvt_pk_fp8_f32 v218, v214, v215
	v_cvt_pk_fp8_f32 v219, v216, v217
	v_pk_mul_f32 v[214:215], v[72:73], s[20:21] op_sel_hi:[1,0]
	v_pk_mul_f32 v[216:217], v[68:69], s[20:21] op_sel_hi:[1,0]
	v_cvt_pk_fp8_f32 v218, v214, v215 op_sel:[0,0,1]
	v_cvt_pk_fp8_f32 v219, v216, v217 op_sel:[0,0,1]
	v_pk_mul_f32 v[214:215], v[34:35], s[20:21] op_sel_hi:[1,0]
	v_pk_mul_f32 v[216:217], v[30:31], s[20:21] op_sel_hi:[1,0]
	v_mov_b32_e32 v220, 0
	v_mov_b32_e32 v221, 0
	v_cvt_pk_fp8_f32 v220, v214, v215
	v_cvt_pk_fp8_f32 v221, v216, v217
	v_pk_mul_f32 v[214:215], v[36:37], s[20:21] op_sel_hi:[1,0]
	v_pk_mul_f32 v[216:217], v[32:33], s[20:21] op_sel_hi:[1,0]
	v_cvt_pk_fp8_f32 v220, v214, v215 op_sel:[0,0,1]
	v_cvt_pk_fp8_f32 v221, v216, v217 op_sel:[0,0,1]
	s_mov_b32 s2, 0x10000
	v_add_co_u32_e32 v214, vcc, s2, v210
	v_lshl_add_u64 v[212:213], v[210:211], 0, s[28:29]
	s_nop 0
	v_addc_co_u32_e32 v215, vcc, 0, v211, vcc
	global_store_dwordx2 v[214:215], v[218:219], off
	global_store_dwordx2 v[212:213], v[220:221], off offset:128
	v_pk_mul_f32 v[214:215], v[62:63], s[20:21] op_sel_hi:[1,0]
	v_pk_mul_f32 v[216:217], v[58:59], s[20:21] op_sel_hi:[1,0]
	v_mov_b32_e32 v218, 0
	v_mov_b32_e32 v219, 0
	v_cvt_pk_fp8_f32 v218, v214, v215
	v_cvt_pk_fp8_f32 v219, v216, v217
	v_pk_mul_f32 v[214:215], v[64:65], s[20:21] op_sel_hi:[1,0]
	v_pk_mul_f32 v[216:217], v[60:61], s[20:21] op_sel_hi:[1,0]
	v_cvt_pk_fp8_f32 v218, v214, v215 op_sel:[0,0,1]
	v_cvt_pk_fp8_f32 v219, v216, v217 op_sel:[0,0,1]
	v_pk_mul_f32 v[214:215], v[18:19], s[20:21] op_sel_hi:[1,0]
	v_pk_mul_f32 v[216:217], v[14:15], s[20:21] op_sel_hi:[1,0]
	v_mov_b32_e32 v220, 0
	v_mov_b32_e32 v221, 0
	v_cvt_pk_fp8_f32 v220, v214, v215
	v_cvt_pk_fp8_f32 v221, v216, v217
	v_pk_mul_f32 v[214:215], v[20:21], s[20:21] op_sel_hi:[1,0]
	v_pk_mul_f32 v[216:217], v[16:17], s[20:21] op_sel_hi:[1,0]
	v_cvt_pk_fp8_f32 v220, v214, v215 op_sel:[0,0,1]
	v_cvt_pk_fp8_f32 v221, v216, v217 op_sel:[0,0,1]
	s_mov_b32 s2, 0x18000
	v_lshl_add_u64 v[212:213], v[210:211], 0, s[30:31]
	v_add_co_u32_e32 v210, vcc, s2, v210
	s_nop 1
	v_addc_co_u32_e32 v211, vcc, 0, v211, vcc
	global_store_dwordx2 v[210:211], v[218:219], off
	global_store_dwordx2 v[212:213], v[220:221], off offset:128
	s_branch .LBB0_1936
